# mla_post transposing gather: 32 LDS u16 reads issued in two batches with one wait each instead of 16 serial round trips
# speedup vs baseline: 1.0075x; 1.0075x over previous
.LBB0_977:
	s_mul_hi_i32 s12, s19, 0x38e38e39
	s_lshr_b32 s13, s12, 31
	s_ashr_i32 s22, s12, 4
	s_add_i32 s22, s22, s13
	s_mul_i32 s13, s22, 0xfffff700
	s_add_i32 s23, s33, s18
	s_add_i32 s12, s18, s13
	s_add_i32 s35, s23, s13
	s_lshl_b32 s13, s22, 8
	s_add_i32 s30, s13, 0x1800
	s_lshl_b32 s31, s22, 11
	s_cmpk_lt_i32 s35, 0x800
	s_cselect_b64 vcc, -1, 0
	s_and_b64 s[20:21], vcc, exec
	s_cselect_b32 s13, s31, s30
	s_mul_i32 s36, s22, 0x900
	s_sub_i32 s13, s13, s36
	s_add_i32 s20, s23, s13
	s_ashr_i32 s21, s20, 31
	v_mad_i64_i32 v[2:3], s[24:25], s20, v45, v[20:21]
	s_lshl_b64 s[24:25], s[20:21], 11
	s_add_i32 s34, s35, 8
	s_cmpk_lt_i32 s35, 0x7f8
	s_cselect_b32 s13, s31, s30
	s_sub_i32 s13, s13, s36
	global_load_ushort v10, v[2:3], off
	v_mad_i64_i32 v[2:3], s[20:21], s20, v46, v[26:27]
	s_add_i32 s13, s23, s13
	v_lshl_add_u64 v[4:5], v[28:29], 0, s[24:25]
	s_add_i32 s20, s13, 8
	global_load_ushort v11, v[2:3], off
	global_load_ushort v12, v[2:3], off offset:128
	global_load_ushort v13, v[2:3], off offset:256
	global_load_ushort v16, v[4:5], off
	global_load_ushort v17, v[4:5], off offset:128
	global_load_ushort v124, v[4:5], off offset:256
	global_load_ushort v125, v[4:5], off offset:384
	global_load_ushort v34, v[2:3], off offset:384
	global_load_ushort v35, v[2:3], off offset:512
	global_load_ushort v36, v[2:3], off offset:640
	global_load_ushort v37, v[4:5], off offset:512
	global_load_ushort v48, v[4:5], off offset:640
	global_load_ushort v120, v[4:5], off offset:768
	global_load_ushort v121, v[4:5], off offset:896
	global_load_ushort v49, v[2:3], off offset:768
	global_load_ushort v52, v[2:3], off offset:896
	global_load_ushort v53, v[2:3], off offset:1024
	global_load_ushort v54, v[4:5], off offset:1024
	global_load_ushort v55, v[4:5], off offset:1152
	global_load_ushort v113, v[4:5], off offset:1280
	global_load_ushort v114, v[4:5], off offset:1408
	global_load_ushort v56, v[2:3], off offset:1152
	global_load_ushort v59, v[2:3], off offset:1280
	global_load_ushort v60, v[2:3], off offset:1408
	global_load_ushort v61, v[4:5], off offset:1536
	global_load_ushort v62, v[4:5], off offset:1664
	global_load_ushort v106, v[4:5], off offset:1792
	global_load_ushort v107, v[4:5], off offset:1920
	s_ashr_i32 s21, s20, 31
	v_mad_i64_i32 v[2:3], s[24:25], s20, v45, v[20:21]
	global_load_ushort v63, v[2:3], off
	s_lshl_b64 s[24:25], s[20:21], 11
	v_mad_i64_i32 v[2:3], s[20:21], s20, v46, v[26:27]
	s_add_i32 s21, s35, 16
	s_cmpk_lt_i32 s35, 0x7f0
	s_cselect_b32 s13, s31, s30
	s_sub_i32 s13, s13, s36
	s_add_i32 s13, s23, s13
	v_lshl_add_u64 v[4:5], v[28:29], 0, s[24:25]
	s_add_i32 s24, s13, 16
	global_load_ushort v66, v[2:3], off
	global_load_ushort v67, v[2:3], off offset:128
	global_load_ushort v68, v[2:3], off offset:256
	global_load_ushort v69, v[4:5], off
	global_load_ushort v72, v[4:5], off offset:128
	global_load_ushort v98, v[4:5], off offset:256
	global_load_ushort v99, v[4:5], off offset:384
	global_load_ushort v73, v[2:3], off offset:384
	global_load_ushort v74, v[2:3], off offset:512
	global_load_ushort v75, v[2:3], off offset:640
	global_load_ushort v76, v[4:5], off offset:512
	global_load_ushort v79, v[4:5], off offset:640
	global_load_ushort v91, v[4:5], off offset:768
	global_load_ushort v92, v[4:5], off offset:896
	global_load_ushort v80, v[2:3], off offset:768
	global_load_ushort v81, v[2:3], off offset:896
	global_load_ushort v82, v[2:3], off offset:1024
	global_load_ushort v83, v[4:5], off offset:1024
	global_load_ushort v86, v[4:5], off offset:1152
	global_load_ushort v84, v[4:5], off offset:1280
	global_load_ushort v85, v[4:5], off offset:1408
	global_load_ushort v87, v[2:3], off offset:1152
	global_load_ushort v88, v[2:3], off offset:1280
	global_load_ushort v89, v[2:3], off offset:1408
	global_load_ushort v90, v[4:5], off offset:1536
	global_load_ushort v93, v[4:5], off offset:1664
	global_load_ushort v77, v[4:5], off offset:1792
	global_load_ushort v78, v[4:5], off offset:1920
	s_ashr_i32 s25, s24, 31
	v_mad_i64_i32 v[2:3], s[28:29], s24, v45, v[20:21]
	s_lshl_b64 s[28:29], s[24:25], 11
	s_add_i32 s13, s35, 24
	s_cmpk_lt_i32 s35, 0x7e8
	s_cselect_b32 s20, s31, s30
	s_sub_i32 s20, s20, s36
	global_load_ushort v94, v[2:3], off
	v_mad_i64_i32 v[2:3], s[24:25], s24, v46, v[26:27]
	s_add_i32 s20, s23, s20
	v_lshl_add_u64 v[4:5], v[28:29], 0, s[28:29]
	s_add_i32 s24, s20, 24
	global_load_ushort v95, v[2:3], off
	global_load_ushort v96, v[2:3], off offset:128
	global_load_ushort v122, v[2:3], off offset:256
	global_load_ushort v123, v[4:5], off
	global_load_ushort v126, v[4:5], off offset:128
	global_load_ushort v70, v[4:5], off offset:256
	global_load_ushort v71, v[4:5], off offset:384
	global_load_ushort v127, v[2:3], off offset:384
	global_load_ushort v128, v[2:3], off offset:512
	global_load_ushort v129, v[2:3], off offset:640
	global_load_ushort v130, v[4:5], off offset:512
	global_load_ushort v131, v[4:5], off offset:640
	global_load_ushort v64, v[4:5], off offset:768
	global_load_ushort v65, v[4:5], off offset:896
	global_load_ushort v132, v[2:3], off offset:768
	global_load_ushort v133, v[2:3], off offset:896
	global_load_ushort v134, v[2:3], off offset:1024
	global_load_ushort v135, v[4:5], off offset:1024
	global_load_ushort v136, v[4:5], off offset:1152
	global_load_ushort v57, v[4:5], off offset:1280
	global_load_ushort v58, v[4:5], off offset:1408
	global_load_ushort v137, v[2:3], off offset:1152
	global_load_ushort v138, v[2:3], off offset:1280
	global_load_ushort v139, v[2:3], off offset:1408
	global_load_ushort v140, v[4:5], off offset:1536
	global_load_ushort v141, v[4:5], off offset:1664
	global_load_ushort v50, v[4:5], off offset:1792
	global_load_ushort v51, v[4:5], off offset:1920
	s_ashr_i32 s25, s24, 31
	v_mad_i64_i32 v[2:3], s[28:29], s24, v45, v[20:21]
	s_lshl_b64 s[28:29], s[24:25], 11
	global_load_ushort v142, v[2:3], off
	v_mad_i64_i32 v[2:3], s[24:25], s24, v46, v[26:27]
	v_lshl_add_u64 v[8:9], v[28:29], 0, s[28:29]
	global_load_ushort v143, v[2:3], off
	global_load_ushort v144, v[2:3], off offset:128
	global_load_ushort v145, v[2:3], off offset:256
	global_load_ushort v146, v[8:9], off
	global_load_ushort v147, v[8:9], off offset:128
	global_load_ushort v14, v[8:9], off offset:256
	global_load_ushort v15, v[8:9], off offset:384
	global_load_ushort v148, v[2:3], off offset:384
	global_load_ushort v149, v[2:3], off offset:512
	global_load_ushort v150, v[2:3], off offset:640
	global_load_ushort v151, v[8:9], off offset:512
	global_load_ushort v152, v[8:9], off offset:640
	global_load_ushort v6, v[8:9], off offset:768
	global_load_ushort v7, v[8:9], off offset:896
	global_load_ushort v153, v[2:3], off offset:768
	global_load_ushort v154, v[2:3], off offset:896
	global_load_ushort v155, v[2:3], off offset:1024
	global_load_ushort v156, v[8:9], off offset:1024
	global_load_ushort v157, v[8:9], off offset:1152
	global_load_ushort v4, v[8:9], off offset:1280
	global_load_ushort v5, v[8:9], off offset:1408
	global_load_ushort v158, v[2:3], off offset:1152
	global_load_ushort v159, v[2:3], off offset:1280
	global_load_ushort v160, v[2:3], off offset:1408
	global_load_ushort v161, v[8:9], off offset:1536
	global_load_ushort v162, v[8:9], off offset:1664
	s_nop 0
	global_load_ushort v2, v[8:9], off offset:1792
	global_load_ushort v3, v[8:9], off offset:1920
	s_waitcnt vmcnt(28)
	s_ashr_i32 s23, s35, 6
	s_and_b32 s24, s35, 63
	s_lshl_b32 s20, s22, 2
	s_ashr_i32 s36, s35, 31
	s_mulk_i32 s22, 0x2400
	s_nop 0
	s_nop 0
	s_waitcnt vmcnt(27)
	s_waitcnt vmcnt(26)
	s_waitcnt vmcnt(25)
	s_waitcnt vmcnt(24)
	s_waitcnt vmcnt(23)
	s_waitcnt vmcnt(22)
	s_waitcnt vmcnt(21)
	s_waitcnt vmcnt(20)
	s_waitcnt vmcnt(19)
	s_waitcnt vmcnt(18)
	s_waitcnt vmcnt(17)
	s_waitcnt vmcnt(16)
	s_waitcnt vmcnt(15)
	s_waitcnt vmcnt(14)
	s_waitcnt vmcnt(13)
	s_waitcnt vmcnt(12)
	s_waitcnt vmcnt(11)
	s_waitcnt vmcnt(10)
	s_waitcnt vmcnt(9)
	s_waitcnt vmcnt(8)
	s_waitcnt vmcnt(7)
	s_waitcnt vmcnt(6)
	s_waitcnt vmcnt(5)
	s_waitcnt vmcnt(4)
	s_waitcnt vmcnt(3)
	s_waitcnt vmcnt(2)
	s_waitcnt vmcnt(1)
	s_waitcnt vmcnt(0)
	v_lshlrev_b32_e32 v167, 16, v11
	v_lshlrev_b32_e32 v168, 16, v12
	v_lshlrev_b32_e32 v169, 16, v13
	v_lshlrev_b32_e32 v173, 16, v35
	v_lshlrev_b32_e32 v174, 16, v36
	v_lshlrev_b32_e32 v175, 16, v37
	global_load_dword v37, v[22:23], off
	global_load_dword v36, v[22:23], off offset:256
	global_load_dword v35, v[22:23], off offset:512
	global_load_dword v13, v[24:25], off
	global_load_dword v12, v[24:25], off offset:256
	global_load_dword v11, v[24:25], off offset:512
	v_lshlrev_b32_e32 v190, 16, v69
	v_lshlrev_b32_e32 v69, 16, v94
	v_lshlrev_b32_e32 v97, 16, v95
	v_lshlrev_b32_e32 v95, 16, v122
	v_lshlrev_b32_e32 v94, 16, v123
	v_mov_b32_e32 v122, s24
	v_mov_b32_e32 v123, s23
	v_cndmask_b32_e64 v122, v122, v123, s[0:1]
	v_cvt_f32_i32_e32 v122, v122
	v_lshlrev_b32_e32 v102, 16, v90
	v_lshlrev_b32_e32 v101, 16, v93
	v_lshlrev_b32_e32 v93, 16, v126
	v_mul_f32_e32 v122, v1, v122
	v_mul_f32_e32 v122, 0.15915494, v122
	v_lshlrev_b32_e32 v90, 16, v127
	v_cos_f32_e32 v126, v122
	v_sin_f32_e32 v127, v122
	v_mul_f32_e32 v122, v168, v168
	v_fmac_f32_e32 v122, v167, v167
	v_fmac_f32_e32 v122, v169, v169
	v_lshlrev_b32_e32 v103, 16, v89
	v_lshlrev_b32_e32 v89, 16, v128
	v_add_f32_dpp v122, v122, v122 quad_perm:[1,0,3,2] row_mask:0xf bank_mask:0xf bound_ctrl:1
	v_lshlrev_b32_e32 v105, 16, v87
	v_lshlrev_b32_e32 v104, 16, v88
	v_add_f32_dpp v122, v122, v122 quad_perm:[2,3,0,1] row_mask:0xf bank_mask:0xf bound_ctrl:1
	v_lshlrev_b32_e32 v88, 16, v129
	v_lshlrev_b32_e32 v87, 16, v130
	v_add_f32_dpp v122, v122, v122 row_half_mirror row_mask:0xf bank_mask:0xf bound_ctrl:1
	v_lshlrev_b32_e32 v171, 16, v17
	v_lshlrev_b32_e32 v170, 16, v16
	v_add_f32_dpp v122, v122, v122 row_mirror row_mask:0xf bank_mask:0xf bound_ctrl:1
	v_lshlrev_b32_e32 v163, 16, v10
	v_readlane_b32 s24, v122, 16
	v_readlane_b32 s28, v122, 48
	v_readlane_b32 s23, v122, 0
	v_readlane_b32 s25, v122, 32
	v_mov_b32_e32 v122, s24
	v_mov_b32_e32 v123, s28
	v_add_f32_e32 v122, s23, v122
	v_add_f32_e32 v123, s25, v123
	v_add_f32_e32 v122, v122, v123
	v_fmamk_f32 v122, v122, 0x3baaaaab, v44
	v_rsq_f32_e32 v122, v122
	s_mul_hi_i32 s23, s20, 0x900
	s_add_u32 s28, s22, s35
	s_addc_u32 s29, s23, s36
	v_mul_f32_e32 v123, v122, v167
	v_mul_f32_e32 v128, v122, v168
	v_mul_f32_e32 v122, v122, v169
	s_mulk_i32 s29, 0x180
	v_lshlrev_b32_e32 v172, 16, v34
	v_lshlrev_b32_e32 v176, 16, v48
	v_lshlrev_b32_e32 v178, 16, v52
	v_lshlrev_b32_e32 v177, 16, v49
	v_lshlrev_b32_e32 v179, 16, v53
	v_lshlrev_b32_e32 v181, 16, v55
	v_lshlrev_b32_e32 v180, 16, v54
	v_lshlrev_b32_e32 v183, 16, v59
	v_lshlrev_b32_e32 v182, 16, v56
	v_lshlrev_b32_e32 v184, 16, v60
	v_lshlrev_b32_e32 v186, 16, v62
	v_lshlrev_b32_e32 v185, 16, v61
	v_lshlrev_b32_e32 v188, 16, v67
	v_lshlrev_b32_e32 v187, 16, v66
	v_lshlrev_b32_e32 v189, 16, v68
	v_lshlrev_b32_e32 v191, 16, v72
	v_lshlrev_b32_e32 v100, 16, v63
	v_lshlrev_b32_e32 v118, 16, v74
	v_lshlrev_b32_e32 v119, 16, v73
	v_lshlrev_b32_e32 v117, 16, v75
	v_lshlrev_b32_e32 v115, 16, v79
	v_lshlrev_b32_e32 v116, 16, v76
	v_lshlrev_b32_e32 v111, 16, v81
	s_waitcnt vmcnt(5)
	v_mul_f32_e32 v123, v37, v123
	s_waitcnt vmcnt(4)
	v_mul_f32_e32 v128, v36, v128
	s_waitcnt vmcnt(3)
	v_mul_f32_e32 v122, v35, v122
	v_mov_b32_e32 v129, v122
	v_mov_b32_e32 v130, v122
	s_nop 1
	v_permlane32_swap_b32_e32 v129, v130
	v_cndmask_b32_e64 v129, v129, v130, s[4:5]
	v_mul_f32_e32 v129, v127, v129
	v_cndmask_b32_e64 v129, v129, -v129, s[4:5]
	v_fmac_f32_e32 v129, v126, v122
	v_cndmask_b32_e32 v129, v122, v129, vcc
	v_cvt_pk_bf16_f32 v130, v123, v19
	v_mad_u64_u32 v[122:123], s[24:25], s28, v47, v[30:31]
	v_add_u32_e32 v123, s29, v123
	v_cvt_pk_bf16_f32 v128, v128, v19
	global_store_short v[122:123], v130, off
	global_store_short v[122:123], v128, off offset:128
	v_cvt_pk_bf16_f32 v128, v129, v19
	global_store_short v[122:123], v128, off offset:256
	v_mul_f32_e32 v122, v171, v171
	v_fmac_f32_e32 v122, v170, v170
	v_fmac_f32_e32 v122, v163, v163
	v_lshlrev_b32_e32 v112, 16, v80
	v_lshlrev_b32_e32 v110, 16, v82
	v_add_f32_dpp v122, v122, v122 quad_perm:[1,0,3,2] row_mask:0xf bank_mask:0xf bound_ctrl:1
	v_lshlrev_b32_e32 v108, 16, v86
	v_lshlrev_b32_e32 v109, 16, v83
	v_add_f32_dpp v122, v122, v122 quad_perm:[2,3,0,1] row_mask:0xf bank_mask:0xf bound_ctrl:1
	v_lshlrev_b32_e32 v96, 16, v96
	v_lshlrev_b32_e32 v86, 16, v131
	v_add_f32_dpp v122, v122, v122 row_half_mirror row_mask:0xf bank_mask:0xf bound_ctrl:1
	v_lshlrev_b32_e32 v82, 16, v133
	v_lshlrev_b32_e32 v83, 16, v132
	v_add_f32_dpp v122, v122, v122 row_mirror row_mask:0xf bank_mask:0xf bound_ctrl:1
	v_lshlrev_b32_e32 v81, 16, v134
	v_readlane_b32 s25, v122, 16
	v_readlane_b32 s31, v122, 48
	v_readlane_b32 s24, v122, 0
	v_readlane_b32 s30, v122, 32
	v_mov_b32_e32 v122, s25
	v_mov_b32_e32 v123, s31
	v_add_f32_e32 v122, s24, v122
	v_add_f32_e32 v123, s30, v123
	v_add_f32_e32 v122, v122, v123
	v_fmamk_f32 v122, v122, 0x3baaaaab, v44
	v_rsq_f32_e32 v122, v122
	v_lshlrev_b32_e32 v79, 16, v136
	v_lshlrev_b32_e32 v80, 16, v135
	v_lshlrev_b32_e32 v75, 16, v138
	v_mul_f32_e32 v123, v122, v170
	v_mul_f32_e32 v128, v122, v171
	v_mul_f32_e32 v122, v122, v163
	s_waitcnt vmcnt(3)
	v_mul_f32_e32 v122, v11, v122
	v_mov_b32_e32 v129, v122
	v_mov_b32_e32 v130, v122
	s_nop 1
	v_permlane32_swap_b32_e32 v129, v130
	v_cndmask_b32_e64 v129, v129, v130, s[4:5]
	v_mul_f32_e32 v129, v127, v129
	v_cndmask_b32_e64 v129, v129, -v129, s[4:5]
	v_mul_f32_e32 v123, v13, v123
	v_fmac_f32_e32 v129, v126, v122
	v_mul_f32_e32 v128, v12, v128
	v_cndmask_b32_e32 v129, v122, v129, vcc
	v_cvt_pk_bf16_f32 v130, v123, v19
	v_mad_u64_u32 v[122:123], s[24:25], s28, v47, v[32:33]
	v_add_u32_e32 v123, s29, v123
	v_cvt_pk_bf16_f32 v128, v128, v19
	global_store_short v[122:123], v130, off
	global_store_short v[122:123], v128, off offset:128
	v_cvt_pk_bf16_f32 v128, v129, v19
	global_store_short v[122:123], v128, off offset:256
	v_mul_f32_e32 v122, v173, v173
	v_fmac_f32_e32 v122, v172, v172
	v_fmac_f32_e32 v122, v174, v174
	ds_write_b16 v38, v124
	ds_write_b16 v38, v125 offset:128
	v_add_f32_dpp v122, v122, v122 quad_perm:[1,0,3,2] row_mask:0xf bank_mask:0xf bound_ctrl:1
	v_lshlrev_b32_e32 v76, 16, v137
	v_lshlrev_b32_e32 v74, 16, v139
	v_add_f32_dpp v122, v122, v122 quad_perm:[2,3,0,1] row_mask:0xf bank_mask:0xf bound_ctrl:1
	v_lshlrev_b32_e32 v72, 16, v141
	v_lshlrev_b32_e32 v73, 16, v140
	v_add_f32_dpp v122, v122, v122 row_half_mirror row_mask:0xf bank_mask:0xf bound_ctrl:1
	v_lshlrev_b32_e32 v67, 16, v144
	v_lshlrev_b32_e32 v68, 16, v143
	v_add_f32_dpp v122, v122, v122 row_mirror row_mask:0xf bank_mask:0xf bound_ctrl:1
	v_lshlrev_b32_e32 v66, 16, v145
	v_readlane_b32 s25, v122, 16
	v_readlane_b32 s29, v122, 48
	v_readlane_b32 s24, v122, 0
	v_readlane_b32 s28, v122, 32
	v_mov_b32_e32 v122, s25
	v_mov_b32_e32 v123, s29
	v_add_f32_e32 v122, s24, v122
	v_add_f32_e32 v123, s28, v123
	v_add_f32_e32 v122, v122, v123
	v_fmamk_f32 v122, v122, 0x3baaaaab, v44
	v_rsq_f32_e32 v122, v122
	s_or_b32 s25, s20, 1
	s_mul_hi_i32 s24, s25, 0x900
	s_mulk_i32 s25, 0x900
	v_mul_f32_e32 v123, v122, v172
	v_mul_f32_e32 v124, v122, v173
	v_mul_f32_e32 v122, v122, v174
	v_mul_f32_e32 v122, v35, v122
	v_mov_b32_e32 v125, v122
	v_mov_b32_e32 v128, v122
	s_nop 1
	v_permlane32_swap_b32_e32 v125, v128
	v_cndmask_b32_e64 v125, v125, v128, s[4:5]
	v_mul_f32_e32 v125, v127, v125
	v_cndmask_b32_e64 v125, v125, -v125, s[4:5]
	s_add_u32 s30, s25, s35
	v_mul_f32_e32 v123, v37, v123
	v_fmac_f32_e32 v125, v126, v122
	s_addc_u32 s31, s24, s36
	v_mul_f32_e32 v124, v36, v124
	v_cndmask_b32_e32 v125, v122, v125, vcc
	v_cvt_pk_bf16_f32 v128, v123, v19
	v_mad_u64_u32 v[122:123], s[28:29], s30, v47, v[30:31]
	s_mulk_i32 s31, 0x180
	v_add_u32_e32 v123, s31, v123
	v_cvt_pk_bf16_f32 v124, v124, v19
	global_store_short v[122:123], v128, off
	global_store_short v[122:123], v124, off offset:128
	v_cvt_pk_bf16_f32 v124, v125, v19
	global_store_short v[122:123], v124, off offset:256
	v_mul_f32_e32 v122, v176, v176
	v_fmac_f32_e32 v122, v175, v175
	v_fmac_f32_e32 v122, v163, v163
	v_lshlrev_b32_e32 v62, 16, v147
	v_lshlrev_b32_e32 v63, 16, v146
	v_add_f32_dpp v122, v122, v122 quad_perm:[1,0,3,2] row_mask:0xf bank_mask:0xf bound_ctrl:1
	v_lshlrev_b32_e32 v8, 16, v142
	v_lshlrev_b32_e32 v60, 16, v149
	v_add_f32_dpp v122, v122, v122 quad_perm:[2,3,0,1] row_mask:0xf bank_mask:0xf bound_ctrl:1
	v_lshlrev_b32_e32 v61, 16, v148
	v_lshlrev_b32_e32 v59, 16, v150
	v_add_f32_dpp v122, v122, v122 row_half_mirror row_mask:0xf bank_mask:0xf bound_ctrl:1
	v_lshlrev_b32_e32 v55, 16, v152
	v_lshlrev_b32_e32 v56, 16, v151
	v_add_f32_dpp v122, v122, v122 row_mirror row_mask:0xf bank_mask:0xf bound_ctrl:1
	v_lshlrev_b32_e32 v53, 16, v154
	v_readlane_b32 s29, v122, 16
	v_readlane_b32 s38, v122, 48
	v_readlane_b32 s28, v122, 0
	v_readlane_b32 s37, v122, 32
	v_mov_b32_e32 v122, s29
	v_mov_b32_e32 v123, s38
	v_add_f32_e32 v122, s28, v122
	v_add_f32_e32 v123, s37, v123
	v_add_f32_e32 v122, v122, v123
	v_fmamk_f32 v122, v122, 0x3baaaaab, v44
	v_rsq_f32_e32 v122, v122
	v_lshlrev_b32_e32 v54, 16, v153
	v_lshlrev_b32_e32 v52, 16, v155
	v_lshlrev_b32_e32 v48, 16, v157
	v_mul_f32_e32 v123, v122, v175
	v_mul_f32_e32 v124, v122, v176
	v_mul_f32_e32 v122, v122, v163
	v_mul_f32_e32 v122, v11, v122
	v_mov_b32_e32 v125, v122
	v_mov_b32_e32 v128, v122
	s_nop 1
	v_permlane32_swap_b32_e32 v125, v128
	v_cndmask_b32_e64 v125, v125, v128, s[4:5]
	v_mul_f32_e32 v125, v127, v125
	v_cndmask_b32_e64 v125, v125, -v125, s[4:5]
	v_mul_f32_e32 v123, v13, v123
	v_fmac_f32_e32 v125, v126, v122
	v_mul_f32_e32 v124, v12, v124
	v_cndmask_b32_e32 v125, v122, v125, vcc
	v_cvt_pk_bf16_f32 v128, v123, v19
	v_mad_u64_u32 v[122:123], s[28:29], s30, v47, v[32:33]
	v_add_u32_e32 v123, s31, v123
	v_cvt_pk_bf16_f32 v124, v124, v19
	global_store_short v[122:123], v128, off
	global_store_short v[122:123], v124, off offset:128
	v_cvt_pk_bf16_f32 v124, v125, v19
	global_store_short v[122:123], v124, off offset:256
	ds_write_b16 v38, v120 offset:256
	ds_write_b16 v38, v121 offset:384
	v_mul_f32_e32 v120, v178, v178
	v_fmac_f32_e32 v120, v177, v177
	v_fmac_f32_e32 v120, v179, v179
	v_lshlrev_b32_e32 v49, 16, v156
	v_lshlrev_b32_e32 v17, 16, v159
	v_add_f32_dpp v120, v120, v120 quad_perm:[1,0,3,2] row_mask:0xf bank_mask:0xf bound_ctrl:1
	v_lshlrev_b32_e32 v34, 16, v158
	v_lshlrev_b32_e32 v16, 16, v160
	v_add_f32_dpp v120, v120, v120 quad_perm:[2,3,0,1] row_mask:0xf bank_mask:0xf bound_ctrl:1
	v_lshlrev_b32_e32 v9, 16, v162
	v_lshlrev_b32_e32 v10, 16, v161
	v_add_f32_dpp v120, v120, v120 row_half_mirror row_mask:0xf bank_mask:0xf bound_ctrl:1
	s_nop 1
	v_add_f32_dpp v120, v120, v120 row_mirror row_mask:0xf bank_mask:0xf bound_ctrl:1
	s_nop 0
	v_readlane_b32 s29, v120, 16
	v_readlane_b32 s31, v120, 48
	v_readlane_b32 s28, v120, 0
	v_readlane_b32 s30, v120, 32
	v_mov_b32_e32 v120, s29
	v_mov_b32_e32 v121, s31
	v_add_f32_e32 v120, s28, v120
	v_add_f32_e32 v121, s30, v121
	v_add_f32_e32 v120, v120, v121
	v_fmamk_f32 v120, v120, 0x3baaaaab, v44
	v_rsq_f32_e32 v120, v120
	s_or_b32 s29, s20, 2
	s_mul_hi_i32 s28, s29, 0x900
	s_mulk_i32 s29, 0x900
	v_mul_f32_e32 v121, v120, v177
	v_mul_f32_e32 v122, v120, v178
	v_mul_f32_e32 v120, v120, v179
	v_mul_f32_e32 v120, v35, v120
	v_mov_b32_e32 v123, v120
	v_mov_b32_e32 v124, v120
	s_nop 1
	v_permlane32_swap_b32_e32 v123, v124
	v_cndmask_b32_e64 v123, v123, v124, s[4:5]
	v_mul_f32_e32 v123, v127, v123
	v_cndmask_b32_e64 v123, v123, -v123, s[4:5]
	s_add_u32 s37, s29, s35
	v_mul_f32_e32 v121, v37, v121
	v_fmac_f32_e32 v123, v126, v120
	s_addc_u32 s38, s28, s36
	v_mul_f32_e32 v122, v36, v122
	v_cndmask_b32_e32 v123, v120, v123, vcc
	v_cvt_pk_bf16_f32 v124, v121, v19
	v_mad_u64_u32 v[120:121], s[30:31], s37, v47, v[30:31]
	s_mulk_i32 s38, 0x180
	v_add_u32_e32 v121, s38, v121
	v_cvt_pk_bf16_f32 v122, v122, v19
	global_store_short v[120:121], v124, off
	global_store_short v[120:121], v122, off offset:128
	v_cvt_pk_bf16_f32 v122, v123, v19
	global_store_short v[120:121], v122, off offset:256
	v_mul_f32_e32 v120, v181, v181
	v_fmac_f32_e32 v120, v180, v180
	v_fmac_f32_e32 v120, v163, v163
	s_nop 1
	v_add_f32_dpp v120, v120, v120 quad_perm:[1,0,3,2] row_mask:0xf bank_mask:0xf bound_ctrl:1
	s_nop 1
	v_add_f32_dpp v120, v120, v120 quad_perm:[2,3,0,1] row_mask:0xf bank_mask:0xf bound_ctrl:1
	s_nop 1
	v_add_f32_dpp v120, v120, v120 row_half_mirror row_mask:0xf bank_mask:0xf bound_ctrl:1
	s_nop 1
	v_add_f32_dpp v120, v120, v120 row_mirror row_mask:0xf bank_mask:0xf bound_ctrl:1
	s_nop 0
	v_readlane_b32 s31, v120, 16
	v_readlane_b32 s40, v120, 48
	v_readlane_b32 s30, v120, 0
	v_readlane_b32 s39, v120, 32
	v_mov_b32_e32 v120, s31
	v_mov_b32_e32 v121, s40
	v_add_f32_e32 v120, s30, v120
	v_add_f32_e32 v121, s39, v121
	v_add_f32_e32 v120, v120, v121
	v_fmamk_f32 v120, v120, 0x3baaaaab, v44
	v_rsq_f32_e32 v120, v120
	s_nop 0
	v_mul_f32_e32 v121, v120, v180
	v_mul_f32_e32 v122, v120, v181
	v_mul_f32_e32 v120, v120, v163
	v_mul_f32_e32 v120, v11, v120
	v_mov_b32_e32 v123, v120
	v_mov_b32_e32 v124, v120
	s_nop 1
	v_permlane32_swap_b32_e32 v123, v124
	v_cndmask_b32_e64 v123, v123, v124, s[4:5]
	v_mul_f32_e32 v123, v127, v123
	v_cndmask_b32_e64 v123, v123, -v123, s[4:5]
	v_mul_f32_e32 v121, v13, v121
	v_fmac_f32_e32 v123, v126, v120
	v_mul_f32_e32 v122, v12, v122
	v_cndmask_b32_e32 v123, v120, v123, vcc
	v_cvt_pk_bf16_f32 v124, v121, v19
	v_mad_u64_u32 v[120:121], s[30:31], s37, v47, v[32:33]
	v_add_u32_e32 v121, s38, v121
	v_cvt_pk_bf16_f32 v122, v122, v19
	global_store_short v[120:121], v124, off
	global_store_short v[120:121], v122, off offset:128
	v_cvt_pk_bf16_f32 v122, v123, v19
	global_store_short v[120:121], v122, off offset:256
	ds_write_b16 v38, v113 offset:512
	ds_write_b16 v38, v114 offset:640
	v_mul_f32_e32 v113, v183, v183
	v_fmac_f32_e32 v113, v182, v182
	v_fmac_f32_e32 v113, v184, v184
	s_nop 1
	v_add_f32_dpp v113, v113, v113 quad_perm:[1,0,3,2] row_mask:0xf bank_mask:0xf bound_ctrl:1
	s_nop 1
	v_add_f32_dpp v113, v113, v113 quad_perm:[2,3,0,1] row_mask:0xf bank_mask:0xf bound_ctrl:1
	s_nop 1
	v_add_f32_dpp v113, v113, v113 row_half_mirror row_mask:0xf bank_mask:0xf bound_ctrl:1
	s_nop 1
	v_add_f32_dpp v113, v113, v113 row_mirror row_mask:0xf bank_mask:0xf bound_ctrl:1
	s_nop 0
	v_readlane_b32 s31, v113, 16
	v_readlane_b32 s38, v113, 48
	v_readlane_b32 s30, v113, 0
	v_readlane_b32 s37, v113, 32
	v_mov_b32_e32 v113, s31
	v_mov_b32_e32 v114, s38
	v_add_f32_e32 v113, s30, v113
	v_add_f32_e32 v114, s37, v114
	v_add_f32_e32 v113, v113, v114
	v_fmamk_f32 v113, v113, 0x3baaaaab, v44
	v_rsq_f32_e32 v113, v113
	s_or_b32 s31, s20, 3
	s_mul_hi_i32 s30, s31, 0x900
	s_mulk_i32 s31, 0x900
	v_mul_f32_e32 v114, v113, v182
	v_mul_f32_e32 v120, v113, v183
	v_mul_f32_e32 v113, v113, v184
	v_mul_f32_e32 v113, v35, v113
	v_mul_f32_e32 v122, v36, v120
	v_mov_b32_e32 v120, v113
	v_mov_b32_e32 v121, v113
	s_nop 1
	v_permlane32_swap_b32_e32 v120, v121
	v_cndmask_b32_e64 v120, v120, v121, s[4:5]
	v_mul_f32_e32 v120, v127, v120
	v_cndmask_b32_e64 v120, v120, -v120, s[4:5]
	s_add_u32 s35, s31, s35
	v_fmac_f32_e32 v120, v126, v113
	s_addc_u32 s38, s30, s36
	v_cndmask_b32_e32 v113, v113, v120, vcc
	v_mad_u64_u32 v[120:121], s[36:37], s35, v47, v[30:31]
	s_mulk_i32 s38, 0x180
	v_add_u32_e32 v121, s38, v121
	v_cvt_pk_bf16_f32 v113, v113, v19
	global_store_short v[120:121], v113, off offset:256
	v_mul_f32_e32 v113, v186, v186
	v_fmac_f32_e32 v113, v185, v185
	v_fmac_f32_e32 v113, v163, v163
	v_mul_f32_e32 v114, v37, v114
	v_cvt_pk_bf16_f32 v114, v114, v19
	global_store_short v[120:121], v114, off
	v_add_f32_dpp v113, v113, v113 quad_perm:[1,0,3,2] row_mask:0xf bank_mask:0xf bound_ctrl:1
	v_cvt_pk_bf16_f32 v114, v122, v19
	global_store_short v[120:121], v114, off offset:128
	s_cmpk_lt_i32 s34, 0x800
	v_add_f32_dpp v113, v113, v113 quad_perm:[2,3,0,1] row_mask:0xf bank_mask:0xf bound_ctrl:1
	s_nop 1
	v_add_f32_dpp v113, v113, v113 row_half_mirror row_mask:0xf bank_mask:0xf bound_ctrl:1
	s_nop 1
	v_add_f32_dpp v113, v113, v113 row_mirror row_mask:0xf bank_mask:0xf bound_ctrl:1
	s_nop 0
	v_readlane_b32 s37, v113, 16
	v_readlane_b32 s40, v113, 48
	v_readlane_b32 s36, v113, 0
	v_readlane_b32 s39, v113, 32
	v_mov_b32_e32 v113, s37
	v_mov_b32_e32 v114, s40
	v_add_f32_e32 v113, s36, v113
	v_add_f32_e32 v114, s39, v114
	v_add_f32_e32 v113, v113, v114
	v_fmamk_f32 v113, v113, 0x3baaaaab, v44
	v_rsq_f32_e32 v113, v113
	s_nop 0
	v_mul_f32_e32 v114, v113, v185
	v_mul_f32_e32 v120, v113, v186
	v_mul_f32_e32 v113, v113, v163
	v_mul_f32_e32 v113, v11, v113
	v_mul_f32_e32 v122, v12, v120
	v_mov_b32_e32 v120, v113
	v_mov_b32_e32 v121, v113
	s_nop 1
	v_permlane32_swap_b32_e32 v120, v121
	v_cndmask_b32_e64 v120, v120, v121, s[4:5]
	v_mul_f32_e32 v120, v127, v120
	v_cndmask_b32_e64 v120, v120, -v120, s[4:5]
	v_fmac_f32_e32 v120, v126, v113
	v_mul_f32_e32 v114, v13, v114
	v_cndmask_b32_e32 v113, v113, v120, vcc
	v_mad_u64_u32 v[120:121], s[36:37], s35, v47, v[32:33]
	v_cvt_pk_bf16_f32 v114, v114, v19
	v_add_u32_e32 v121, s38, v121
	s_cselect_b64 vcc, -1, 0
	s_ashr_i32 s35, s34, 6
	s_and_b32 s36, s34, 63
	global_store_short v[120:121], v114, off
	v_cvt_pk_bf16_f32 v114, v122, v19
	global_store_short v[120:121], v114, off offset:128
	v_cvt_pk_bf16_f32 v113, v113, v19
	global_store_short v[120:121], v113, off offset:256
	ds_write_b16 v38, v106 offset:768
	ds_write_b16 v38, v107 offset:896
	v_mov_b32_e32 v106, s36
	v_mov_b32_e32 v107, s35
	v_cndmask_b32_e64 v106, v106, v107, s[0:1]
	v_cvt_f32_i32_e32 v106, v106
	s_ashr_i32 s35, s34, 31
	v_mul_f32_e32 v106, v1, v106
	v_mul_f32_e32 v106, 0.15915494, v106
	v_cos_f32_e32 v113, v106
	v_sin_f32_e32 v114, v106
	v_mul_f32_e32 v106, v188, v188
	v_fmac_f32_e32 v106, v187, v187
	v_fmac_f32_e32 v106, v189, v189
	s_nop 1
	v_add_f32_dpp v106, v106, v106 quad_perm:[1,0,3,2] row_mask:0xf bank_mask:0xf bound_ctrl:1
	s_nop 1
	v_add_f32_dpp v106, v106, v106 quad_perm:[2,3,0,1] row_mask:0xf bank_mask:0xf bound_ctrl:1
	s_nop 1
	v_add_f32_dpp v106, v106, v106 row_half_mirror row_mask:0xf bank_mask:0xf bound_ctrl:1
	s_nop 1
	v_add_f32_dpp v106, v106, v106 row_mirror row_mask:0xf bank_mask:0xf bound_ctrl:1
	s_nop 0
	v_readlane_b32 s37, v106, 16
	v_readlane_b32 s39, v106, 48
	v_readlane_b32 s36, v106, 0
	v_readlane_b32 s38, v106, 32
	v_mov_b32_e32 v106, s37
	v_mov_b32_e32 v107, s39
	v_add_f32_e32 v106, s36, v106
	v_add_f32_e32 v107, s38, v107
	v_add_f32_e32 v106, v106, v107
	v_fmamk_f32 v106, v106, 0x3baaaaab, v44
	v_rsq_f32_e32 v106, v106
	s_add_u32 s38, s22, s34
	s_addc_u32 s39, s23, s35
	s_mulk_i32 s39, 0x180
	v_mul_f32_e32 v107, v106, v187
	v_mul_f32_e32 v120, v106, v188
	v_mul_f32_e32 v106, v106, v189
	v_mul_f32_e32 v106, v35, v106
	v_mov_b32_e32 v121, v106
	v_mov_b32_e32 v122, v106
	s_nop 1
	v_permlane32_swap_b32_e32 v121, v122
	v_cndmask_b32_e64 v121, v121, v122, s[4:5]
	v_mul_f32_e32 v121, v114, v121
	v_cndmask_b32_e64 v121, v121, -v121, s[4:5]
	v_mul_f32_e32 v107, v37, v107
	v_fmac_f32_e32 v121, v113, v106
	v_mul_f32_e32 v120, v36, v120
	v_cndmask_b32_e32 v121, v106, v121, vcc
	v_cvt_pk_bf16_f32 v122, v107, v19
	v_mad_u64_u32 v[106:107], s[36:37], s38, v47, v[30:31]
	v_add_u32_e32 v107, s39, v107
	v_cvt_pk_bf16_f32 v120, v120, v19
	global_store_short v[106:107], v122, off
	global_store_short v[106:107], v120, off offset:128
	v_cvt_pk_bf16_f32 v120, v121, v19
	global_store_short v[106:107], v120, off offset:256
	v_mul_f32_e32 v106, v191, v191
	v_fmac_f32_e32 v106, v190, v190
	v_fmac_f32_e32 v106, v100, v100
	s_nop 1
	v_add_f32_dpp v106, v106, v106 quad_perm:[1,0,3,2] row_mask:0xf bank_mask:0xf bound_ctrl:1
	s_nop 1
	v_add_f32_dpp v106, v106, v106 quad_perm:[2,3,0,1] row_mask:0xf bank_mask:0xf bound_ctrl:1
	s_nop 1
	v_add_f32_dpp v106, v106, v106 row_half_mirror row_mask:0xf bank_mask:0xf bound_ctrl:1
	s_nop 1
	v_add_f32_dpp v106, v106, v106 row_mirror row_mask:0xf bank_mask:0xf bound_ctrl:1
	s_nop 0
	v_readlane_b32 s37, v106, 16
	v_readlane_b32 s41, v106, 48
	v_readlane_b32 s36, v106, 0
	v_readlane_b32 s40, v106, 32
	v_mov_b32_e32 v106, s37
	v_mov_b32_e32 v107, s41
	v_add_f32_e32 v106, s36, v106
	v_add_f32_e32 v107, s40, v107
	v_add_f32_e32 v106, v106, v107
	v_fmamk_f32 v106, v106, 0x3baaaaab, v44
	v_rsq_f32_e32 v106, v106
	s_nop 0
	v_mul_f32_e32 v107, v106, v190
	v_mul_f32_e32 v120, v106, v191
	v_mul_f32_e32 v106, v106, v100
	v_mul_f32_e32 v106, v11, v106
	v_mov_b32_e32 v121, v106
	v_mov_b32_e32 v122, v106
	s_nop 1
	v_permlane32_swap_b32_e32 v121, v122
	v_cndmask_b32_e64 v121, v121, v122, s[4:5]
	v_mul_f32_e32 v121, v114, v121
	v_cndmask_b32_e64 v121, v121, -v121, s[4:5]
	v_mul_f32_e32 v107, v13, v107
	v_fmac_f32_e32 v121, v113, v106
	v_mul_f32_e32 v120, v12, v120
	v_cndmask_b32_e32 v121, v106, v121, vcc
	v_cvt_pk_bf16_f32 v122, v107, v19
	v_mad_u64_u32 v[106:107], s[36:37], s38, v47, v[32:33]
	v_add_u32_e32 v107, s39, v107
	v_cvt_pk_bf16_f32 v120, v120, v19
	global_store_short v[106:107], v122, off
	global_store_short v[106:107], v120, off offset:128
	v_cvt_pk_bf16_f32 v120, v121, v19
	global_store_short v[106:107], v120, off offset:256
	ds_write_b16 v39, v98
	ds_write_b16 v39, v99 offset:128
	v_mul_f32_e32 v98, v118, v118
	v_fmac_f32_e32 v98, v119, v119
	v_fmac_f32_e32 v98, v117, v117
	s_nop 1
	v_add_f32_dpp v98, v98, v98 quad_perm:[1,0,3,2] row_mask:0xf bank_mask:0xf bound_ctrl:1
	s_nop 1
	v_add_f32_dpp v98, v98, v98 quad_perm:[2,3,0,1] row_mask:0xf bank_mask:0xf bound_ctrl:1
	s_nop 1
	v_add_f32_dpp v98, v98, v98 row_half_mirror row_mask:0xf bank_mask:0xf bound_ctrl:1
	s_nop 1
	v_add_f32_dpp v98, v98, v98 row_mirror row_mask:0xf bank_mask:0xf bound_ctrl:1
	s_nop 0
	v_readlane_b32 s37, v98, 16
	v_readlane_b32 s39, v98, 48
	v_readlane_b32 s36, v98, 0
	v_readlane_b32 s38, v98, 32
	v_mov_b32_e32 v98, s37
	v_mov_b32_e32 v99, s39
	v_add_f32_e32 v98, s36, v98
	v_add_f32_e32 v99, s38, v99
	v_add_f32_e32 v98, v98, v99
	v_fmamk_f32 v98, v98, 0x3baaaaab, v44
	v_rsq_f32_e32 v98, v98
	s_add_u32 s38, s25, s34
	s_addc_u32 s39, s24, s35
	s_mulk_i32 s39, 0x180
	v_mul_f32_e32 v99, v98, v119
	v_mul_f32_e32 v106, v98, v118
	v_mul_f32_e32 v98, v98, v117
	v_mul_f32_e32 v98, v35, v98
	v_mov_b32_e32 v107, v98
	v_mov_b32_e32 v117, v98
	s_nop 1
	v_permlane32_swap_b32_e32 v107, v117
	v_cndmask_b32_e64 v107, v107, v117, s[4:5]
	v_mul_f32_e32 v107, v114, v107
	v_cndmask_b32_e64 v107, v107, -v107, s[4:5]
	v_mul_f32_e32 v99, v37, v99
	v_fmac_f32_e32 v107, v113, v98
	v_mul_f32_e32 v106, v36, v106
	v_cndmask_b32_e32 v107, v98, v107, vcc
	v_cvt_pk_bf16_f32 v117, v99, v19
	v_mad_u64_u32 v[98:99], s[36:37], s38, v47, v[30:31]
	v_add_u32_e32 v99, s39, v99
	v_cvt_pk_bf16_f32 v106, v106, v19
	global_store_short v[98:99], v117, off
	global_store_short v[98:99], v106, off offset:128
	v_cvt_pk_bf16_f32 v106, v107, v19
	global_store_short v[98:99], v106, off offset:256
	v_mul_f32_e32 v98, v115, v115
	v_fmac_f32_e32 v98, v116, v116
	v_fmac_f32_e32 v98, v100, v100
	s_nop 1
	v_add_f32_dpp v98, v98, v98 quad_perm:[1,0,3,2] row_mask:0xf bank_mask:0xf bound_ctrl:1
	s_nop 1
	v_add_f32_dpp v98, v98, v98 quad_perm:[2,3,0,1] row_mask:0xf bank_mask:0xf bound_ctrl:1
	s_nop 1
	v_add_f32_dpp v98, v98, v98 row_half_mirror row_mask:0xf bank_mask:0xf bound_ctrl:1
	s_nop 1
	v_add_f32_dpp v98, v98, v98 row_mirror row_mask:0xf bank_mask:0xf bound_ctrl:1
	s_nop 0
	v_readlane_b32 s37, v98, 16
	v_readlane_b32 s41, v98, 48
	v_readlane_b32 s36, v98, 0
	v_readlane_b32 s40, v98, 32
	v_mov_b32_e32 v98, s37
	v_mov_b32_e32 v99, s41
	v_add_f32_e32 v98, s36, v98
	v_add_f32_e32 v99, s40, v99
	v_add_f32_e32 v98, v98, v99
	v_fmamk_f32 v98, v98, 0x3baaaaab, v44
	v_rsq_f32_e32 v98, v98
	s_nop 0
	v_mul_f32_e32 v99, v98, v116
	v_mul_f32_e32 v106, v98, v115
	v_mul_f32_e32 v98, v98, v100
	v_mul_f32_e32 v98, v11, v98
	v_mov_b32_e32 v107, v98
	v_mov_b32_e32 v115, v98
	s_nop 1
	v_permlane32_swap_b32_e32 v107, v115
	v_cndmask_b32_e64 v107, v107, v115, s[4:5]
	v_mul_f32_e32 v107, v114, v107
	v_cndmask_b32_e64 v107, v107, -v107, s[4:5]
	v_mul_f32_e32 v99, v13, v99
	v_fmac_f32_e32 v107, v113, v98
	v_mul_f32_e32 v106, v12, v106
	v_cndmask_b32_e32 v107, v98, v107, vcc
	v_cvt_pk_bf16_f32 v115, v99, v19
	v_mad_u64_u32 v[98:99], s[36:37], s38, v47, v[32:33]
	v_add_u32_e32 v99, s39, v99
	v_cvt_pk_bf16_f32 v106, v106, v19
	global_store_short v[98:99], v115, off
	global_store_short v[98:99], v106, off offset:128
	v_cvt_pk_bf16_f32 v106, v107, v19
	global_store_short v[98:99], v106, off offset:256
	ds_write_b16 v39, v91 offset:256
	ds_write_b16 v39, v92 offset:384
	v_mul_f32_e32 v91, v111, v111
	v_fmac_f32_e32 v91, v112, v112
	v_fmac_f32_e32 v91, v110, v110
	s_nop 1
	v_add_f32_dpp v91, v91, v91 quad_perm:[1,0,3,2] row_mask:0xf bank_mask:0xf bound_ctrl:1
	s_nop 1
	v_add_f32_dpp v91, v91, v91 quad_perm:[2,3,0,1] row_mask:0xf bank_mask:0xf bound_ctrl:1
	s_nop 1
	v_add_f32_dpp v91, v91, v91 row_half_mirror row_mask:0xf bank_mask:0xf bound_ctrl:1
	s_nop 1
	v_add_f32_dpp v91, v91, v91 row_mirror row_mask:0xf bank_mask:0xf bound_ctrl:1
	s_nop 0
	v_readlane_b32 s37, v91, 16
	v_readlane_b32 s39, v91, 48
	v_readlane_b32 s36, v91, 0
	v_readlane_b32 s38, v91, 32
	v_mov_b32_e32 v91, s37
	v_mov_b32_e32 v92, s39
	v_add_f32_e32 v91, s36, v91
	v_add_f32_e32 v92, s38, v92
	v_add_f32_e32 v91, v91, v92
	v_fmamk_f32 v91, v91, 0x3baaaaab, v44
	v_rsq_f32_e32 v91, v91
	s_add_u32 s38, s29, s34
	s_addc_u32 s39, s28, s35
	s_mulk_i32 s39, 0x180
	v_mul_f32_e32 v92, v91, v112
	v_mul_f32_e32 v98, v91, v111
	v_mul_f32_e32 v91, v91, v110
	v_mul_f32_e32 v91, v35, v91
	v_mul_f32_e32 v106, v36, v98
	v_mov_b32_e32 v98, v91
	v_mov_b32_e32 v99, v91
	s_nop 1
	v_permlane32_swap_b32_e32 v98, v99
	v_cndmask_b32_e64 v98, v98, v99, s[4:5]
	v_mul_f32_e32 v98, v114, v98
	v_cndmask_b32_e64 v98, v98, -v98, s[4:5]
	v_fmac_f32_e32 v98, v113, v91
	v_cndmask_b32_e32 v91, v91, v98, vcc
	v_mad_u64_u32 v[98:99], s[36:37], s38, v47, v[30:31]
	v_add_u32_e32 v99, s39, v99
	v_cvt_pk_bf16_f32 v91, v91, v19
	global_store_short v[98:99], v91, off offset:256
	v_mul_f32_e32 v91, v108, v108
	v_fmac_f32_e32 v91, v109, v109
	v_fmac_f32_e32 v91, v100, v100
	v_mul_f32_e32 v92, v37, v92
	v_cvt_pk_bf16_f32 v92, v92, v19
	global_store_short v[98:99], v92, off
	v_add_f32_dpp v91, v91, v91 quad_perm:[1,0,3,2] row_mask:0xf bank_mask:0xf bound_ctrl:1
	v_cvt_pk_bf16_f32 v92, v106, v19
	global_store_short v[98:99], v92, off offset:128
	s_nop 0
	v_add_f32_dpp v91, v91, v91 quad_perm:[2,3,0,1] row_mask:0xf bank_mask:0xf bound_ctrl:1
	s_nop 1
	v_add_f32_dpp v91, v91, v91 row_half_mirror row_mask:0xf bank_mask:0xf bound_ctrl:1
	s_nop 1
	v_add_f32_dpp v91, v91, v91 row_mirror row_mask:0xf bank_mask:0xf bound_ctrl:1
	s_nop 0
	v_readlane_b32 s37, v91, 16
	v_readlane_b32 s41, v91, 48
	v_readlane_b32 s36, v91, 0
	v_readlane_b32 s40, v91, 32
	v_mov_b32_e32 v91, s37
	v_mov_b32_e32 v92, s41
	v_add_f32_e32 v91, s36, v91
	v_add_f32_e32 v92, s40, v92
	v_add_f32_e32 v91, v91, v92
	v_fmamk_f32 v91, v91, 0x3baaaaab, v44
	v_rsq_f32_e32 v91, v91
	s_nop 0
	v_mul_f32_e32 v92, v91, v109
	v_mul_f32_e32 v98, v91, v108
	v_mul_f32_e32 v91, v91, v100
	v_mul_f32_e32 v91, v11, v91
	v_mul_f32_e32 v106, v12, v98
	v_mov_b32_e32 v98, v91
	v_mov_b32_e32 v99, v91
	s_nop 1
	v_permlane32_swap_b32_e32 v98, v99
	v_cndmask_b32_e64 v98, v98, v99, s[4:5]
	v_mul_f32_e32 v98, v114, v98
	v_cndmask_b32_e64 v98, v98, -v98, s[4:5]
	v_fmac_f32_e32 v98, v113, v91
	v_mul_f32_e32 v92, v13, v92
	v_cndmask_b32_e32 v91, v91, v98, vcc
	v_mad_u64_u32 v[98:99], s[36:37], s38, v47, v[32:33]
	v_cvt_pk_bf16_f32 v92, v92, v19
	v_add_u32_e32 v99, s39, v99
	global_store_short v[98:99], v92, off
	v_cvt_pk_bf16_f32 v92, v106, v19
	global_store_short v[98:99], v92, off offset:128
	v_cvt_pk_bf16_f32 v91, v91, v19
	global_store_short v[98:99], v91, off offset:256
	ds_write_b16 v39, v84 offset:512
	ds_write_b16 v39, v85 offset:640
	v_mul_f32_e32 v84, v104, v104
	v_fmac_f32_e32 v84, v105, v105
	v_fmac_f32_e32 v84, v103, v103
	s_nop 1
	v_add_f32_dpp v84, v84, v84 quad_perm:[1,0,3,2] row_mask:0xf bank_mask:0xf bound_ctrl:1
	s_nop 1
	v_add_f32_dpp v84, v84, v84 quad_perm:[2,3,0,1] row_mask:0xf bank_mask:0xf bound_ctrl:1
	s_nop 1
	v_add_f32_dpp v84, v84, v84 row_half_mirror row_mask:0xf bank_mask:0xf bound_ctrl:1
	s_nop 1
	v_add_f32_dpp v84, v84, v84 row_mirror row_mask:0xf bank_mask:0xf bound_ctrl:1
	s_nop 0
	v_readlane_b32 s37, v84, 16
	v_readlane_b32 s39, v84, 48
	v_readlane_b32 s36, v84, 0
	v_readlane_b32 s38, v84, 32
	v_mov_b32_e32 v84, s37
	v_mov_b32_e32 v85, s39
	v_add_f32_e32 v84, s36, v84
	v_add_f32_e32 v85, s38, v85
	v_add_f32_e32 v84, v84, v85
	v_fmamk_f32 v84, v84, 0x3baaaaab, v44
	v_rsq_f32_e32 v84, v84
	s_add_u32 s36, s31, s34
	s_addc_u32 s37, s30, s35
	s_mulk_i32 s37, 0x180
	v_mul_f32_e32 v85, v84, v105
	v_mul_f32_e32 v91, v84, v104
	v_mul_f32_e32 v84, v84, v103
	v_mul_f32_e32 v84, v35, v84
	v_mov_b32_e32 v92, v84
	v_mov_b32_e32 v98, v84
	s_nop 1
	v_permlane32_swap_b32_e32 v92, v98
	v_cndmask_b32_e64 v92, v92, v98, s[4:5]
	v_mul_f32_e32 v92, v114, v92
	v_cndmask_b32_e64 v92, v92, -v92, s[4:5]
	v_mul_f32_e32 v85, v37, v85
	v_fmac_f32_e32 v92, v113, v84
	v_mul_f32_e32 v91, v36, v91
	v_cndmask_b32_e32 v92, v84, v92, vcc
	v_cvt_pk_bf16_f32 v98, v85, v19
	v_mad_u64_u32 v[84:85], s[34:35], s36, v47, v[30:31]
	v_add_u32_e32 v85, s37, v85
	v_cvt_pk_bf16_f32 v91, v91, v19
	global_store_short v[84:85], v98, off
	global_store_short v[84:85], v91, off offset:128
	v_cvt_pk_bf16_f32 v91, v92, v19
	global_store_short v[84:85], v91, off offset:256
	v_mul_f32_e32 v84, v101, v101
	v_fmac_f32_e32 v84, v102, v102
	v_fmac_f32_e32 v84, v100, v100
	s_cmpk_lt_i32 s21, 0x800
	s_nop 0
	v_add_f32_dpp v84, v84, v84 quad_perm:[1,0,3,2] row_mask:0xf bank_mask:0xf bound_ctrl:1
	s_nop 1
	v_add_f32_dpp v84, v84, v84 quad_perm:[2,3,0,1] row_mask:0xf bank_mask:0xf bound_ctrl:1
	s_nop 1
	v_add_f32_dpp v84, v84, v84 row_half_mirror row_mask:0xf bank_mask:0xf bound_ctrl:1
	s_nop 1
	v_add_f32_dpp v84, v84, v84 row_mirror row_mask:0xf bank_mask:0xf bound_ctrl:1
	s_nop 0
	v_readlane_b32 s35, v84, 16
	v_readlane_b32 s39, v84, 48
	v_readlane_b32 s34, v84, 0
	v_readlane_b32 s38, v84, 32
	v_mov_b32_e32 v84, s35
	v_mov_b32_e32 v85, s39
	v_add_f32_e32 v84, s34, v84
	v_add_f32_e32 v85, s38, v85
	v_add_f32_e32 v84, v84, v85
	v_fmamk_f32 v84, v84, 0x3baaaaab, v44
	v_rsq_f32_e32 v84, v84
	s_nop 0
	v_mul_f32_e32 v85, v84, v102
	v_mul_f32_e32 v91, v84, v101
	v_mul_f32_e32 v84, v84, v100
	v_mul_f32_e32 v84, v11, v84
	v_mov_b32_e32 v92, v84
	v_mov_b32_e32 v98, v84
	s_nop 1
	v_permlane32_swap_b32_e32 v92, v98
	v_cndmask_b32_e64 v92, v92, v98, s[4:5]
	v_mul_f32_e32 v92, v114, v92
	v_cndmask_b32_e64 v92, v92, -v92, s[4:5]
	v_mul_f32_e32 v85, v13, v85
	v_fmac_f32_e32 v92, v113, v84
	v_mul_f32_e32 v91, v12, v91
	v_cndmask_b32_e32 v92, v84, v92, vcc
	v_cvt_pk_bf16_f32 v98, v85, v19
	v_mad_u64_u32 v[84:85], s[34:35], s36, v47, v[32:33]
	v_add_u32_e32 v85, s37, v85
	v_cvt_pk_bf16_f32 v91, v91, v19
	global_store_short v[84:85], v98, off
	global_store_short v[84:85], v91, off offset:128
	v_cvt_pk_bf16_f32 v91, v92, v19
	global_store_short v[84:85], v91, off offset:256
	v_mul_f32_e32 v84, v96, v96
	v_fmac_f32_e32 v84, v97, v97
	v_fmac_f32_e32 v84, v95, v95
	s_cselect_b64 vcc, -1, 0
	s_and_b32 s35, s21, 63
	v_add_f32_dpp v84, v84, v84 quad_perm:[1,0,3,2] row_mask:0xf bank_mask:0xf bound_ctrl:1
	ds_write_b16 v39, v77 offset:768
	ds_write_b16 v39, v78 offset:896
	v_add_f32_dpp v84, v84, v84 quad_perm:[2,3,0,1] row_mask:0xf bank_mask:0xf bound_ctrl:1
	s_ashr_i32 s34, s21, 6
	v_mov_b32_e32 v77, s35
	v_add_f32_dpp v84, v84, v84 row_half_mirror row_mask:0xf bank_mask:0xf bound_ctrl:1
	v_mov_b32_e32 v78, s34
	v_cndmask_b32_e64 v77, v77, v78, s[0:1]
	v_add_f32_dpp v84, v84, v84 row_mirror row_mask:0xf bank_mask:0xf bound_ctrl:1
	v_cvt_f32_i32_e32 v77, v77
	v_readlane_b32 s36, v84, 16
	v_readlane_b32 s38, v84, 48
	v_readlane_b32 s35, v84, 0
	v_readlane_b32 s37, v84, 32
	v_mov_b32_e32 v84, s36
	v_mov_b32_e32 v85, s38
	v_add_f32_e32 v84, s35, v84
	v_add_f32_e32 v85, s37, v85
	v_add_f32_e32 v84, v84, v85
	v_fmamk_f32 v84, v84, 0x3baaaaab, v44
	v_rsq_f32_e32 v84, v84
	v_mul_f32_e32 v77, v1, v77
	v_mul_f32_e32 v77, 0.15915494, v77
	v_cos_f32_e32 v78, v77
	v_mul_f32_e32 v85, v84, v97
	v_mul_f32_e32 v91, v84, v96
	v_mul_f32_e32 v84, v84, v95
	v_sin_f32_e32 v77, v77
	v_mul_f32_e32 v84, v35, v84
	v_mov_b32_e32 v92, v84
	v_mov_b32_e32 v95, v84
	s_nop 1
	v_permlane32_swap_b32_e32 v92, v95
	v_cndmask_b32_e64 v92, v92, v95, s[4:5]
	s_ashr_i32 s34, s21, 31
	v_mul_f32_e32 v92, v77, v92
	v_cndmask_b32_e64 v92, v92, -v92, s[4:5]
	s_add_u32 s35, s22, s21
	v_mul_f32_e32 v85, v37, v85
	v_fmac_f32_e32 v92, v78, v84
	s_addc_u32 s38, s23, s34
	v_mul_f32_e32 v91, v36, v91
	v_cndmask_b32_e32 v92, v84, v92, vcc
	v_cvt_pk_bf16_f32 v95, v85, v19
	v_mad_u64_u32 v[84:85], s[36:37], s35, v47, v[30:31]
	s_mulk_i32 s38, 0x180
	v_add_u32_e32 v85, s38, v85
	v_cvt_pk_bf16_f32 v91, v91, v19
	global_store_short v[84:85], v95, off
	global_store_short v[84:85], v91, off offset:128
	v_cvt_pk_bf16_f32 v91, v92, v19
	global_store_short v[84:85], v91, off offset:256
	v_mul_f32_e32 v84, v93, v93
	v_fmac_f32_e32 v84, v94, v94
	v_fmac_f32_e32 v84, v69, v69
	s_nop 1
	v_add_f32_dpp v84, v84, v84 quad_perm:[1,0,3,2] row_mask:0xf bank_mask:0xf bound_ctrl:1
	s_nop 1
	v_add_f32_dpp v84, v84, v84 quad_perm:[2,3,0,1] row_mask:0xf bank_mask:0xf bound_ctrl:1
	s_nop 1
	v_add_f32_dpp v84, v84, v84 row_half_mirror row_mask:0xf bank_mask:0xf bound_ctrl:1
	s_nop 1
	v_add_f32_dpp v84, v84, v84 row_mirror row_mask:0xf bank_mask:0xf bound_ctrl:1
	s_nop 0
	v_readlane_b32 s37, v84, 16
	v_readlane_b32 s40, v84, 48
	v_readlane_b32 s36, v84, 0
	v_readlane_b32 s39, v84, 32
	v_mov_b32_e32 v84, s37
	v_mov_b32_e32 v85, s40
	v_add_f32_e32 v84, s36, v84
	v_add_f32_e32 v85, s39, v85
	v_add_f32_e32 v84, v84, v85
	v_fmamk_f32 v84, v84, 0x3baaaaab, v44
	v_rsq_f32_e32 v84, v84
	s_nop 0
	v_mul_f32_e32 v85, v84, v94
	v_mul_f32_e32 v91, v84, v93
	v_mul_f32_e32 v84, v84, v69
	v_mul_f32_e32 v84, v11, v84
	v_mov_b32_e32 v92, v84
	v_mov_b32_e32 v93, v84
	s_nop 1
	v_permlane32_swap_b32_e32 v92, v93
	v_cndmask_b32_e64 v92, v92, v93, s[4:5]
	v_mul_f32_e32 v92, v77, v92
	v_cndmask_b32_e64 v92, v92, -v92, s[4:5]
	v_mul_f32_e32 v85, v13, v85
	v_fmac_f32_e32 v92, v78, v84
	v_mul_f32_e32 v91, v12, v91
	v_cndmask_b32_e32 v92, v84, v92, vcc
	v_cvt_pk_bf16_f32 v93, v85, v19
	v_mad_u64_u32 v[84:85], s[36:37], s35, v47, v[32:33]
	v_add_u32_e32 v85, s38, v85
	v_cvt_pk_bf16_f32 v91, v91, v19
	global_store_short v[84:85], v93, off
	global_store_short v[84:85], v91, off offset:128
	v_cvt_pk_bf16_f32 v91, v92, v19
	global_store_short v[84:85], v91, off offset:256
	ds_write_b16 v40, v70
	ds_write_b16 v40, v71 offset:128
	v_mul_f32_e32 v70, v89, v89
	v_fmac_f32_e32 v70, v90, v90
	v_fmac_f32_e32 v70, v88, v88
	s_nop 1
	v_add_f32_dpp v70, v70, v70 quad_perm:[1,0,3,2] row_mask:0xf bank_mask:0xf bound_ctrl:1
	s_nop 1
	v_add_f32_dpp v70, v70, v70 quad_perm:[2,3,0,1] row_mask:0xf bank_mask:0xf bound_ctrl:1
	s_nop 1
	v_add_f32_dpp v70, v70, v70 row_half_mirror row_mask:0xf bank_mask:0xf bound_ctrl:1
	s_nop 1
	v_add_f32_dpp v70, v70, v70 row_mirror row_mask:0xf bank_mask:0xf bound_ctrl:1
	s_nop 0
	v_readlane_b32 s36, v70, 16
	v_readlane_b32 s38, v70, 48
	v_readlane_b32 s35, v70, 0
	v_readlane_b32 s37, v70, 32
	v_mov_b32_e32 v70, s36
	v_mov_b32_e32 v71, s38
	v_add_f32_e32 v70, s35, v70
	v_add_f32_e32 v71, s37, v71
	v_add_f32_e32 v70, v70, v71
	v_fmamk_f32 v70, v70, 0x3baaaaab, v44
	v_rsq_f32_e32 v70, v70
	s_add_u32 s35, s25, s21
	s_addc_u32 s38, s24, s34
	s_mulk_i32 s38, 0x180
	v_mul_f32_e32 v71, v70, v90
	v_mul_f32_e32 v84, v70, v89
	v_mul_f32_e32 v70, v70, v88
	v_mul_f32_e32 v70, v35, v70
	v_mov_b32_e32 v85, v70
	v_mov_b32_e32 v88, v70
	s_nop 1
	v_permlane32_swap_b32_e32 v85, v88
	v_cndmask_b32_e64 v85, v85, v88, s[4:5]
	v_mul_f32_e32 v85, v77, v85
	v_cndmask_b32_e64 v85, v85, -v85, s[4:5]
	v_mul_f32_e32 v71, v37, v71
	v_fmac_f32_e32 v85, v78, v70
	v_mul_f32_e32 v84, v36, v84
	v_cndmask_b32_e32 v85, v70, v85, vcc
	v_cvt_pk_bf16_f32 v88, v71, v19
	v_mad_u64_u32 v[70:71], s[36:37], s35, v47, v[30:31]
	v_add_u32_e32 v71, s38, v71
	v_cvt_pk_bf16_f32 v84, v84, v19
	global_store_short v[70:71], v88, off
	global_store_short v[70:71], v84, off offset:128
	v_cvt_pk_bf16_f32 v84, v85, v19
	global_store_short v[70:71], v84, off offset:256
	v_mul_f32_e32 v70, v86, v86
	v_fmac_f32_e32 v70, v87, v87
	v_fmac_f32_e32 v70, v69, v69
	s_nop 1
	v_add_f32_dpp v70, v70, v70 quad_perm:[1,0,3,2] row_mask:0xf bank_mask:0xf bound_ctrl:1
	s_nop 1
	v_add_f32_dpp v70, v70, v70 quad_perm:[2,3,0,1] row_mask:0xf bank_mask:0xf bound_ctrl:1
	s_nop 1
	v_add_f32_dpp v70, v70, v70 row_half_mirror row_mask:0xf bank_mask:0xf bound_ctrl:1
	s_nop 1
	v_add_f32_dpp v70, v70, v70 row_mirror row_mask:0xf bank_mask:0xf bound_ctrl:1
	s_nop 0
	v_readlane_b32 s37, v70, 16
	v_readlane_b32 s40, v70, 48
	v_readlane_b32 s36, v70, 0
	v_readlane_b32 s39, v70, 32
	v_mov_b32_e32 v70, s37
	v_mov_b32_e32 v71, s40
	v_add_f32_e32 v70, s36, v70
	v_add_f32_e32 v71, s39, v71
	v_add_f32_e32 v70, v70, v71
	v_fmamk_f32 v70, v70, 0x3baaaaab, v44
	v_rsq_f32_e32 v70, v70
	s_nop 0
	v_mul_f32_e32 v71, v70, v87
	v_mul_f32_e32 v84, v70, v86
	v_mul_f32_e32 v70, v70, v69
	v_mul_f32_e32 v70, v11, v70
	v_mov_b32_e32 v85, v70
	v_mov_b32_e32 v86, v70
	s_nop 1
	v_permlane32_swap_b32_e32 v85, v86
	v_cndmask_b32_e64 v85, v85, v86, s[4:5]
	v_mul_f32_e32 v85, v77, v85
	v_cndmask_b32_e64 v85, v85, -v85, s[4:5]
	v_mul_f32_e32 v71, v13, v71
	v_fmac_f32_e32 v85, v78, v70
	v_mul_f32_e32 v84, v12, v84
	v_cndmask_b32_e32 v85, v70, v85, vcc
	v_cvt_pk_bf16_f32 v86, v71, v19
	v_mad_u64_u32 v[70:71], s[36:37], s35, v47, v[32:33]
	v_add_u32_e32 v71, s38, v71
	v_cvt_pk_bf16_f32 v84, v84, v19
	global_store_short v[70:71], v86, off
	global_store_short v[70:71], v84, off offset:128
	v_cvt_pk_bf16_f32 v84, v85, v19
	global_store_short v[70:71], v84, off offset:256
	ds_write_b16 v40, v64 offset:256
	ds_write_b16 v40, v65 offset:384
	v_mul_f32_e32 v64, v82, v82
	v_fmac_f32_e32 v64, v83, v83
	v_fmac_f32_e32 v64, v81, v81
	s_nop 1
	v_add_f32_dpp v64, v64, v64 quad_perm:[1,0,3,2] row_mask:0xf bank_mask:0xf bound_ctrl:1
	s_nop 1
	v_add_f32_dpp v64, v64, v64 quad_perm:[2,3,0,1] row_mask:0xf bank_mask:0xf bound_ctrl:1
	s_nop 1
	v_add_f32_dpp v64, v64, v64 row_half_mirror row_mask:0xf bank_mask:0xf bound_ctrl:1
	s_nop 1
	v_add_f32_dpp v64, v64, v64 row_mirror row_mask:0xf bank_mask:0xf bound_ctrl:1
	s_nop 0
	v_readlane_b32 s36, v64, 16
	v_readlane_b32 s38, v64, 48
	v_readlane_b32 s35, v64, 0
	v_readlane_b32 s37, v64, 32
	v_mov_b32_e32 v64, s36
	v_mov_b32_e32 v65, s38
	v_add_f32_e32 v64, s35, v64
	v_add_f32_e32 v65, s37, v65
	v_add_f32_e32 v64, v64, v65
	v_fmamk_f32 v64, v64, 0x3baaaaab, v44
	v_rsq_f32_e32 v64, v64
	s_add_u32 s35, s29, s21
	s_addc_u32 s38, s28, s34
	s_mulk_i32 s38, 0x180
	v_mul_f32_e32 v65, v64, v83
	v_mul_f32_e32 v70, v64, v82
	v_mul_f32_e32 v64, v64, v81
	v_mul_f32_e32 v64, v35, v64
	v_mov_b32_e32 v71, v64
	v_mov_b32_e32 v81, v64
	s_nop 1
	v_permlane32_swap_b32_e32 v71, v81
	v_cndmask_b32_e64 v71, v71, v81, s[4:5]
	v_mul_f32_e32 v71, v77, v71
	v_cndmask_b32_e64 v71, v71, -v71, s[4:5]
	v_mul_f32_e32 v65, v37, v65
	v_fmac_f32_e32 v71, v78, v64
	v_mul_f32_e32 v70, v36, v70
	v_cndmask_b32_e32 v71, v64, v71, vcc
	v_cvt_pk_bf16_f32 v81, v65, v19
	v_mad_u64_u32 v[64:65], s[36:37], s35, v47, v[30:31]
	v_add_u32_e32 v65, s38, v65
	v_cvt_pk_bf16_f32 v70, v70, v19
	global_store_short v[64:65], v81, off
	global_store_short v[64:65], v70, off offset:128
	v_cvt_pk_bf16_f32 v70, v71, v19
	global_store_short v[64:65], v70, off offset:256
	v_mul_f32_e32 v64, v79, v79
	v_fmac_f32_e32 v64, v80, v80
	v_fmac_f32_e32 v64, v69, v69
	s_add_u32 s21, s31, s21
	s_nop 0
	v_add_f32_dpp v64, v64, v64 quad_perm:[1,0,3,2] row_mask:0xf bank_mask:0xf bound_ctrl:1
	s_nop 1
	v_add_f32_dpp v64, v64, v64 quad_perm:[2,3,0,1] row_mask:0xf bank_mask:0xf bound_ctrl:1
	s_nop 1
	v_add_f32_dpp v64, v64, v64 row_half_mirror row_mask:0xf bank_mask:0xf bound_ctrl:1
	s_nop 1
	v_add_f32_dpp v64, v64, v64 row_mirror row_mask:0xf bank_mask:0xf bound_ctrl:1
	s_nop 0
	v_readlane_b32 s37, v64, 16
	v_readlane_b32 s40, v64, 48
	v_readlane_b32 s36, v64, 0
	v_readlane_b32 s39, v64, 32
	v_mov_b32_e32 v64, s37
	v_mov_b32_e32 v65, s40
	v_add_f32_e32 v64, s36, v64
	v_add_f32_e32 v65, s39, v65
	v_add_f32_e32 v64, v64, v65
	v_fmamk_f32 v64, v64, 0x3baaaaab, v44
	v_rsq_f32_e32 v64, v64
	s_nop 0
	v_mul_f32_e32 v65, v64, v80
	v_mul_f32_e32 v70, v64, v79
	v_mul_f32_e32 v64, v64, v69
	v_mul_f32_e32 v64, v11, v64
	v_mov_b32_e32 v71, v64
	v_mov_b32_e32 v79, v64
	s_nop 1
	v_permlane32_swap_b32_e32 v71, v79
	v_cndmask_b32_e64 v71, v71, v79, s[4:5]
	v_mul_f32_e32 v71, v77, v71
	v_cndmask_b32_e64 v71, v71, -v71, s[4:5]
	v_mul_f32_e32 v65, v13, v65
	v_fmac_f32_e32 v71, v78, v64
	v_mul_f32_e32 v70, v12, v70
	v_cndmask_b32_e32 v71, v64, v71, vcc
	v_cvt_pk_bf16_f32 v79, v65, v19
	v_mad_u64_u32 v[64:65], s[36:37], s35, v47, v[32:33]
	v_add_u32_e32 v65, s38, v65
	v_cvt_pk_bf16_f32 v70, v70, v19
	global_store_short v[64:65], v79, off
	global_store_short v[64:65], v70, off offset:128
	v_cvt_pk_bf16_f32 v70, v71, v19
	global_store_short v[64:65], v70, off offset:256
	ds_write_b16 v40, v57 offset:512
	ds_write_b16 v40, v58 offset:640
	v_mul_f32_e32 v57, v75, v75
	v_fmac_f32_e32 v57, v76, v76
	v_fmac_f32_e32 v57, v74, v74
	s_nop 1
	v_add_f32_dpp v57, v57, v57 quad_perm:[1,0,3,2] row_mask:0xf bank_mask:0xf bound_ctrl:1
	s_nop 1
	v_add_f32_dpp v57, v57, v57 quad_perm:[2,3,0,1] row_mask:0xf bank_mask:0xf bound_ctrl:1
	s_nop 1
	v_add_f32_dpp v57, v57, v57 row_half_mirror row_mask:0xf bank_mask:0xf bound_ctrl:1
	s_nop 1
	v_add_f32_dpp v57, v57, v57 row_mirror row_mask:0xf bank_mask:0xf bound_ctrl:1
	s_nop 0
	v_readlane_b32 s36, v57, 16
	v_readlane_b32 s38, v57, 48
	v_readlane_b32 s35, v57, 0
	v_readlane_b32 s37, v57, 32
	v_mov_b32_e32 v57, s36
	v_mov_b32_e32 v58, s38
	v_add_f32_e32 v57, s35, v57
	v_add_f32_e32 v58, s37, v58
	v_add_f32_e32 v57, v57, v58
	v_fmamk_f32 v57, v57, 0x3baaaaab, v44
	v_rsq_f32_e32 v57, v57
	s_addc_u32 s36, s30, s34
	s_mulk_i32 s36, 0x180
	s_cmpk_lt_i32 s13, 0x800
	v_mul_f32_e32 v58, v57, v76
	v_mul_f32_e32 v64, v57, v75
	v_mul_f32_e32 v57, v57, v74
	v_mul_f32_e32 v57, v35, v57
	v_mul_f32_e32 v70, v36, v64
	v_mov_b32_e32 v64, v57
	v_mov_b32_e32 v65, v57
	s_nop 1
	v_permlane32_swap_b32_e32 v64, v65
	v_cndmask_b32_e64 v64, v64, v65, s[4:5]
	v_mul_f32_e32 v64, v77, v64
	v_cndmask_b32_e64 v64, v64, -v64, s[4:5]
	v_fmac_f32_e32 v64, v78, v57
	v_cndmask_b32_e32 v57, v57, v64, vcc
	v_mad_u64_u32 v[64:65], s[34:35], s21, v47, v[30:31]
	v_add_u32_e32 v65, s36, v65
	v_cvt_pk_bf16_f32 v57, v57, v19
	global_store_short v[64:65], v57, off offset:256
	v_mul_f32_e32 v57, v72, v72
	v_fmac_f32_e32 v57, v73, v73
	v_fmac_f32_e32 v57, v69, v69
	v_mul_f32_e32 v58, v37, v58
	v_cvt_pk_bf16_f32 v58, v58, v19
	global_store_short v[64:65], v58, off
	v_add_f32_dpp v57, v57, v57 quad_perm:[1,0,3,2] row_mask:0xf bank_mask:0xf bound_ctrl:1
	v_cvt_pk_bf16_f32 v58, v70, v19
	global_store_short v[64:65], v58, off offset:128
	s_nop 0
	v_add_f32_dpp v57, v57, v57 quad_perm:[2,3,0,1] row_mask:0xf bank_mask:0xf bound_ctrl:1
	s_nop 1
	v_add_f32_dpp v57, v57, v57 row_half_mirror row_mask:0xf bank_mask:0xf bound_ctrl:1
	s_nop 1
	v_add_f32_dpp v57, v57, v57 row_mirror row_mask:0xf bank_mask:0xf bound_ctrl:1
	s_nop 0
	v_readlane_b32 s35, v57, 16
	v_readlane_b32 s38, v57, 48
	v_readlane_b32 s34, v57, 0
	v_readlane_b32 s37, v57, 32
	v_mov_b32_e32 v57, s35
	v_mov_b32_e32 v58, s38
	v_add_f32_e32 v57, s34, v57
	v_add_f32_e32 v58, s37, v58
	v_add_f32_e32 v57, v57, v58
	v_fmamk_f32 v57, v57, 0x3baaaaab, v44
	v_rsq_f32_e32 v57, v57
	s_nop 0
	v_mul_f32_e32 v58, v57, v73
	v_mul_f32_e32 v64, v57, v72
	v_mul_f32_e32 v57, v57, v69
	v_mul_f32_e32 v57, v11, v57
	v_mul_f32_e32 v70, v12, v64
	v_mov_b32_e32 v64, v57
	v_mov_b32_e32 v65, v57
	s_nop 1
	v_permlane32_swap_b32_e32 v64, v65
	v_cndmask_b32_e64 v64, v64, v65, s[4:5]
	v_mul_f32_e32 v64, v77, v64
	v_cndmask_b32_e64 v64, v64, -v64, s[4:5]
	v_fmac_f32_e32 v64, v78, v57
	v_mul_f32_e32 v58, v13, v58
	v_cndmask_b32_e32 v57, v57, v64, vcc
	v_mad_u64_u32 v[64:65], s[34:35], s21, v47, v[32:33]
	v_cvt_pk_bf16_f32 v58, v58, v19
	v_add_u32_e32 v65, s36, v65
	s_cselect_b64 vcc, -1, 0
	s_ashr_i32 s21, s13, 6
	s_and_b32 s34, s13, 63
	global_store_short v[64:65], v58, off
	v_cvt_pk_bf16_f32 v58, v70, v19
	global_store_short v[64:65], v58, off offset:128
	v_cvt_pk_bf16_f32 v57, v57, v19
	global_store_short v[64:65], v57, off offset:256
	ds_write_b16 v40, v50 offset:768
	ds_write_b16 v40, v51 offset:896
	v_mov_b32_e32 v50, s34
	v_mov_b32_e32 v51, s21
	v_cndmask_b32_e64 v50, v50, v51, s[0:1]
	v_cvt_f32_i32_e32 v50, v50
	s_ashr_i32 s21, s13, 31
	v_mul_f32_e32 v50, v1, v50
	v_mul_f32_e32 v50, 0.15915494, v50
	v_cos_f32_e32 v57, v50
	v_sin_f32_e32 v58, v50
	v_mul_f32_e32 v50, v67, v67
	v_fmac_f32_e32 v50, v68, v68
	v_fmac_f32_e32 v50, v66, v66
	s_nop 1
	v_add_f32_dpp v50, v50, v50 quad_perm:[1,0,3,2] row_mask:0xf bank_mask:0xf bound_ctrl:1
	s_nop 1
	v_add_f32_dpp v50, v50, v50 quad_perm:[2,3,0,1] row_mask:0xf bank_mask:0xf bound_ctrl:1
	s_nop 1
	v_add_f32_dpp v50, v50, v50 row_half_mirror row_mask:0xf bank_mask:0xf bound_ctrl:1
	s_nop 1
	v_add_f32_dpp v50, v50, v50 row_mirror row_mask:0xf bank_mask:0xf bound_ctrl:1
	s_nop 0
	v_readlane_b32 s35, v50, 16
	v_readlane_b32 s37, v50, 48
	v_readlane_b32 s34, v50, 0
	v_readlane_b32 s36, v50, 32
	v_mov_b32_e32 v50, s35
	v_mov_b32_e32 v51, s37
	v_add_f32_e32 v50, s34, v50
	v_add_f32_e32 v51, s36, v51
	v_add_f32_e32 v50, v50, v51
	v_fmamk_f32 v50, v50, 0x3baaaaab, v44
	v_rsq_f32_e32 v50, v50
	s_add_u32 s34, s22, s13
	s_addc_u32 s35, s23, s21
	s_mulk_i32 s35, 0x180
	v_mul_f32_e32 v51, v50, v68
	v_mul_f32_e32 v64, v50, v67
	v_mul_f32_e32 v50, v50, v66
	v_mul_f32_e32 v50, v35, v50
	v_mov_b32_e32 v65, v50
	v_mov_b32_e32 v66, v50
	s_nop 1
	v_permlane32_swap_b32_e32 v65, v66
	v_cndmask_b32_e64 v65, v65, v66, s[4:5]
	v_mul_f32_e32 v65, v58, v65
	v_cndmask_b32_e64 v65, v65, -v65, s[4:5]
	v_mul_f32_e32 v51, v37, v51
	v_fmac_f32_e32 v65, v57, v50
	v_mul_f32_e32 v64, v36, v64
	v_cndmask_b32_e32 v65, v50, v65, vcc
	v_cvt_pk_bf16_f32 v66, v51, v19
	v_mad_u64_u32 v[50:51], s[22:23], s34, v47, v[30:31]
	v_add_u32_e32 v51, s35, v51
	v_cvt_pk_bf16_f32 v64, v64, v19
	global_store_short v[50:51], v66, off
	global_store_short v[50:51], v64, off offset:128
	v_cvt_pk_bf16_f32 v64, v65, v19
	global_store_short v[50:51], v64, off offset:256
	v_mul_f32_e32 v50, v62, v62
	v_fmac_f32_e32 v50, v63, v63
	v_fmac_f32_e32 v50, v8, v8
	s_add_u32 s25, s25, s13
	s_addc_u32 s24, s24, s21
	v_add_f32_dpp v50, v50, v50 quad_perm:[1,0,3,2] row_mask:0xf bank_mask:0xf bound_ctrl:1
	s_mulk_i32 s24, 0x180
	s_nop 0
	v_add_f32_dpp v50, v50, v50 quad_perm:[2,3,0,1] row_mask:0xf bank_mask:0xf bound_ctrl:1
	s_nop 1
	v_add_f32_dpp v50, v50, v50 row_half_mirror row_mask:0xf bank_mask:0xf bound_ctrl:1
	s_nop 1
	v_add_f32_dpp v50, v50, v50 row_mirror row_mask:0xf bank_mask:0xf bound_ctrl:1
	s_nop 0
	v_readlane_b32 s23, v50, 16
	v_readlane_b32 s37, v50, 48
	v_readlane_b32 s22, v50, 0
	v_readlane_b32 s36, v50, 32
	v_mov_b32_e32 v50, s23
	v_mov_b32_e32 v51, s37
	v_add_f32_e32 v50, s22, v50
	v_add_f32_e32 v51, s36, v51
	v_add_f32_e32 v50, v50, v51
	v_fmamk_f32 v50, v50, 0x3baaaaab, v44
	v_rsq_f32_e32 v50, v50
	s_nop 0
	v_mul_f32_e32 v51, v50, v63
	v_mul_f32_e32 v62, v50, v62
	v_mul_f32_e32 v50, v50, v8
	v_mul_f32_e32 v50, v11, v50
	v_mov_b32_e32 v63, v50
	v_mov_b32_e32 v64, v50
	s_nop 1
	v_permlane32_swap_b32_e32 v63, v64
	v_cndmask_b32_e64 v63, v63, v64, s[4:5]
	v_mul_f32_e32 v63, v58, v63
	v_cndmask_b32_e64 v63, v63, -v63, s[4:5]
	v_mul_f32_e32 v51, v13, v51
	v_fmac_f32_e32 v63, v57, v50
	v_mul_f32_e32 v62, v12, v62
	v_cndmask_b32_e32 v63, v50, v63, vcc
	v_cvt_pk_bf16_f32 v64, v51, v19
	v_mad_u64_u32 v[50:51], s[22:23], s34, v47, v[32:33]
	v_add_u32_e32 v51, s35, v51
	v_cvt_pk_bf16_f32 v62, v62, v19
	global_store_short v[50:51], v64, off
	global_store_short v[50:51], v62, off offset:128
	v_cvt_pk_bf16_f32 v62, v63, v19
	global_store_short v[50:51], v62, off offset:256
	ds_write_b16 v41, v14
	ds_write_b16 v41, v15 offset:128
	v_mul_f32_e32 v14, v60, v60
	v_fmac_f32_e32 v14, v61, v61
	v_fmac_f32_e32 v14, v59, v59
	s_nop 1
	v_add_f32_dpp v14, v14, v14 quad_perm:[1,0,3,2] row_mask:0xf bank_mask:0xf bound_ctrl:1
	s_nop 1
	v_add_f32_dpp v14, v14, v14 quad_perm:[2,3,0,1] row_mask:0xf bank_mask:0xf bound_ctrl:1
	s_nop 1
	v_add_f32_dpp v14, v14, v14 row_half_mirror row_mask:0xf bank_mask:0xf bound_ctrl:1
	s_nop 1
	v_add_f32_dpp v14, v14, v14 row_mirror row_mask:0xf bank_mask:0xf bound_ctrl:1
	s_nop 0
	v_readlane_b32 s23, v14, 16
	v_readlane_b32 s35, v14, 48
	v_readlane_b32 s22, v14, 0
	v_readlane_b32 s34, v14, 32
	v_mov_b32_e32 v14, s23
	v_mov_b32_e32 v15, s35
	v_add_f32_e32 v14, s22, v14
	v_add_f32_e32 v15, s34, v15
	v_add_f32_e32 v14, v14, v15
	v_fmamk_f32 v14, v14, 0x3baaaaab, v44
	v_rsq_f32_e32 v14, v14
	s_nop 0
	v_mul_f32_e32 v15, v14, v61
	v_mul_f32_e32 v50, v14, v60
	v_mul_f32_e32 v14, v14, v59
	v_mul_f32_e32 v14, v35, v14
	v_mov_b32_e32 v51, v14
	v_mov_b32_e32 v59, v14
	s_nop 1
	v_permlane32_swap_b32_e32 v51, v59
	v_cndmask_b32_e64 v51, v51, v59, s[4:5]
	v_mul_f32_e32 v51, v58, v51
	v_cndmask_b32_e64 v51, v51, -v51, s[4:5]
	v_mul_f32_e32 v15, v37, v15
	v_fmac_f32_e32 v51, v57, v14
	v_mul_f32_e32 v50, v36, v50
	v_cndmask_b32_e32 v51, v14, v51, vcc
	v_cvt_pk_bf16_f32 v59, v15, v19
	v_mad_u64_u32 v[14:15], s[22:23], s25, v47, v[30:31]
	v_add_u32_e32 v15, s24, v15
	v_cvt_pk_bf16_f32 v50, v50, v19
	global_store_short v[14:15], v59, off
	global_store_short v[14:15], v50, off offset:128
	v_cvt_pk_bf16_f32 v50, v51, v19
	global_store_short v[14:15], v50, off offset:256
	v_mul_f32_e32 v14, v55, v55
	v_fmac_f32_e32 v14, v56, v56
	v_fmac_f32_e32 v14, v8, v8
	s_nop 1
	v_add_f32_dpp v14, v14, v14 quad_perm:[1,0,3,2] row_mask:0xf bank_mask:0xf bound_ctrl:1
	s_nop 1
	v_add_f32_dpp v14, v14, v14 quad_perm:[2,3,0,1] row_mask:0xf bank_mask:0xf bound_ctrl:1
	s_nop 1
	v_add_f32_dpp v14, v14, v14 row_half_mirror row_mask:0xf bank_mask:0xf bound_ctrl:1
	s_nop 1
	v_add_f32_dpp v14, v14, v14 row_mirror row_mask:0xf bank_mask:0xf bound_ctrl:1
	s_nop 0
	v_readlane_b32 s23, v14, 16
	v_readlane_b32 s35, v14, 48
	v_readlane_b32 s22, v14, 0
	v_readlane_b32 s34, v14, 32
	v_mov_b32_e32 v14, s23
	v_mov_b32_e32 v15, s35
	v_add_f32_e32 v14, s22, v14
	v_add_f32_e32 v15, s34, v15
	v_add_f32_e32 v14, v14, v15
	v_fmamk_f32 v14, v14, 0x3baaaaab, v44
	v_rsq_f32_e32 v14, v14
	s_nop 0
	v_mul_f32_e32 v15, v14, v56
	v_mul_f32_e32 v50, v14, v55
	v_mul_f32_e32 v14, v14, v8
	v_mul_f32_e32 v14, v11, v14
	v_mov_b32_e32 v51, v14
	v_mov_b32_e32 v55, v14
	s_nop 1
	v_permlane32_swap_b32_e32 v51, v55
	v_cndmask_b32_e64 v51, v51, v55, s[4:5]
	v_mul_f32_e32 v51, v58, v51
	v_cndmask_b32_e64 v51, v51, -v51, s[4:5]
	v_mul_f32_e32 v15, v13, v15
	v_fmac_f32_e32 v51, v57, v14
	v_mul_f32_e32 v50, v12, v50
	v_cndmask_b32_e32 v51, v14, v51, vcc
	v_cvt_pk_bf16_f32 v55, v15, v19
	v_mad_u64_u32 v[14:15], s[22:23], s25, v47, v[32:33]
	v_add_u32_e32 v15, s24, v15
	v_cvt_pk_bf16_f32 v50, v50, v19
	global_store_short v[14:15], v55, off
	global_store_short v[14:15], v50, off offset:128
	v_cvt_pk_bf16_f32 v50, v51, v19
	global_store_short v[14:15], v50, off offset:256
	ds_write_b16 v41, v6 offset:256
	ds_write_b16 v41, v7 offset:384
	v_mul_f32_e32 v6, v53, v53
	v_fmac_f32_e32 v6, v54, v54
	v_fmac_f32_e32 v6, v52, v52
	s_nop 1
	v_add_f32_dpp v6, v6, v6 quad_perm:[1,0,3,2] row_mask:0xf bank_mask:0xf bound_ctrl:1
	s_nop 1
	v_add_f32_dpp v6, v6, v6 quad_perm:[2,3,0,1] row_mask:0xf bank_mask:0xf bound_ctrl:1
	s_nop 1
	v_add_f32_dpp v6, v6, v6 row_half_mirror row_mask:0xf bank_mask:0xf bound_ctrl:1
	s_nop 1
	v_add_f32_dpp v6, v6, v6 row_mirror row_mask:0xf bank_mask:0xf bound_ctrl:1
	s_nop 0
	v_readlane_b32 s23, v6, 16
	v_readlane_b32 s25, v6, 48
	v_readlane_b32 s22, v6, 0
	v_readlane_b32 s24, v6, 32
	v_mov_b32_e32 v6, s23
	v_mov_b32_e32 v7, s25
	v_add_f32_e32 v6, s22, v6
	v_add_f32_e32 v7, s24, v7
	v_add_f32_e32 v6, v6, v7
	v_fmamk_f32 v6, v6, 0x3baaaaab, v44
	v_rsq_f32_e32 v6, v6
	s_add_u32 s24, s29, s13
	s_addc_u32 s25, s28, s21
	s_mulk_i32 s25, 0x180
	v_mul_f32_e32 v7, v6, v54
	v_mul_f32_e32 v14, v6, v53
	v_mul_f32_e32 v6, v6, v52
	v_mul_f32_e32 v6, v35, v6
	v_mov_b32_e32 v15, v6
	v_mov_b32_e32 v50, v6
	s_nop 1
	v_permlane32_swap_b32_e32 v15, v50
	v_cndmask_b32_e64 v15, v15, v50, s[4:5]
	v_mul_f32_e32 v15, v58, v15
	v_cndmask_b32_e64 v15, v15, -v15, s[4:5]
	v_mul_f32_e32 v7, v37, v7
	v_fmac_f32_e32 v15, v57, v6
	v_mul_f32_e32 v14, v36, v14
	v_cndmask_b32_e32 v15, v6, v15, vcc
	v_cvt_pk_bf16_f32 v50, v7, v19
	v_mad_u64_u32 v[6:7], s[22:23], s24, v47, v[30:31]
	v_add_u32_e32 v7, s25, v7
	v_cvt_pk_bf16_f32 v14, v14, v19
	global_store_short v[6:7], v50, off
	global_store_short v[6:7], v14, off offset:128
	v_cvt_pk_bf16_f32 v14, v15, v19
	global_store_short v[6:7], v14, off offset:256
	v_mul_f32_e32 v6, v48, v48
	v_fmac_f32_e32 v6, v49, v49
	v_fmac_f32_e32 v6, v8, v8
	s_add_u32 s13, s31, s13
	s_addc_u32 s21, s30, s21
	v_add_f32_dpp v6, v6, v6 quad_perm:[1,0,3,2] row_mask:0xf bank_mask:0xf bound_ctrl:1
	s_mulk_i32 s21, 0x180
	s_add_i32 s19, s19, s3
	v_add_f32_dpp v6, v6, v6 quad_perm:[2,3,0,1] row_mask:0xf bank_mask:0xf bound_ctrl:1
	s_add_i32 s18, s18, s16
	s_nop 0
	v_add_f32_dpp v6, v6, v6 row_half_mirror row_mask:0xf bank_mask:0xf bound_ctrl:1
	s_nop 1
	v_add_f32_dpp v6, v6, v6 row_mirror row_mask:0xf bank_mask:0xf bound_ctrl:1
	s_nop 0
	v_readlane_b32 s23, v6, 16
	v_readlane_b32 s29, v6, 48
	v_readlane_b32 s22, v6, 0
	v_readlane_b32 s28, v6, 32
	v_mov_b32_e32 v6, s23
	v_mov_b32_e32 v7, s29
	v_add_f32_e32 v6, s22, v6
	v_add_f32_e32 v7, s28, v7
	v_add_f32_e32 v6, v6, v7
	v_fmamk_f32 v6, v6, 0x3baaaaab, v44
	v_rsq_f32_e32 v6, v6
	s_nop 0
	v_mul_f32_e32 v7, v6, v49
	v_mul_f32_e32 v14, v6, v48
	v_mul_f32_e32 v6, v6, v8
	v_mul_f32_e32 v6, v11, v6
	v_mov_b32_e32 v15, v6
	v_mov_b32_e32 v48, v6
	s_nop 1
	v_permlane32_swap_b32_e32 v15, v48
	v_cndmask_b32_e64 v15, v15, v48, s[4:5]
	v_mul_f32_e32 v15, v58, v15
	v_cndmask_b32_e64 v15, v15, -v15, s[4:5]
	v_mul_f32_e32 v7, v13, v7
	v_fmac_f32_e32 v15, v57, v6
	v_mul_f32_e32 v14, v12, v14
	v_cndmask_b32_e32 v15, v6, v15, vcc
	v_cvt_pk_bf16_f32 v48, v7, v19
	v_mad_u64_u32 v[6:7], s[22:23], s24, v47, v[32:33]
	v_add_u32_e32 v7, s25, v7
	v_cvt_pk_bf16_f32 v14, v14, v19
	global_store_short v[6:7], v48, off
	global_store_short v[6:7], v14, off offset:128
	v_cvt_pk_bf16_f32 v14, v15, v19
	global_store_short v[6:7], v14, off offset:256
	ds_write_b16 v41, v4 offset:512
	ds_write_b16 v41, v5 offset:640
	v_mul_f32_e32 v4, v17, v17
	v_fmac_f32_e32 v4, v34, v34
	v_fmac_f32_e32 v4, v16, v16
	s_nop 1
	v_add_f32_dpp v4, v4, v4 quad_perm:[1,0,3,2] row_mask:0xf bank_mask:0xf bound_ctrl:1
	s_nop 1
	v_add_f32_dpp v4, v4, v4 quad_perm:[2,3,0,1] row_mask:0xf bank_mask:0xf bound_ctrl:1
	s_nop 1
	v_add_f32_dpp v4, v4, v4 row_half_mirror row_mask:0xf bank_mask:0xf bound_ctrl:1
	s_nop 1
	v_add_f32_dpp v4, v4, v4 row_mirror row_mask:0xf bank_mask:0xf bound_ctrl:1
	s_nop 0
	v_readlane_b32 s23, v4, 16
	v_readlane_b32 s25, v4, 48
	v_readlane_b32 s22, v4, 0
	v_readlane_b32 s24, v4, 32
	v_mov_b32_e32 v4, s23
	v_mov_b32_e32 v5, s25
	v_add_f32_e32 v4, s22, v4
	v_add_f32_e32 v5, s24, v5
	v_add_f32_e32 v4, v4, v5
	v_fmamk_f32 v4, v4, 0x3baaaaab, v44
	v_rsq_f32_e32 v4, v4
	s_nop 0
	v_mul_f32_e32 v5, v4, v34
	v_mul_f32_e32 v6, v4, v17
	v_mul_f32_e32 v4, v4, v16
	v_mul_f32_e32 v4, v35, v4
	v_mov_b32_e32 v7, v4
	v_mov_b32_e32 v14, v4
	s_nop 1
	v_permlane32_swap_b32_e32 v7, v14
	v_cndmask_b32_e64 v7, v7, v14, s[4:5]
	v_mul_f32_e32 v7, v58, v7
	v_cndmask_b32_e64 v7, v7, -v7, s[4:5]
	v_mul_f32_e32 v5, v37, v5
	v_fmac_f32_e32 v7, v57, v4
	v_mul_f32_e32 v6, v36, v6
	v_cndmask_b32_e32 v7, v4, v7, vcc
	v_cvt_pk_bf16_f32 v14, v5, v19
	v_mad_u64_u32 v[4:5], s[22:23], s13, v47, v[30:31]
	v_add_u32_e32 v5, s21, v5
	v_cvt_pk_bf16_f32 v6, v6, v19
	global_store_short v[4:5], v14, off
	global_store_short v[4:5], v6, off offset:128
	v_cvt_pk_bf16_f32 v6, v7, v19
	global_store_short v[4:5], v6, off offset:256
	v_mul_f32_e32 v4, v9, v9
	v_fmac_f32_e32 v4, v10, v10
	v_fmac_f32_e32 v4, v8, v8
	v_mov_b64_e32 v[36:37], s[8:9]
	s_nop 0
	v_add_f32_dpp v4, v4, v4 quad_perm:[1,0,3,2] row_mask:0xf bank_mask:0xf bound_ctrl:1
	s_nop 1
	v_add_f32_dpp v4, v4, v4 quad_perm:[2,3,0,1] row_mask:0xf bank_mask:0xf bound_ctrl:1
	s_nop 1
	v_add_f32_dpp v4, v4, v4 row_half_mirror row_mask:0xf bank_mask:0xf bound_ctrl:1
	s_nop 1
	v_add_f32_dpp v4, v4, v4 row_mirror row_mask:0xf bank_mask:0xf bound_ctrl:1
	s_nop 0
	v_readlane_b32 s23, v4, 16
	v_readlane_b32 s25, v4, 48
	v_readlane_b32 s22, v4, 0
	v_readlane_b32 s24, v4, 32
	v_mov_b32_e32 v4, s23
	v_mov_b32_e32 v5, s25
	v_add_f32_e32 v4, s22, v4
	v_add_f32_e32 v5, s24, v5
	v_add_f32_e32 v4, v4, v5
	v_fmamk_f32 v4, v4, 0x3baaaaab, v44
	v_rsq_f32_e32 v4, v4
	s_nop 0
	v_mul_f32_e32 v5, v4, v10
	v_mul_f32_e32 v6, v4, v9
	v_mul_f32_e32 v4, v4, v8
	v_mul_f32_e32 v4, v11, v4
	v_mov_b32_e32 v7, v4
	v_mov_b32_e32 v8, v4
	s_nop 1
	v_permlane32_swap_b32_e32 v7, v8
	v_cndmask_b32_e64 v7, v7, v8, s[4:5]
	v_mul_f32_e32 v7, v58, v7
	v_cndmask_b32_e64 v7, v7, -v7, s[4:5]
	v_mul_f32_e32 v5, v13, v5
	v_fmac_f32_e32 v7, v57, v4
	v_mul_f32_e32 v6, v12, v6
	v_cndmask_b32_e32 v7, v4, v7, vcc
	v_cvt_pk_bf16_f32 v8, v5, v19
	v_mad_u64_u32 v[4:5], s[22:23], s13, v47, v[32:33]
	v_add_u32_e32 v5, s21, v5
	v_cvt_pk_bf16_f32 v6, v6, v19
	global_store_short v[4:5], v8, off
	global_store_short v[4:5], v6, off offset:128
	v_cvt_pk_bf16_f32 v6, v7, v19
	global_store_short v[4:5], v6, off offset:256
	ds_write_b16 v41, v2 offset:768
	ds_write_b16 v41, v3 offset:896
	s_waitcnt lgkmcnt(0)
	s_barrier
	ds_read_u16 v2, v42
	ds_read_u16 v248, v42 offset:1040
	ds_read_u16 v3, v42 offset:2080
	ds_read_u16 v249, v42 offset:3120
	ds_read_u16 v4, v42 offset:4160
	ds_read_u16 v250, v42 offset:5200
	ds_read_u16 v5, v42 offset:6240
	ds_read_u16 v251, v42 offset:7280
	ds_read_u16 v6, v42 offset:8320
	ds_read_u16 v252, v42 offset:9360
	ds_read_u16 v7, v42 offset:10400
	ds_read_u16 v253, v42 offset:11440
	ds_read_u16 v8, v42 offset:12480
	ds_read_u16 v254, v42 offset:13520
	ds_read_u16 v9, v42 offset:14560
	ds_read_u16 v255, v42 offset:15600
	s_ashr_i32 s13, s12, 31
	s_cmpk_gt_i32 s19, 0x11f
	s_waitcnt lgkmcnt(0)
	v_lshl_or_b32 v2, v248, 16, v2
	v_lshl_or_b32 v3, v249, 16, v3
	v_lshl_or_b32 v4, v250, 16, v4
	v_lshl_or_b32 v5, v251, 16, v5
	v_lshl_or_b32 v6, v252, 16, v6
	v_lshl_or_b32 v7, v253, 16, v7
	v_lshl_or_b32 v8, v254, 16, v8
	v_lshl_or_b32 v9, v255, 16, v9
	ds_read_u16 v10, v42 offset:16640
	ds_read_u16 v248, v42 offset:17680
	ds_read_u16 v11, v42 offset:18720
	ds_read_u16 v249, v42 offset:19760
	ds_read_u16 v12, v42 offset:20800
	ds_read_u16 v250, v42 offset:21840
	ds_read_u16 v13, v42 offset:22880
	ds_read_u16 v251, v42 offset:23920
	ds_read_u16 v14, v42 offset:24960
	ds_read_u16 v252, v42 offset:26000
	ds_read_u16 v15, v42 offset:27040
	ds_read_u16 v253, v42 offset:28080
	ds_read_u16 v16, v42 offset:29120
	ds_read_u16 v254, v42 offset:30160
	ds_read_u16 v17, v42 offset:31200
	ds_read_u16 v255, v42 offset:32240
	s_waitcnt lgkmcnt(0)
	v_lshl_or_b32 v10, v248, 16, v10
	v_lshl_or_b32 v11, v249, 16, v11
	v_lshl_or_b32 v12, v250, 16, v12
	v_lshl_or_b32 v13, v251, 16, v13
	v_lshl_or_b32 v14, v252, 16, v14
	v_lshl_or_b32 v15, v253, 16, v15
	v_lshl_or_b32 v16, v254, 16, v16
	v_lshl_or_b32 v17, v255, 16, v17
	v_or_b32_e32 v34, s20, v43
	v_ashrrev_i32_e32 v35, 31, v34
	v_lshlrev_b64 v[34:35], 7, v[34:35]
	v_or_b32_e32 v34, v34, v18
	v_mad_u64_u32 v[36:37], s[20:21], v34, s17, v[36:37]
	v_mad_i32_i24 v37, v35, s17, v37
	v_lshl_add_u64 v[34:35], s[12:13], 1, v[36:37]
	global_store_dwordx4 v[34:35], v[2:5], off
	global_store_dwordx4 v[34:35], v[6:9], off offset:16
	global_store_dwordx4 v[34:35], v[10:13], off offset:32
	global_store_dwordx4 v[34:35], v[14:17], off offset:48
	s_waitcnt vmcnt(63) expcnt(7) lgkmcnt(15)
	s_barrier
	s_cbranch_scc0 .LBB0_977
	s_branch .LBB0_974

.LBB0_3145:
	s_mul_hi_i32 s12, s19, 0x38e38e39
	s_lshr_b32 s13, s12, 31
	s_ashr_i32 s22, s12, 4
	s_add_i32 s22, s22, s13
	s_mul_i32 s13, s22, 0xfffff700
	s_add_i32 s23, s33, s18
	s_add_i32 s12, s18, s13
	s_add_i32 s35, s23, s13
	s_lshl_b32 s13, s22, 8
	s_add_i32 s30, s13, 0x1800
	s_lshl_b32 s31, s22, 11
	s_cmpk_lt_i32 s35, 0x800
	s_cselect_b64 vcc, -1, 0
	s_and_b64 s[20:21], vcc, exec
	s_cselect_b32 s13, s31, s30
	s_mul_i32 s36, s22, 0x900
	s_sub_i32 s13, s13, s36
	s_add_i32 s20, s23, s13
	s_ashr_i32 s21, s20, 31
	v_mad_i64_i32 v[2:3], s[24:25], s20, v45, v[20:21]
	s_lshl_b64 s[24:25], s[20:21], 11
	s_add_i32 s34, s35, 8
	s_cmpk_lt_i32 s35, 0x7f8
	s_cselect_b32 s13, s31, s30
	s_sub_i32 s13, s13, s36
	global_load_ushort v10, v[2:3], off
	v_mad_i64_i32 v[2:3], s[20:21], s20, v46, v[26:27]
	s_add_i32 s13, s23, s13
	v_lshl_add_u64 v[4:5], v[28:29], 0, s[24:25]
	s_add_i32 s20, s13, 8
	global_load_ushort v11, v[2:3], off
	global_load_ushort v12, v[2:3], off offset:128
	global_load_ushort v13, v[2:3], off offset:256
	global_load_ushort v16, v[4:5], off
	global_load_ushort v17, v[4:5], off offset:128
	global_load_ushort v124, v[4:5], off offset:256
	global_load_ushort v125, v[4:5], off offset:384
	global_load_ushort v34, v[2:3], off offset:384
	global_load_ushort v35, v[2:3], off offset:512
	global_load_ushort v36, v[2:3], off offset:640
	global_load_ushort v37, v[4:5], off offset:512
	global_load_ushort v48, v[4:5], off offset:640
	global_load_ushort v120, v[4:5], off offset:768
	global_load_ushort v121, v[4:5], off offset:896
	global_load_ushort v49, v[2:3], off offset:768
	global_load_ushort v52, v[2:3], off offset:896
	global_load_ushort v53, v[2:3], off offset:1024
	global_load_ushort v54, v[4:5], off offset:1024
	global_load_ushort v55, v[4:5], off offset:1152
	global_load_ushort v113, v[4:5], off offset:1280
	global_load_ushort v114, v[4:5], off offset:1408
	global_load_ushort v56, v[2:3], off offset:1152
	global_load_ushort v59, v[2:3], off offset:1280
	global_load_ushort v60, v[2:3], off offset:1408
	global_load_ushort v61, v[4:5], off offset:1536
	global_load_ushort v62, v[4:5], off offset:1664
	global_load_ushort v106, v[4:5], off offset:1792
	global_load_ushort v107, v[4:5], off offset:1920
	s_ashr_i32 s21, s20, 31
	v_mad_i64_i32 v[2:3], s[24:25], s20, v45, v[20:21]
	global_load_ushort v63, v[2:3], off
	s_lshl_b64 s[24:25], s[20:21], 11
	v_mad_i64_i32 v[2:3], s[20:21], s20, v46, v[26:27]
	s_add_i32 s21, s35, 16
	s_cmpk_lt_i32 s35, 0x7f0
	s_cselect_b32 s13, s31, s30
	s_sub_i32 s13, s13, s36
	s_add_i32 s13, s23, s13
	v_lshl_add_u64 v[4:5], v[28:29], 0, s[24:25]
	s_add_i32 s24, s13, 16
	global_load_ushort v66, v[2:3], off
	global_load_ushort v67, v[2:3], off offset:128
	global_load_ushort v68, v[2:3], off offset:256
	global_load_ushort v69, v[4:5], off
	global_load_ushort v72, v[4:5], off offset:128
	global_load_ushort v98, v[4:5], off offset:256
	global_load_ushort v99, v[4:5], off offset:384
	global_load_ushort v73, v[2:3], off offset:384
	global_load_ushort v74, v[2:3], off offset:512
	global_load_ushort v75, v[2:3], off offset:640
	global_load_ushort v76, v[4:5], off offset:512
	global_load_ushort v79, v[4:5], off offset:640
	global_load_ushort v91, v[4:5], off offset:768
	global_load_ushort v92, v[4:5], off offset:896
	global_load_ushort v80, v[2:3], off offset:768
	global_load_ushort v81, v[2:3], off offset:896
	global_load_ushort v82, v[2:3], off offset:1024
	global_load_ushort v83, v[4:5], off offset:1024
	global_load_ushort v86, v[4:5], off offset:1152
	global_load_ushort v84, v[4:5], off offset:1280
	global_load_ushort v85, v[4:5], off offset:1408
	global_load_ushort v87, v[2:3], off offset:1152
	global_load_ushort v88, v[2:3], off offset:1280
	global_load_ushort v89, v[2:3], off offset:1408
	global_load_ushort v90, v[4:5], off offset:1536
	global_load_ushort v93, v[4:5], off offset:1664
	global_load_ushort v77, v[4:5], off offset:1792
	global_load_ushort v78, v[4:5], off offset:1920
	s_ashr_i32 s25, s24, 31
	v_mad_i64_i32 v[2:3], s[28:29], s24, v45, v[20:21]
	s_lshl_b64 s[28:29], s[24:25], 11
	s_add_i32 s13, s35, 24
	s_cmpk_lt_i32 s35, 0x7e8
	s_cselect_b32 s20, s31, s30
	s_sub_i32 s20, s20, s36
	global_load_ushort v94, v[2:3], off
	v_mad_i64_i32 v[2:3], s[24:25], s24, v46, v[26:27]
	s_add_i32 s20, s23, s20
	v_lshl_add_u64 v[4:5], v[28:29], 0, s[28:29]
	s_add_i32 s24, s20, 24
	global_load_ushort v95, v[2:3], off
	global_load_ushort v96, v[2:3], off offset:128
	global_load_ushort v122, v[2:3], off offset:256
	global_load_ushort v123, v[4:5], off
	global_load_ushort v126, v[4:5], off offset:128
	global_load_ushort v70, v[4:5], off offset:256
	global_load_ushort v71, v[4:5], off offset:384
	global_load_ushort v127, v[2:3], off offset:384
	global_load_ushort v128, v[2:3], off offset:512
	global_load_ushort v129, v[2:3], off offset:640
	global_load_ushort v130, v[4:5], off offset:512
	global_load_ushort v131, v[4:5], off offset:640
	global_load_ushort v64, v[4:5], off offset:768
	global_load_ushort v65, v[4:5], off offset:896
	global_load_ushort v132, v[2:3], off offset:768
	global_load_ushort v133, v[2:3], off offset:896
	global_load_ushort v134, v[2:3], off offset:1024
	global_load_ushort v135, v[4:5], off offset:1024
	global_load_ushort v136, v[4:5], off offset:1152
	global_load_ushort v57, v[4:5], off offset:1280
	global_load_ushort v58, v[4:5], off offset:1408
	global_load_ushort v137, v[2:3], off offset:1152
	global_load_ushort v138, v[2:3], off offset:1280
	global_load_ushort v139, v[2:3], off offset:1408
	global_load_ushort v140, v[4:5], off offset:1536
	global_load_ushort v141, v[4:5], off offset:1664
	global_load_ushort v50, v[4:5], off offset:1792
	global_load_ushort v51, v[4:5], off offset:1920
	s_ashr_i32 s25, s24, 31
	v_mad_i64_i32 v[2:3], s[28:29], s24, v45, v[20:21]
	s_lshl_b64 s[28:29], s[24:25], 11
	global_load_ushort v142, v[2:3], off
	v_mad_i64_i32 v[2:3], s[24:25], s24, v46, v[26:27]
	v_lshl_add_u64 v[8:9], v[28:29], 0, s[28:29]
	global_load_ushort v143, v[2:3], off
	global_load_ushort v144, v[2:3], off offset:128
	global_load_ushort v145, v[2:3], off offset:256
	global_load_ushort v146, v[8:9], off
	global_load_ushort v147, v[8:9], off offset:128
	global_load_ushort v14, v[8:9], off offset:256
	global_load_ushort v15, v[8:9], off offset:384
	global_load_ushort v148, v[2:3], off offset:384
	global_load_ushort v149, v[2:3], off offset:512
	global_load_ushort v150, v[2:3], off offset:640
	global_load_ushort v151, v[8:9], off offset:512
	global_load_ushort v152, v[8:9], off offset:640
	global_load_ushort v6, v[8:9], off offset:768
	global_load_ushort v7, v[8:9], off offset:896
	global_load_ushort v153, v[2:3], off offset:768
	global_load_ushort v154, v[2:3], off offset:896
	global_load_ushort v155, v[2:3], off offset:1024
	global_load_ushort v156, v[8:9], off offset:1024
	global_load_ushort v157, v[8:9], off offset:1152
	global_load_ushort v4, v[8:9], off offset:1280
	global_load_ushort v5, v[8:9], off offset:1408
	global_load_ushort v158, v[2:3], off offset:1152
	global_load_ushort v159, v[2:3], off offset:1280
	global_load_ushort v160, v[2:3], off offset:1408
	global_load_ushort v161, v[8:9], off offset:1536
	global_load_ushort v162, v[8:9], off offset:1664
	s_nop 0
	global_load_ushort v2, v[8:9], off offset:1792
	global_load_ushort v3, v[8:9], off offset:1920
	s_waitcnt vmcnt(28)
	s_ashr_i32 s23, s35, 6
	s_and_b32 s24, s35, 63
	s_lshl_b32 s20, s22, 2
	s_ashr_i32 s36, s35, 31
	s_mulk_i32 s22, 0x2400
	s_nop 0
	s_nop 0
	s_waitcnt vmcnt(27)
	s_waitcnt vmcnt(26)
	s_waitcnt vmcnt(25)
	s_waitcnt vmcnt(24)
	s_waitcnt vmcnt(23)
	s_waitcnt vmcnt(22)
	s_waitcnt vmcnt(21)
	s_waitcnt vmcnt(20)
	s_waitcnt vmcnt(19)
	s_waitcnt vmcnt(18)
	s_waitcnt vmcnt(17)
	s_waitcnt vmcnt(16)
	s_waitcnt vmcnt(15)
	s_waitcnt vmcnt(14)
	s_waitcnt vmcnt(13)
	s_waitcnt vmcnt(12)
	s_waitcnt vmcnt(11)
	s_waitcnt vmcnt(10)
	s_waitcnt vmcnt(9)
	s_waitcnt vmcnt(8)
	s_waitcnt vmcnt(7)
	s_waitcnt vmcnt(6)
	s_waitcnt vmcnt(5)
	s_waitcnt vmcnt(4)
	s_waitcnt vmcnt(3)
	s_waitcnt vmcnt(2)
	s_waitcnt vmcnt(1)
	s_waitcnt vmcnt(0)
	v_lshlrev_b32_e32 v167, 16, v11
	v_lshlrev_b32_e32 v168, 16, v12
	v_lshlrev_b32_e32 v169, 16, v13
	v_lshlrev_b32_e32 v173, 16, v35
	v_lshlrev_b32_e32 v174, 16, v36
	v_lshlrev_b32_e32 v175, 16, v37
	global_load_dword v37, v[22:23], off offset:768
	global_load_dword v36, v[22:23], off offset:1024
	global_load_dword v35, v[22:23], off offset:1280
	global_load_dword v13, v[24:25], off offset:768
	global_load_dword v12, v[24:25], off offset:1024
	global_load_dword v11, v[24:25], off offset:1280
	v_lshlrev_b32_e32 v190, 16, v69
	v_lshlrev_b32_e32 v69, 16, v94
	v_lshlrev_b32_e32 v97, 16, v95
	v_lshlrev_b32_e32 v95, 16, v122
	v_lshlrev_b32_e32 v94, 16, v123
	v_mov_b32_e32 v122, s24
	v_mov_b32_e32 v123, s23
	v_cndmask_b32_e64 v122, v122, v123, s[0:1]
	v_cvt_f32_i32_e32 v122, v122
	v_lshlrev_b32_e32 v102, 16, v90
	v_lshlrev_b32_e32 v101, 16, v93
	v_lshlrev_b32_e32 v93, 16, v126
	v_mul_f32_e32 v122, v1, v122
	v_mul_f32_e32 v122, 0.15915494, v122
	v_lshlrev_b32_e32 v90, 16, v127
	v_cos_f32_e32 v126, v122
	v_sin_f32_e32 v127, v122
	v_mul_f32_e32 v122, v168, v168
	v_fmac_f32_e32 v122, v167, v167
	v_fmac_f32_e32 v122, v169, v169
	v_lshlrev_b32_e32 v103, 16, v89
	v_lshlrev_b32_e32 v89, 16, v128
	v_add_f32_dpp v122, v122, v122 quad_perm:[1,0,3,2] row_mask:0xf bank_mask:0xf bound_ctrl:1
	v_lshlrev_b32_e32 v105, 16, v87
	v_lshlrev_b32_e32 v104, 16, v88
	v_add_f32_dpp v122, v122, v122 quad_perm:[2,3,0,1] row_mask:0xf bank_mask:0xf bound_ctrl:1
	v_lshlrev_b32_e32 v88, 16, v129
	v_lshlrev_b32_e32 v87, 16, v130
	v_add_f32_dpp v122, v122, v122 row_half_mirror row_mask:0xf bank_mask:0xf bound_ctrl:1
	v_lshlrev_b32_e32 v171, 16, v17
	v_lshlrev_b32_e32 v170, 16, v16
	v_add_f32_dpp v122, v122, v122 row_mirror row_mask:0xf bank_mask:0xf bound_ctrl:1
	v_lshlrev_b32_e32 v163, 16, v10
	v_readlane_b32 s24, v122, 16
	v_readlane_b32 s28, v122, 48
	v_readlane_b32 s23, v122, 0
	v_readlane_b32 s25, v122, 32
	v_mov_b32_e32 v122, s24
	v_mov_b32_e32 v123, s28
	v_add_f32_e32 v122, s23, v122
	v_add_f32_e32 v123, s25, v123
	v_add_f32_e32 v122, v122, v123
	v_fmamk_f32 v122, v122, 0x3baaaaab, v44
	v_rsq_f32_e32 v122, v122
	s_mul_hi_i32 s23, s20, 0x900
	s_add_u32 s28, s22, s35
	s_addc_u32 s29, s23, s36
	v_mul_f32_e32 v123, v122, v167
	v_mul_f32_e32 v128, v122, v168
	v_mul_f32_e32 v122, v122, v169
	s_mulk_i32 s29, 0x180
	v_lshlrev_b32_e32 v172, 16, v34
	v_lshlrev_b32_e32 v176, 16, v48
	v_lshlrev_b32_e32 v178, 16, v52
	v_lshlrev_b32_e32 v177, 16, v49
	v_lshlrev_b32_e32 v179, 16, v53
	v_lshlrev_b32_e32 v181, 16, v55
	v_lshlrev_b32_e32 v180, 16, v54
	v_lshlrev_b32_e32 v183, 16, v59
	v_lshlrev_b32_e32 v182, 16, v56
	v_lshlrev_b32_e32 v184, 16, v60
	v_lshlrev_b32_e32 v186, 16, v62
	v_lshlrev_b32_e32 v185, 16, v61
	v_lshlrev_b32_e32 v188, 16, v67
	v_lshlrev_b32_e32 v187, 16, v66
	v_lshlrev_b32_e32 v189, 16, v68
	v_lshlrev_b32_e32 v191, 16, v72
	v_lshlrev_b32_e32 v100, 16, v63
	v_lshlrev_b32_e32 v118, 16, v74
	v_lshlrev_b32_e32 v119, 16, v73
	v_lshlrev_b32_e32 v117, 16, v75
	v_lshlrev_b32_e32 v115, 16, v79
	v_lshlrev_b32_e32 v116, 16, v76
	v_lshlrev_b32_e32 v111, 16, v81
	s_waitcnt vmcnt(5)
	v_mul_f32_e32 v123, v37, v123
	s_waitcnt vmcnt(4)
	v_mul_f32_e32 v128, v36, v128
	s_waitcnt vmcnt(3)
	v_mul_f32_e32 v122, v35, v122
	v_mov_b32_e32 v129, v122
	v_mov_b32_e32 v130, v122
	s_nop 1
	v_permlane32_swap_b32_e32 v129, v130
	v_cndmask_b32_e64 v129, v129, v130, s[4:5]
	v_mul_f32_e32 v129, v127, v129
	v_cndmask_b32_e64 v129, v129, -v129, s[4:5]
	v_fmac_f32_e32 v129, v126, v122
	v_cndmask_b32_e32 v129, v122, v129, vcc
	v_cvt_pk_bf16_f32 v130, v123, v19
	v_mad_u64_u32 v[122:123], s[24:25], s28, v47, v[30:31]
	v_add_u32_e32 v123, s29, v123
	v_cvt_pk_bf16_f32 v128, v128, v19
	global_store_short v[122:123], v130, off
	global_store_short v[122:123], v128, off offset:128
	v_cvt_pk_bf16_f32 v128, v129, v19
	global_store_short v[122:123], v128, off offset:256
	v_mul_f32_e32 v122, v171, v171
	v_fmac_f32_e32 v122, v170, v170
	v_fmac_f32_e32 v122, v163, v163
	v_lshlrev_b32_e32 v112, 16, v80
	v_lshlrev_b32_e32 v110, 16, v82
	v_add_f32_dpp v122, v122, v122 quad_perm:[1,0,3,2] row_mask:0xf bank_mask:0xf bound_ctrl:1
	v_lshlrev_b32_e32 v108, 16, v86
	v_lshlrev_b32_e32 v109, 16, v83
	v_add_f32_dpp v122, v122, v122 quad_perm:[2,3,0,1] row_mask:0xf bank_mask:0xf bound_ctrl:1
	v_lshlrev_b32_e32 v96, 16, v96
	v_lshlrev_b32_e32 v86, 16, v131
	v_add_f32_dpp v122, v122, v122 row_half_mirror row_mask:0xf bank_mask:0xf bound_ctrl:1
	v_lshlrev_b32_e32 v82, 16, v133
	v_lshlrev_b32_e32 v83, 16, v132
	v_add_f32_dpp v122, v122, v122 row_mirror row_mask:0xf bank_mask:0xf bound_ctrl:1
	v_lshlrev_b32_e32 v81, 16, v134
	v_readlane_b32 s25, v122, 16
	v_readlane_b32 s31, v122, 48
	v_readlane_b32 s24, v122, 0
	v_readlane_b32 s30, v122, 32
	v_mov_b32_e32 v122, s25
	v_mov_b32_e32 v123, s31
	v_add_f32_e32 v122, s24, v122
	v_add_f32_e32 v123, s30, v123
	v_add_f32_e32 v122, v122, v123
	v_fmamk_f32 v122, v122, 0x3baaaaab, v44
	v_rsq_f32_e32 v122, v122
	v_lshlrev_b32_e32 v79, 16, v136
	v_lshlrev_b32_e32 v80, 16, v135
	v_lshlrev_b32_e32 v75, 16, v138
	v_mul_f32_e32 v123, v122, v170
	v_mul_f32_e32 v128, v122, v171
	v_mul_f32_e32 v122, v122, v163
	s_waitcnt vmcnt(3)
	v_mul_f32_e32 v122, v11, v122
	v_mov_b32_e32 v129, v122
	v_mov_b32_e32 v130, v122
	s_nop 1
	v_permlane32_swap_b32_e32 v129, v130
	v_cndmask_b32_e64 v129, v129, v130, s[4:5]
	v_mul_f32_e32 v129, v127, v129
	v_cndmask_b32_e64 v129, v129, -v129, s[4:5]
	v_mul_f32_e32 v123, v13, v123
	v_fmac_f32_e32 v129, v126, v122
	v_mul_f32_e32 v128, v12, v128
	v_cndmask_b32_e32 v129, v122, v129, vcc
	v_cvt_pk_bf16_f32 v130, v123, v19
	v_mad_u64_u32 v[122:123], s[24:25], s28, v47, v[32:33]
	v_add_u32_e32 v123, s29, v123
	v_cvt_pk_bf16_f32 v128, v128, v19
	global_store_short v[122:123], v130, off
	global_store_short v[122:123], v128, off offset:128
	v_cvt_pk_bf16_f32 v128, v129, v19
	global_store_short v[122:123], v128, off offset:256
	v_mul_f32_e32 v122, v173, v173
	v_fmac_f32_e32 v122, v172, v172
	v_fmac_f32_e32 v122, v174, v174
	ds_write_b16 v38, v124
	ds_write_b16 v38, v125 offset:128
	v_add_f32_dpp v122, v122, v122 quad_perm:[1,0,3,2] row_mask:0xf bank_mask:0xf bound_ctrl:1
	v_lshlrev_b32_e32 v76, 16, v137
	v_lshlrev_b32_e32 v74, 16, v139
	v_add_f32_dpp v122, v122, v122 quad_perm:[2,3,0,1] row_mask:0xf bank_mask:0xf bound_ctrl:1
	v_lshlrev_b32_e32 v72, 16, v141
	v_lshlrev_b32_e32 v73, 16, v140
	v_add_f32_dpp v122, v122, v122 row_half_mirror row_mask:0xf bank_mask:0xf bound_ctrl:1
	v_lshlrev_b32_e32 v67, 16, v144
	v_lshlrev_b32_e32 v68, 16, v143
	v_add_f32_dpp v122, v122, v122 row_mirror row_mask:0xf bank_mask:0xf bound_ctrl:1
	v_lshlrev_b32_e32 v66, 16, v145
	v_readlane_b32 s25, v122, 16
	v_readlane_b32 s29, v122, 48
	v_readlane_b32 s24, v122, 0
	v_readlane_b32 s28, v122, 32
	v_mov_b32_e32 v122, s25
	v_mov_b32_e32 v123, s29
	v_add_f32_e32 v122, s24, v122
	v_add_f32_e32 v123, s28, v123
	v_add_f32_e32 v122, v122, v123
	v_fmamk_f32 v122, v122, 0x3baaaaab, v44
	v_rsq_f32_e32 v122, v122
	s_or_b32 s25, s20, 1
	s_mul_hi_i32 s24, s25, 0x900
	s_mulk_i32 s25, 0x900
	v_mul_f32_e32 v123, v122, v172
	v_mul_f32_e32 v124, v122, v173
	v_mul_f32_e32 v122, v122, v174
	v_mul_f32_e32 v122, v35, v122
	v_mov_b32_e32 v125, v122
	v_mov_b32_e32 v128, v122
	s_nop 1
	v_permlane32_swap_b32_e32 v125, v128
	v_cndmask_b32_e64 v125, v125, v128, s[4:5]
	v_mul_f32_e32 v125, v127, v125
	v_cndmask_b32_e64 v125, v125, -v125, s[4:5]
	s_add_u32 s30, s25, s35
	v_mul_f32_e32 v123, v37, v123
	v_fmac_f32_e32 v125, v126, v122
	s_addc_u32 s31, s24, s36
	v_mul_f32_e32 v124, v36, v124
	v_cndmask_b32_e32 v125, v122, v125, vcc
	v_cvt_pk_bf16_f32 v128, v123, v19
	v_mad_u64_u32 v[122:123], s[28:29], s30, v47, v[30:31]
	s_mulk_i32 s31, 0x180
	v_add_u32_e32 v123, s31, v123
	v_cvt_pk_bf16_f32 v124, v124, v19
	global_store_short v[122:123], v128, off
	global_store_short v[122:123], v124, off offset:128
	v_cvt_pk_bf16_f32 v124, v125, v19
	global_store_short v[122:123], v124, off offset:256
	v_mul_f32_e32 v122, v176, v176
	v_fmac_f32_e32 v122, v175, v175
	v_fmac_f32_e32 v122, v163, v163
	v_lshlrev_b32_e32 v62, 16, v147
	v_lshlrev_b32_e32 v63, 16, v146
	v_add_f32_dpp v122, v122, v122 quad_perm:[1,0,3,2] row_mask:0xf bank_mask:0xf bound_ctrl:1
	v_lshlrev_b32_e32 v8, 16, v142
	v_lshlrev_b32_e32 v60, 16, v149
	v_add_f32_dpp v122, v122, v122 quad_perm:[2,3,0,1] row_mask:0xf bank_mask:0xf bound_ctrl:1
	v_lshlrev_b32_e32 v61, 16, v148
	v_lshlrev_b32_e32 v59, 16, v150
	v_add_f32_dpp v122, v122, v122 row_half_mirror row_mask:0xf bank_mask:0xf bound_ctrl:1
	v_lshlrev_b32_e32 v55, 16, v152
	v_lshlrev_b32_e32 v56, 16, v151
	v_add_f32_dpp v122, v122, v122 row_mirror row_mask:0xf bank_mask:0xf bound_ctrl:1
	v_lshlrev_b32_e32 v53, 16, v154
	v_readlane_b32 s29, v122, 16
	v_readlane_b32 s38, v122, 48
	v_readlane_b32 s28, v122, 0
	v_readlane_b32 s37, v122, 32
	v_mov_b32_e32 v122, s29
	v_mov_b32_e32 v123, s38
	v_add_f32_e32 v122, s28, v122
	v_add_f32_e32 v123, s37, v123
	v_add_f32_e32 v122, v122, v123
	v_fmamk_f32 v122, v122, 0x3baaaaab, v44
	v_rsq_f32_e32 v122, v122
	v_lshlrev_b32_e32 v54, 16, v153
	v_lshlrev_b32_e32 v52, 16, v155
	v_lshlrev_b32_e32 v48, 16, v157
	v_mul_f32_e32 v123, v122, v175
	v_mul_f32_e32 v124, v122, v176
	v_mul_f32_e32 v122, v122, v163
	v_mul_f32_e32 v122, v11, v122
	v_mov_b32_e32 v125, v122
	v_mov_b32_e32 v128, v122
	s_nop 1
	v_permlane32_swap_b32_e32 v125, v128
	v_cndmask_b32_e64 v125, v125, v128, s[4:5]
	v_mul_f32_e32 v125, v127, v125
	v_cndmask_b32_e64 v125, v125, -v125, s[4:5]
	v_mul_f32_e32 v123, v13, v123
	v_fmac_f32_e32 v125, v126, v122
	v_mul_f32_e32 v124, v12, v124
	v_cndmask_b32_e32 v125, v122, v125, vcc
	v_cvt_pk_bf16_f32 v128, v123, v19
	v_mad_u64_u32 v[122:123], s[28:29], s30, v47, v[32:33]
	v_add_u32_e32 v123, s31, v123
	v_cvt_pk_bf16_f32 v124, v124, v19
	global_store_short v[122:123], v128, off
	global_store_short v[122:123], v124, off offset:128
	v_cvt_pk_bf16_f32 v124, v125, v19
	global_store_short v[122:123], v124, off offset:256
	ds_write_b16 v38, v120 offset:256
	ds_write_b16 v38, v121 offset:384
	v_mul_f32_e32 v120, v178, v178
	v_fmac_f32_e32 v120, v177, v177
	v_fmac_f32_e32 v120, v179, v179
	v_lshlrev_b32_e32 v49, 16, v156
	v_lshlrev_b32_e32 v17, 16, v159
	v_add_f32_dpp v120, v120, v120 quad_perm:[1,0,3,2] row_mask:0xf bank_mask:0xf bound_ctrl:1
	v_lshlrev_b32_e32 v34, 16, v158
	v_lshlrev_b32_e32 v16, 16, v160
	v_add_f32_dpp v120, v120, v120 quad_perm:[2,3,0,1] row_mask:0xf bank_mask:0xf bound_ctrl:1
	v_lshlrev_b32_e32 v9, 16, v162
	v_lshlrev_b32_e32 v10, 16, v161
	v_add_f32_dpp v120, v120, v120 row_half_mirror row_mask:0xf bank_mask:0xf bound_ctrl:1
	s_nop 1
	v_add_f32_dpp v120, v120, v120 row_mirror row_mask:0xf bank_mask:0xf bound_ctrl:1
	s_nop 0
	v_readlane_b32 s29, v120, 16
	v_readlane_b32 s31, v120, 48
	v_readlane_b32 s28, v120, 0
	v_readlane_b32 s30, v120, 32
	v_mov_b32_e32 v120, s29
	v_mov_b32_e32 v121, s31
	v_add_f32_e32 v120, s28, v120
	v_add_f32_e32 v121, s30, v121
	v_add_f32_e32 v120, v120, v121
	v_fmamk_f32 v120, v120, 0x3baaaaab, v44
	v_rsq_f32_e32 v120, v120
	s_or_b32 s29, s20, 2
	s_mul_hi_i32 s28, s29, 0x900
	s_mulk_i32 s29, 0x900
	v_mul_f32_e32 v121, v120, v177
	v_mul_f32_e32 v122, v120, v178
	v_mul_f32_e32 v120, v120, v179
	v_mul_f32_e32 v120, v35, v120
	v_mov_b32_e32 v123, v120
	v_mov_b32_e32 v124, v120
	s_nop 1
	v_permlane32_swap_b32_e32 v123, v124
	v_cndmask_b32_e64 v123, v123, v124, s[4:5]
	v_mul_f32_e32 v123, v127, v123
	v_cndmask_b32_e64 v123, v123, -v123, s[4:5]
	s_add_u32 s37, s29, s35
	v_mul_f32_e32 v121, v37, v121
	v_fmac_f32_e32 v123, v126, v120
	s_addc_u32 s38, s28, s36
	v_mul_f32_e32 v122, v36, v122
	v_cndmask_b32_e32 v123, v120, v123, vcc
	v_cvt_pk_bf16_f32 v124, v121, v19
	v_mad_u64_u32 v[120:121], s[30:31], s37, v47, v[30:31]
	s_mulk_i32 s38, 0x180
	v_add_u32_e32 v121, s38, v121
	v_cvt_pk_bf16_f32 v122, v122, v19
	global_store_short v[120:121], v124, off
	global_store_short v[120:121], v122, off offset:128
	v_cvt_pk_bf16_f32 v122, v123, v19
	global_store_short v[120:121], v122, off offset:256
	v_mul_f32_e32 v120, v181, v181
	v_fmac_f32_e32 v120, v180, v180
	v_fmac_f32_e32 v120, v163, v163
	s_nop 1
	v_add_f32_dpp v120, v120, v120 quad_perm:[1,0,3,2] row_mask:0xf bank_mask:0xf bound_ctrl:1
	s_nop 1
	v_add_f32_dpp v120, v120, v120 quad_perm:[2,3,0,1] row_mask:0xf bank_mask:0xf bound_ctrl:1
	s_nop 1
	v_add_f32_dpp v120, v120, v120 row_half_mirror row_mask:0xf bank_mask:0xf bound_ctrl:1
	s_nop 1
	v_add_f32_dpp v120, v120, v120 row_mirror row_mask:0xf bank_mask:0xf bound_ctrl:1
	s_nop 0
	v_readlane_b32 s31, v120, 16
	v_readlane_b32 s40, v120, 48
	v_readlane_b32 s30, v120, 0
	v_readlane_b32 s39, v120, 32
	v_mov_b32_e32 v120, s31
	v_mov_b32_e32 v121, s40
	v_add_f32_e32 v120, s30, v120
	v_add_f32_e32 v121, s39, v121
	v_add_f32_e32 v120, v120, v121
	v_fmamk_f32 v120, v120, 0x3baaaaab, v44
	v_rsq_f32_e32 v120, v120
	s_nop 0
	v_mul_f32_e32 v121, v120, v180
	v_mul_f32_e32 v122, v120, v181
	v_mul_f32_e32 v120, v120, v163
	v_mul_f32_e32 v120, v11, v120
	v_mov_b32_e32 v123, v120
	v_mov_b32_e32 v124, v120
	s_nop 1
	v_permlane32_swap_b32_e32 v123, v124
	v_cndmask_b32_e64 v123, v123, v124, s[4:5]
	v_mul_f32_e32 v123, v127, v123
	v_cndmask_b32_e64 v123, v123, -v123, s[4:5]
	v_mul_f32_e32 v121, v13, v121
	v_fmac_f32_e32 v123, v126, v120
	v_mul_f32_e32 v122, v12, v122
	v_cndmask_b32_e32 v123, v120, v123, vcc
	v_cvt_pk_bf16_f32 v124, v121, v19
	v_mad_u64_u32 v[120:121], s[30:31], s37, v47, v[32:33]
	v_add_u32_e32 v121, s38, v121
	v_cvt_pk_bf16_f32 v122, v122, v19
	global_store_short v[120:121], v124, off
	global_store_short v[120:121], v122, off offset:128
	v_cvt_pk_bf16_f32 v122, v123, v19
	global_store_short v[120:121], v122, off offset:256
	ds_write_b16 v38, v113 offset:512
	ds_write_b16 v38, v114 offset:640
	v_mul_f32_e32 v113, v183, v183
	v_fmac_f32_e32 v113, v182, v182
	v_fmac_f32_e32 v113, v184, v184
	s_nop 1
	v_add_f32_dpp v113, v113, v113 quad_perm:[1,0,3,2] row_mask:0xf bank_mask:0xf bound_ctrl:1
	s_nop 1
	v_add_f32_dpp v113, v113, v113 quad_perm:[2,3,0,1] row_mask:0xf bank_mask:0xf bound_ctrl:1
	s_nop 1
	v_add_f32_dpp v113, v113, v113 row_half_mirror row_mask:0xf bank_mask:0xf bound_ctrl:1
	s_nop 1
	v_add_f32_dpp v113, v113, v113 row_mirror row_mask:0xf bank_mask:0xf bound_ctrl:1
	s_nop 0
	v_readlane_b32 s31, v113, 16
	v_readlane_b32 s38, v113, 48
	v_readlane_b32 s30, v113, 0
	v_readlane_b32 s37, v113, 32
	v_mov_b32_e32 v113, s31
	v_mov_b32_e32 v114, s38
	v_add_f32_e32 v113, s30, v113
	v_add_f32_e32 v114, s37, v114
	v_add_f32_e32 v113, v113, v114
	v_fmamk_f32 v113, v113, 0x3baaaaab, v44
	v_rsq_f32_e32 v113, v113
	s_or_b32 s31, s20, 3
	s_mul_hi_i32 s30, s31, 0x900
	s_mulk_i32 s31, 0x900
	v_mul_f32_e32 v114, v113, v182
	v_mul_f32_e32 v120, v113, v183
	v_mul_f32_e32 v113, v113, v184
	v_mul_f32_e32 v113, v35, v113
	v_mul_f32_e32 v122, v36, v120
	v_mov_b32_e32 v120, v113
	v_mov_b32_e32 v121, v113
	s_nop 1
	v_permlane32_swap_b32_e32 v120, v121
	v_cndmask_b32_e64 v120, v120, v121, s[4:5]
	v_mul_f32_e32 v120, v127, v120
	v_cndmask_b32_e64 v120, v120, -v120, s[4:5]
	s_add_u32 s35, s31, s35
	v_fmac_f32_e32 v120, v126, v113
	s_addc_u32 s38, s30, s36
	v_cndmask_b32_e32 v113, v113, v120, vcc
	v_mad_u64_u32 v[120:121], s[36:37], s35, v47, v[30:31]
	s_mulk_i32 s38, 0x180
	v_add_u32_e32 v121, s38, v121
	v_cvt_pk_bf16_f32 v113, v113, v19
	global_store_short v[120:121], v113, off offset:256
	v_mul_f32_e32 v113, v186, v186
	v_fmac_f32_e32 v113, v185, v185
	v_fmac_f32_e32 v113, v163, v163
	v_mul_f32_e32 v114, v37, v114
	v_cvt_pk_bf16_f32 v114, v114, v19
	global_store_short v[120:121], v114, off
	v_add_f32_dpp v113, v113, v113 quad_perm:[1,0,3,2] row_mask:0xf bank_mask:0xf bound_ctrl:1
	v_cvt_pk_bf16_f32 v114, v122, v19
	global_store_short v[120:121], v114, off offset:128
	s_cmpk_lt_i32 s34, 0x800
	v_add_f32_dpp v113, v113, v113 quad_perm:[2,3,0,1] row_mask:0xf bank_mask:0xf bound_ctrl:1
	s_nop 1
	v_add_f32_dpp v113, v113, v113 row_half_mirror row_mask:0xf bank_mask:0xf bound_ctrl:1
	s_nop 1
	v_add_f32_dpp v113, v113, v113 row_mirror row_mask:0xf bank_mask:0xf bound_ctrl:1
	s_nop 0
	v_readlane_b32 s37, v113, 16
	v_readlane_b32 s40, v113, 48
	v_readlane_b32 s36, v113, 0
	v_readlane_b32 s39, v113, 32
	v_mov_b32_e32 v113, s37
	v_mov_b32_e32 v114, s40
	v_add_f32_e32 v113, s36, v113
	v_add_f32_e32 v114, s39, v114
	v_add_f32_e32 v113, v113, v114
	v_fmamk_f32 v113, v113, 0x3baaaaab, v44
	v_rsq_f32_e32 v113, v113
	s_nop 0
	v_mul_f32_e32 v114, v113, v185
	v_mul_f32_e32 v120, v113, v186
	v_mul_f32_e32 v113, v113, v163
	v_mul_f32_e32 v113, v11, v113
	v_mul_f32_e32 v122, v12, v120
	v_mov_b32_e32 v120, v113
	v_mov_b32_e32 v121, v113
	s_nop 1
	v_permlane32_swap_b32_e32 v120, v121
	v_cndmask_b32_e64 v120, v120, v121, s[4:5]
	v_mul_f32_e32 v120, v127, v120
	v_cndmask_b32_e64 v120, v120, -v120, s[4:5]
	v_fmac_f32_e32 v120, v126, v113
	v_mul_f32_e32 v114, v13, v114
	v_cndmask_b32_e32 v113, v113, v120, vcc
	v_mad_u64_u32 v[120:121], s[36:37], s35, v47, v[32:33]
	v_cvt_pk_bf16_f32 v114, v114, v19
	v_add_u32_e32 v121, s38, v121
	s_cselect_b64 vcc, -1, 0
	s_ashr_i32 s35, s34, 6
	s_and_b32 s36, s34, 63
	global_store_short v[120:121], v114, off
	v_cvt_pk_bf16_f32 v114, v122, v19
	global_store_short v[120:121], v114, off offset:128
	v_cvt_pk_bf16_f32 v113, v113, v19
	global_store_short v[120:121], v113, off offset:256
	ds_write_b16 v38, v106 offset:768
	ds_write_b16 v38, v107 offset:896
	v_mov_b32_e32 v106, s36
	v_mov_b32_e32 v107, s35
	v_cndmask_b32_e64 v106, v106, v107, s[0:1]
	v_cvt_f32_i32_e32 v106, v106
	s_ashr_i32 s35, s34, 31
	v_mul_f32_e32 v106, v1, v106
	v_mul_f32_e32 v106, 0.15915494, v106
	v_cos_f32_e32 v113, v106
	v_sin_f32_e32 v114, v106
	v_mul_f32_e32 v106, v188, v188
	v_fmac_f32_e32 v106, v187, v187
	v_fmac_f32_e32 v106, v189, v189
	s_nop 1
	v_add_f32_dpp v106, v106, v106 quad_perm:[1,0,3,2] row_mask:0xf bank_mask:0xf bound_ctrl:1
	s_nop 1
	v_add_f32_dpp v106, v106, v106 quad_perm:[2,3,0,1] row_mask:0xf bank_mask:0xf bound_ctrl:1
	s_nop 1
	v_add_f32_dpp v106, v106, v106 row_half_mirror row_mask:0xf bank_mask:0xf bound_ctrl:1
	s_nop 1
	v_add_f32_dpp v106, v106, v106 row_mirror row_mask:0xf bank_mask:0xf bound_ctrl:1
	s_nop 0
	v_readlane_b32 s37, v106, 16
	v_readlane_b32 s39, v106, 48
	v_readlane_b32 s36, v106, 0
	v_readlane_b32 s38, v106, 32
	v_mov_b32_e32 v106, s37
	v_mov_b32_e32 v107, s39
	v_add_f32_e32 v106, s36, v106
	v_add_f32_e32 v107, s38, v107
	v_add_f32_e32 v106, v106, v107
	v_fmamk_f32 v106, v106, 0x3baaaaab, v44
	v_rsq_f32_e32 v106, v106
	s_add_u32 s38, s22, s34
	s_addc_u32 s39, s23, s35
	s_mulk_i32 s39, 0x180
	v_mul_f32_e32 v107, v106, v187
	v_mul_f32_e32 v120, v106, v188
	v_mul_f32_e32 v106, v106, v189
	v_mul_f32_e32 v106, v35, v106
	v_mov_b32_e32 v121, v106
	v_mov_b32_e32 v122, v106
	s_nop 1
	v_permlane32_swap_b32_e32 v121, v122
	v_cndmask_b32_e64 v121, v121, v122, s[4:5]
	v_mul_f32_e32 v121, v114, v121
	v_cndmask_b32_e64 v121, v121, -v121, s[4:5]
	v_mul_f32_e32 v107, v37, v107
	v_fmac_f32_e32 v121, v113, v106
	v_mul_f32_e32 v120, v36, v120
	v_cndmask_b32_e32 v121, v106, v121, vcc
	v_cvt_pk_bf16_f32 v122, v107, v19
	v_mad_u64_u32 v[106:107], s[36:37], s38, v47, v[30:31]
	v_add_u32_e32 v107, s39, v107
	v_cvt_pk_bf16_f32 v120, v120, v19
	global_store_short v[106:107], v122, off
	global_store_short v[106:107], v120, off offset:128
	v_cvt_pk_bf16_f32 v120, v121, v19
	global_store_short v[106:107], v120, off offset:256
	v_mul_f32_e32 v106, v191, v191
	v_fmac_f32_e32 v106, v190, v190
	v_fmac_f32_e32 v106, v100, v100
	s_nop 1
	v_add_f32_dpp v106, v106, v106 quad_perm:[1,0,3,2] row_mask:0xf bank_mask:0xf bound_ctrl:1
	s_nop 1
	v_add_f32_dpp v106, v106, v106 quad_perm:[2,3,0,1] row_mask:0xf bank_mask:0xf bound_ctrl:1
	s_nop 1
	v_add_f32_dpp v106, v106, v106 row_half_mirror row_mask:0xf bank_mask:0xf bound_ctrl:1
	s_nop 1
	v_add_f32_dpp v106, v106, v106 row_mirror row_mask:0xf bank_mask:0xf bound_ctrl:1
	s_nop 0
	v_readlane_b32 s37, v106, 16
	v_readlane_b32 s41, v106, 48
	v_readlane_b32 s36, v106, 0
	v_readlane_b32 s40, v106, 32
	v_mov_b32_e32 v106, s37
	v_mov_b32_e32 v107, s41
	v_add_f32_e32 v106, s36, v106
	v_add_f32_e32 v107, s40, v107
	v_add_f32_e32 v106, v106, v107
	v_fmamk_f32 v106, v106, 0x3baaaaab, v44
	v_rsq_f32_e32 v106, v106
	s_nop 0
	v_mul_f32_e32 v107, v106, v190
	v_mul_f32_e32 v120, v106, v191
	v_mul_f32_e32 v106, v106, v100
	v_mul_f32_e32 v106, v11, v106
	v_mov_b32_e32 v121, v106
	v_mov_b32_e32 v122, v106
	s_nop 1
	v_permlane32_swap_b32_e32 v121, v122
	v_cndmask_b32_e64 v121, v121, v122, s[4:5]
	v_mul_f32_e32 v121, v114, v121
	v_cndmask_b32_e64 v121, v121, -v121, s[4:5]
	v_mul_f32_e32 v107, v13, v107
	v_fmac_f32_e32 v121, v113, v106
	v_mul_f32_e32 v120, v12, v120
	v_cndmask_b32_e32 v121, v106, v121, vcc
	v_cvt_pk_bf16_f32 v122, v107, v19
	v_mad_u64_u32 v[106:107], s[36:37], s38, v47, v[32:33]
	v_add_u32_e32 v107, s39, v107
	v_cvt_pk_bf16_f32 v120, v120, v19
	global_store_short v[106:107], v122, off
	global_store_short v[106:107], v120, off offset:128
	v_cvt_pk_bf16_f32 v120, v121, v19
	global_store_short v[106:107], v120, off offset:256
	ds_write_b16 v39, v98
	ds_write_b16 v39, v99 offset:128
	v_mul_f32_e32 v98, v118, v118
	v_fmac_f32_e32 v98, v119, v119
	v_fmac_f32_e32 v98, v117, v117
	s_nop 1
	v_add_f32_dpp v98, v98, v98 quad_perm:[1,0,3,2] row_mask:0xf bank_mask:0xf bound_ctrl:1
	s_nop 1
	v_add_f32_dpp v98, v98, v98 quad_perm:[2,3,0,1] row_mask:0xf bank_mask:0xf bound_ctrl:1
	s_nop 1
	v_add_f32_dpp v98, v98, v98 row_half_mirror row_mask:0xf bank_mask:0xf bound_ctrl:1
	s_nop 1
	v_add_f32_dpp v98, v98, v98 row_mirror row_mask:0xf bank_mask:0xf bound_ctrl:1
	s_nop 0
	v_readlane_b32 s37, v98, 16
	v_readlane_b32 s39, v98, 48
	v_readlane_b32 s36, v98, 0
	v_readlane_b32 s38, v98, 32
	v_mov_b32_e32 v98, s37
	v_mov_b32_e32 v99, s39
	v_add_f32_e32 v98, s36, v98
	v_add_f32_e32 v99, s38, v99
	v_add_f32_e32 v98, v98, v99
	v_fmamk_f32 v98, v98, 0x3baaaaab, v44
	v_rsq_f32_e32 v98, v98
	s_add_u32 s38, s25, s34
	s_addc_u32 s39, s24, s35
	s_mulk_i32 s39, 0x180
	v_mul_f32_e32 v99, v98, v119
	v_mul_f32_e32 v106, v98, v118
	v_mul_f32_e32 v98, v98, v117
	v_mul_f32_e32 v98, v35, v98
	v_mov_b32_e32 v107, v98
	v_mov_b32_e32 v117, v98
	s_nop 1
	v_permlane32_swap_b32_e32 v107, v117
	v_cndmask_b32_e64 v107, v107, v117, s[4:5]
	v_mul_f32_e32 v107, v114, v107
	v_cndmask_b32_e64 v107, v107, -v107, s[4:5]
	v_mul_f32_e32 v99, v37, v99
	v_fmac_f32_e32 v107, v113, v98
	v_mul_f32_e32 v106, v36, v106
	v_cndmask_b32_e32 v107, v98, v107, vcc
	v_cvt_pk_bf16_f32 v117, v99, v19
	v_mad_u64_u32 v[98:99], s[36:37], s38, v47, v[30:31]
	v_add_u32_e32 v99, s39, v99
	v_cvt_pk_bf16_f32 v106, v106, v19
	global_store_short v[98:99], v117, off
	global_store_short v[98:99], v106, off offset:128
	v_cvt_pk_bf16_f32 v106, v107, v19
	global_store_short v[98:99], v106, off offset:256
	v_mul_f32_e32 v98, v115, v115
	v_fmac_f32_e32 v98, v116, v116
	v_fmac_f32_e32 v98, v100, v100
	s_nop 1
	v_add_f32_dpp v98, v98, v98 quad_perm:[1,0,3,2] row_mask:0xf bank_mask:0xf bound_ctrl:1
	s_nop 1
	v_add_f32_dpp v98, v98, v98 quad_perm:[2,3,0,1] row_mask:0xf bank_mask:0xf bound_ctrl:1
	s_nop 1
	v_add_f32_dpp v98, v98, v98 row_half_mirror row_mask:0xf bank_mask:0xf bound_ctrl:1
	s_nop 1
	v_add_f32_dpp v98, v98, v98 row_mirror row_mask:0xf bank_mask:0xf bound_ctrl:1
	s_nop 0
	v_readlane_b32 s37, v98, 16
	v_readlane_b32 s41, v98, 48
	v_readlane_b32 s36, v98, 0
	v_readlane_b32 s40, v98, 32
	v_mov_b32_e32 v98, s37
	v_mov_b32_e32 v99, s41
	v_add_f32_e32 v98, s36, v98
	v_add_f32_e32 v99, s40, v99
	v_add_f32_e32 v98, v98, v99
	v_fmamk_f32 v98, v98, 0x3baaaaab, v44
	v_rsq_f32_e32 v98, v98
	s_nop 0
	v_mul_f32_e32 v99, v98, v116
	v_mul_f32_e32 v106, v98, v115
	v_mul_f32_e32 v98, v98, v100
	v_mul_f32_e32 v98, v11, v98
	v_mov_b32_e32 v107, v98
	v_mov_b32_e32 v115, v98
	s_nop 1
	v_permlane32_swap_b32_e32 v107, v115
	v_cndmask_b32_e64 v107, v107, v115, s[4:5]
	v_mul_f32_e32 v107, v114, v107
	v_cndmask_b32_e64 v107, v107, -v107, s[4:5]
	v_mul_f32_e32 v99, v13, v99
	v_fmac_f32_e32 v107, v113, v98
	v_mul_f32_e32 v106, v12, v106
	v_cndmask_b32_e32 v107, v98, v107, vcc
	v_cvt_pk_bf16_f32 v115, v99, v19
	v_mad_u64_u32 v[98:99], s[36:37], s38, v47, v[32:33]
	v_add_u32_e32 v99, s39, v99
	v_cvt_pk_bf16_f32 v106, v106, v19
	global_store_short v[98:99], v115, off
	global_store_short v[98:99], v106, off offset:128
	v_cvt_pk_bf16_f32 v106, v107, v19
	global_store_short v[98:99], v106, off offset:256
	ds_write_b16 v39, v91 offset:256
	ds_write_b16 v39, v92 offset:384
	v_mul_f32_e32 v91, v111, v111
	v_fmac_f32_e32 v91, v112, v112
	v_fmac_f32_e32 v91, v110, v110
	s_nop 1
	v_add_f32_dpp v91, v91, v91 quad_perm:[1,0,3,2] row_mask:0xf bank_mask:0xf bound_ctrl:1
	s_nop 1
	v_add_f32_dpp v91, v91, v91 quad_perm:[2,3,0,1] row_mask:0xf bank_mask:0xf bound_ctrl:1
	s_nop 1
	v_add_f32_dpp v91, v91, v91 row_half_mirror row_mask:0xf bank_mask:0xf bound_ctrl:1
	s_nop 1
	v_add_f32_dpp v91, v91, v91 row_mirror row_mask:0xf bank_mask:0xf bound_ctrl:1
	s_nop 0
	v_readlane_b32 s37, v91, 16
	v_readlane_b32 s39, v91, 48
	v_readlane_b32 s36, v91, 0
	v_readlane_b32 s38, v91, 32
	v_mov_b32_e32 v91, s37
	v_mov_b32_e32 v92, s39
	v_add_f32_e32 v91, s36, v91
	v_add_f32_e32 v92, s38, v92
	v_add_f32_e32 v91, v91, v92
	v_fmamk_f32 v91, v91, 0x3baaaaab, v44
	v_rsq_f32_e32 v91, v91
	s_add_u32 s38, s29, s34
	s_addc_u32 s39, s28, s35
	s_mulk_i32 s39, 0x180
	v_mul_f32_e32 v92, v91, v112
	v_mul_f32_e32 v98, v91, v111
	v_mul_f32_e32 v91, v91, v110
	v_mul_f32_e32 v91, v35, v91
	v_mul_f32_e32 v106, v36, v98
	v_mov_b32_e32 v98, v91
	v_mov_b32_e32 v99, v91
	s_nop 1
	v_permlane32_swap_b32_e32 v98, v99
	v_cndmask_b32_e64 v98, v98, v99, s[4:5]
	v_mul_f32_e32 v98, v114, v98
	v_cndmask_b32_e64 v98, v98, -v98, s[4:5]
	v_fmac_f32_e32 v98, v113, v91
	v_cndmask_b32_e32 v91, v91, v98, vcc
	v_mad_u64_u32 v[98:99], s[36:37], s38, v47, v[30:31]
	v_add_u32_e32 v99, s39, v99
	v_cvt_pk_bf16_f32 v91, v91, v19
	global_store_short v[98:99], v91, off offset:256
	v_mul_f32_e32 v91, v108, v108
	v_fmac_f32_e32 v91, v109, v109
	v_fmac_f32_e32 v91, v100, v100
	v_mul_f32_e32 v92, v37, v92
	v_cvt_pk_bf16_f32 v92, v92, v19
	global_store_short v[98:99], v92, off
	v_add_f32_dpp v91, v91, v91 quad_perm:[1,0,3,2] row_mask:0xf bank_mask:0xf bound_ctrl:1
	v_cvt_pk_bf16_f32 v92, v106, v19
	global_store_short v[98:99], v92, off offset:128
	s_nop 0
	v_add_f32_dpp v91, v91, v91 quad_perm:[2,3,0,1] row_mask:0xf bank_mask:0xf bound_ctrl:1
	s_nop 1
	v_add_f32_dpp v91, v91, v91 row_half_mirror row_mask:0xf bank_mask:0xf bound_ctrl:1
	s_nop 1
	v_add_f32_dpp v91, v91, v91 row_mirror row_mask:0xf bank_mask:0xf bound_ctrl:1
	s_nop 0
	v_readlane_b32 s37, v91, 16
	v_readlane_b32 s41, v91, 48
	v_readlane_b32 s36, v91, 0
	v_readlane_b32 s40, v91, 32
	v_mov_b32_e32 v91, s37
	v_mov_b32_e32 v92, s41
	v_add_f32_e32 v91, s36, v91
	v_add_f32_e32 v92, s40, v92
	v_add_f32_e32 v91, v91, v92
	v_fmamk_f32 v91, v91, 0x3baaaaab, v44
	v_rsq_f32_e32 v91, v91
	s_nop 0
	v_mul_f32_e32 v92, v91, v109
	v_mul_f32_e32 v98, v91, v108
	v_mul_f32_e32 v91, v91, v100
	v_mul_f32_e32 v91, v11, v91
	v_mul_f32_e32 v106, v12, v98
	v_mov_b32_e32 v98, v91
	v_mov_b32_e32 v99, v91
	s_nop 1
	v_permlane32_swap_b32_e32 v98, v99
	v_cndmask_b32_e64 v98, v98, v99, s[4:5]
	v_mul_f32_e32 v98, v114, v98
	v_cndmask_b32_e64 v98, v98, -v98, s[4:5]
	v_fmac_f32_e32 v98, v113, v91
	v_mul_f32_e32 v92, v13, v92
	v_cndmask_b32_e32 v91, v91, v98, vcc
	v_mad_u64_u32 v[98:99], s[36:37], s38, v47, v[32:33]
	v_cvt_pk_bf16_f32 v92, v92, v19
	v_add_u32_e32 v99, s39, v99
	global_store_short v[98:99], v92, off
	v_cvt_pk_bf16_f32 v92, v106, v19
	global_store_short v[98:99], v92, off offset:128
	v_cvt_pk_bf16_f32 v91, v91, v19
	global_store_short v[98:99], v91, off offset:256
	ds_write_b16 v39, v84 offset:512
	ds_write_b16 v39, v85 offset:640
	v_mul_f32_e32 v84, v104, v104
	v_fmac_f32_e32 v84, v105, v105
	v_fmac_f32_e32 v84, v103, v103
	s_nop 1
	v_add_f32_dpp v84, v84, v84 quad_perm:[1,0,3,2] row_mask:0xf bank_mask:0xf bound_ctrl:1
	s_nop 1
	v_add_f32_dpp v84, v84, v84 quad_perm:[2,3,0,1] row_mask:0xf bank_mask:0xf bound_ctrl:1
	s_nop 1
	v_add_f32_dpp v84, v84, v84 row_half_mirror row_mask:0xf bank_mask:0xf bound_ctrl:1
	s_nop 1
	v_add_f32_dpp v84, v84, v84 row_mirror row_mask:0xf bank_mask:0xf bound_ctrl:1
	s_nop 0
	v_readlane_b32 s37, v84, 16
	v_readlane_b32 s39, v84, 48
	v_readlane_b32 s36, v84, 0
	v_readlane_b32 s38, v84, 32
	v_mov_b32_e32 v84, s37
	v_mov_b32_e32 v85, s39
	v_add_f32_e32 v84, s36, v84
	v_add_f32_e32 v85, s38, v85
	v_add_f32_e32 v84, v84, v85
	v_fmamk_f32 v84, v84, 0x3baaaaab, v44
	v_rsq_f32_e32 v84, v84
	s_add_u32 s36, s31, s34
	s_addc_u32 s37, s30, s35
	s_mulk_i32 s37, 0x180
	v_mul_f32_e32 v85, v84, v105
	v_mul_f32_e32 v91, v84, v104
	v_mul_f32_e32 v84, v84, v103
	v_mul_f32_e32 v84, v35, v84
	v_mov_b32_e32 v92, v84
	v_mov_b32_e32 v98, v84
	s_nop 1
	v_permlane32_swap_b32_e32 v92, v98
	v_cndmask_b32_e64 v92, v92, v98, s[4:5]
	v_mul_f32_e32 v92, v114, v92
	v_cndmask_b32_e64 v92, v92, -v92, s[4:5]
	v_mul_f32_e32 v85, v37, v85
	v_fmac_f32_e32 v92, v113, v84
	v_mul_f32_e32 v91, v36, v91
	v_cndmask_b32_e32 v92, v84, v92, vcc
	v_cvt_pk_bf16_f32 v98, v85, v19
	v_mad_u64_u32 v[84:85], s[34:35], s36, v47, v[30:31]
	v_add_u32_e32 v85, s37, v85
	v_cvt_pk_bf16_f32 v91, v91, v19
	global_store_short v[84:85], v98, off
	global_store_short v[84:85], v91, off offset:128
	v_cvt_pk_bf16_f32 v91, v92, v19
	global_store_short v[84:85], v91, off offset:256
	v_mul_f32_e32 v84, v101, v101
	v_fmac_f32_e32 v84, v102, v102
	v_fmac_f32_e32 v84, v100, v100
	s_cmpk_lt_i32 s21, 0x800
	s_nop 0
	v_add_f32_dpp v84, v84, v84 quad_perm:[1,0,3,2] row_mask:0xf bank_mask:0xf bound_ctrl:1
	s_nop 1
	v_add_f32_dpp v84, v84, v84 quad_perm:[2,3,0,1] row_mask:0xf bank_mask:0xf bound_ctrl:1
	s_nop 1
	v_add_f32_dpp v84, v84, v84 row_half_mirror row_mask:0xf bank_mask:0xf bound_ctrl:1
	s_nop 1
	v_add_f32_dpp v84, v84, v84 row_mirror row_mask:0xf bank_mask:0xf bound_ctrl:1
	s_nop 0
	v_readlane_b32 s35, v84, 16
	v_readlane_b32 s39, v84, 48
	v_readlane_b32 s34, v84, 0
	v_readlane_b32 s38, v84, 32
	v_mov_b32_e32 v84, s35
	v_mov_b32_e32 v85, s39
	v_add_f32_e32 v84, s34, v84
	v_add_f32_e32 v85, s38, v85
	v_add_f32_e32 v84, v84, v85
	v_fmamk_f32 v84, v84, 0x3baaaaab, v44
	v_rsq_f32_e32 v84, v84
	s_nop 0
	v_mul_f32_e32 v85, v84, v102
	v_mul_f32_e32 v91, v84, v101
	v_mul_f32_e32 v84, v84, v100
	v_mul_f32_e32 v84, v11, v84
	v_mov_b32_e32 v92, v84
	v_mov_b32_e32 v98, v84
	s_nop 1
	v_permlane32_swap_b32_e32 v92, v98
	v_cndmask_b32_e64 v92, v92, v98, s[4:5]
	v_mul_f32_e32 v92, v114, v92
	v_cndmask_b32_e64 v92, v92, -v92, s[4:5]
	v_mul_f32_e32 v85, v13, v85
	v_fmac_f32_e32 v92, v113, v84
	v_mul_f32_e32 v91, v12, v91
	v_cndmask_b32_e32 v92, v84, v92, vcc
	v_cvt_pk_bf16_f32 v98, v85, v19
	v_mad_u64_u32 v[84:85], s[34:35], s36, v47, v[32:33]
	v_add_u32_e32 v85, s37, v85
	v_cvt_pk_bf16_f32 v91, v91, v19
	global_store_short v[84:85], v98, off
	global_store_short v[84:85], v91, off offset:128
	v_cvt_pk_bf16_f32 v91, v92, v19
	global_store_short v[84:85], v91, off offset:256
	v_mul_f32_e32 v84, v96, v96
	v_fmac_f32_e32 v84, v97, v97
	v_fmac_f32_e32 v84, v95, v95
	s_cselect_b64 vcc, -1, 0
	s_and_b32 s35, s21, 63
	v_add_f32_dpp v84, v84, v84 quad_perm:[1,0,3,2] row_mask:0xf bank_mask:0xf bound_ctrl:1
	ds_write_b16 v39, v77 offset:768
	ds_write_b16 v39, v78 offset:896
	v_add_f32_dpp v84, v84, v84 quad_perm:[2,3,0,1] row_mask:0xf bank_mask:0xf bound_ctrl:1
	s_ashr_i32 s34, s21, 6
	v_mov_b32_e32 v77, s35
	v_add_f32_dpp v84, v84, v84 row_half_mirror row_mask:0xf bank_mask:0xf bound_ctrl:1
	v_mov_b32_e32 v78, s34
	v_cndmask_b32_e64 v77, v77, v78, s[0:1]
	v_add_f32_dpp v84, v84, v84 row_mirror row_mask:0xf bank_mask:0xf bound_ctrl:1
	v_cvt_f32_i32_e32 v77, v77
	v_readlane_b32 s36, v84, 16
	v_readlane_b32 s38, v84, 48
	v_readlane_b32 s35, v84, 0
	v_readlane_b32 s37, v84, 32
	v_mov_b32_e32 v84, s36
	v_mov_b32_e32 v85, s38
	v_add_f32_e32 v84, s35, v84
	v_add_f32_e32 v85, s37, v85
	v_add_f32_e32 v84, v84, v85
	v_fmamk_f32 v84, v84, 0x3baaaaab, v44
	v_rsq_f32_e32 v84, v84
	v_mul_f32_e32 v77, v1, v77
	v_mul_f32_e32 v77, 0.15915494, v77
	v_cos_f32_e32 v78, v77
	v_mul_f32_e32 v85, v84, v97
	v_mul_f32_e32 v91, v84, v96
	v_mul_f32_e32 v84, v84, v95
	v_sin_f32_e32 v77, v77
	v_mul_f32_e32 v84, v35, v84
	v_mov_b32_e32 v92, v84
	v_mov_b32_e32 v95, v84
	s_nop 1
	v_permlane32_swap_b32_e32 v92, v95
	v_cndmask_b32_e64 v92, v92, v95, s[4:5]
	s_ashr_i32 s34, s21, 31
	v_mul_f32_e32 v92, v77, v92
	v_cndmask_b32_e64 v92, v92, -v92, s[4:5]
	s_add_u32 s35, s22, s21
	v_mul_f32_e32 v85, v37, v85
	v_fmac_f32_e32 v92, v78, v84
	s_addc_u32 s38, s23, s34
	v_mul_f32_e32 v91, v36, v91
	v_cndmask_b32_e32 v92, v84, v92, vcc
	v_cvt_pk_bf16_f32 v95, v85, v19
	v_mad_u64_u32 v[84:85], s[36:37], s35, v47, v[30:31]
	s_mulk_i32 s38, 0x180
	v_add_u32_e32 v85, s38, v85
	v_cvt_pk_bf16_f32 v91, v91, v19
	global_store_short v[84:85], v95, off
	global_store_short v[84:85], v91, off offset:128
	v_cvt_pk_bf16_f32 v91, v92, v19
	global_store_short v[84:85], v91, off offset:256
	v_mul_f32_e32 v84, v93, v93
	v_fmac_f32_e32 v84, v94, v94
	v_fmac_f32_e32 v84, v69, v69
	s_nop 1
	v_add_f32_dpp v84, v84, v84 quad_perm:[1,0,3,2] row_mask:0xf bank_mask:0xf bound_ctrl:1
	s_nop 1
	v_add_f32_dpp v84, v84, v84 quad_perm:[2,3,0,1] row_mask:0xf bank_mask:0xf bound_ctrl:1
	s_nop 1
	v_add_f32_dpp v84, v84, v84 row_half_mirror row_mask:0xf bank_mask:0xf bound_ctrl:1
	s_nop 1
	v_add_f32_dpp v84, v84, v84 row_mirror row_mask:0xf bank_mask:0xf bound_ctrl:1
	s_nop 0
	v_readlane_b32 s37, v84, 16
	v_readlane_b32 s40, v84, 48
	v_readlane_b32 s36, v84, 0
	v_readlane_b32 s39, v84, 32
	v_mov_b32_e32 v84, s37
	v_mov_b32_e32 v85, s40
	v_add_f32_e32 v84, s36, v84
	v_add_f32_e32 v85, s39, v85
	v_add_f32_e32 v84, v84, v85
	v_fmamk_f32 v84, v84, 0x3baaaaab, v44
	v_rsq_f32_e32 v84, v84
	s_nop 0
	v_mul_f32_e32 v85, v84, v94
	v_mul_f32_e32 v91, v84, v93
	v_mul_f32_e32 v84, v84, v69
	v_mul_f32_e32 v84, v11, v84
	v_mov_b32_e32 v92, v84
	v_mov_b32_e32 v93, v84
	s_nop 1
	v_permlane32_swap_b32_e32 v92, v93
	v_cndmask_b32_e64 v92, v92, v93, s[4:5]
	v_mul_f32_e32 v92, v77, v92
	v_cndmask_b32_e64 v92, v92, -v92, s[4:5]
	v_mul_f32_e32 v85, v13, v85
	v_fmac_f32_e32 v92, v78, v84
	v_mul_f32_e32 v91, v12, v91
	v_cndmask_b32_e32 v92, v84, v92, vcc
	v_cvt_pk_bf16_f32 v93, v85, v19
	v_mad_u64_u32 v[84:85], s[36:37], s35, v47, v[32:33]
	v_add_u32_e32 v85, s38, v85
	v_cvt_pk_bf16_f32 v91, v91, v19
	global_store_short v[84:85], v93, off
	global_store_short v[84:85], v91, off offset:128
	v_cvt_pk_bf16_f32 v91, v92, v19
	global_store_short v[84:85], v91, off offset:256
	ds_write_b16 v40, v70
	ds_write_b16 v40, v71 offset:128
	v_mul_f32_e32 v70, v89, v89
	v_fmac_f32_e32 v70, v90, v90
	v_fmac_f32_e32 v70, v88, v88
	s_nop 1
	v_add_f32_dpp v70, v70, v70 quad_perm:[1,0,3,2] row_mask:0xf bank_mask:0xf bound_ctrl:1
	s_nop 1
	v_add_f32_dpp v70, v70, v70 quad_perm:[2,3,0,1] row_mask:0xf bank_mask:0xf bound_ctrl:1
	s_nop 1
	v_add_f32_dpp v70, v70, v70 row_half_mirror row_mask:0xf bank_mask:0xf bound_ctrl:1
	s_nop 1
	v_add_f32_dpp v70, v70, v70 row_mirror row_mask:0xf bank_mask:0xf bound_ctrl:1
	s_nop 0
	v_readlane_b32 s36, v70, 16
	v_readlane_b32 s38, v70, 48
	v_readlane_b32 s35, v70, 0
	v_readlane_b32 s37, v70, 32
	v_mov_b32_e32 v70, s36
	v_mov_b32_e32 v71, s38
	v_add_f32_e32 v70, s35, v70
	v_add_f32_e32 v71, s37, v71
	v_add_f32_e32 v70, v70, v71
	v_fmamk_f32 v70, v70, 0x3baaaaab, v44
	v_rsq_f32_e32 v70, v70
	s_add_u32 s35, s25, s21
	s_addc_u32 s38, s24, s34
	s_mulk_i32 s38, 0x180
	v_mul_f32_e32 v71, v70, v90
	v_mul_f32_e32 v84, v70, v89
	v_mul_f32_e32 v70, v70, v88
	v_mul_f32_e32 v70, v35, v70
	v_mov_b32_e32 v85, v70
	v_mov_b32_e32 v88, v70
	s_nop 1
	v_permlane32_swap_b32_e32 v85, v88
	v_cndmask_b32_e64 v85, v85, v88, s[4:5]
	v_mul_f32_e32 v85, v77, v85
	v_cndmask_b32_e64 v85, v85, -v85, s[4:5]
	v_mul_f32_e32 v71, v37, v71
	v_fmac_f32_e32 v85, v78, v70
	v_mul_f32_e32 v84, v36, v84
	v_cndmask_b32_e32 v85, v70, v85, vcc
	v_cvt_pk_bf16_f32 v88, v71, v19
	v_mad_u64_u32 v[70:71], s[36:37], s35, v47, v[30:31]
	v_add_u32_e32 v71, s38, v71
	v_cvt_pk_bf16_f32 v84, v84, v19
	global_store_short v[70:71], v88, off
	global_store_short v[70:71], v84, off offset:128
	v_cvt_pk_bf16_f32 v84, v85, v19
	global_store_short v[70:71], v84, off offset:256
	v_mul_f32_e32 v70, v86, v86
	v_fmac_f32_e32 v70, v87, v87
	v_fmac_f32_e32 v70, v69, v69
	s_nop 1
	v_add_f32_dpp v70, v70, v70 quad_perm:[1,0,3,2] row_mask:0xf bank_mask:0xf bound_ctrl:1
	s_nop 1
	v_add_f32_dpp v70, v70, v70 quad_perm:[2,3,0,1] row_mask:0xf bank_mask:0xf bound_ctrl:1
	s_nop 1
	v_add_f32_dpp v70, v70, v70 row_half_mirror row_mask:0xf bank_mask:0xf bound_ctrl:1
	s_nop 1
	v_add_f32_dpp v70, v70, v70 row_mirror row_mask:0xf bank_mask:0xf bound_ctrl:1
	s_nop 0
	v_readlane_b32 s37, v70, 16
	v_readlane_b32 s40, v70, 48
	v_readlane_b32 s36, v70, 0
	v_readlane_b32 s39, v70, 32
	v_mov_b32_e32 v70, s37
	v_mov_b32_e32 v71, s40
	v_add_f32_e32 v70, s36, v70
	v_add_f32_e32 v71, s39, v71
	v_add_f32_e32 v70, v70, v71
	v_fmamk_f32 v70, v70, 0x3baaaaab, v44
	v_rsq_f32_e32 v70, v70
	s_nop 0
	v_mul_f32_e32 v71, v70, v87
	v_mul_f32_e32 v84, v70, v86
	v_mul_f32_e32 v70, v70, v69
	v_mul_f32_e32 v70, v11, v70
	v_mov_b32_e32 v85, v70
	v_mov_b32_e32 v86, v70
	s_nop 1
	v_permlane32_swap_b32_e32 v85, v86
	v_cndmask_b32_e64 v85, v85, v86, s[4:5]
	v_mul_f32_e32 v85, v77, v85
	v_cndmask_b32_e64 v85, v85, -v85, s[4:5]
	v_mul_f32_e32 v71, v13, v71
	v_fmac_f32_e32 v85, v78, v70
	v_mul_f32_e32 v84, v12, v84
	v_cndmask_b32_e32 v85, v70, v85, vcc
	v_cvt_pk_bf16_f32 v86, v71, v19
	v_mad_u64_u32 v[70:71], s[36:37], s35, v47, v[32:33]
	v_add_u32_e32 v71, s38, v71
	v_cvt_pk_bf16_f32 v84, v84, v19
	global_store_short v[70:71], v86, off
	global_store_short v[70:71], v84, off offset:128
	v_cvt_pk_bf16_f32 v84, v85, v19
	global_store_short v[70:71], v84, off offset:256
	ds_write_b16 v40, v64 offset:256
	ds_write_b16 v40, v65 offset:384
	v_mul_f32_e32 v64, v82, v82
	v_fmac_f32_e32 v64, v83, v83
	v_fmac_f32_e32 v64, v81, v81
	s_nop 1
	v_add_f32_dpp v64, v64, v64 quad_perm:[1,0,3,2] row_mask:0xf bank_mask:0xf bound_ctrl:1
	s_nop 1
	v_add_f32_dpp v64, v64, v64 quad_perm:[2,3,0,1] row_mask:0xf bank_mask:0xf bound_ctrl:1
	s_nop 1
	v_add_f32_dpp v64, v64, v64 row_half_mirror row_mask:0xf bank_mask:0xf bound_ctrl:1
	s_nop 1
	v_add_f32_dpp v64, v64, v64 row_mirror row_mask:0xf bank_mask:0xf bound_ctrl:1
	s_nop 0
	v_readlane_b32 s36, v64, 16
	v_readlane_b32 s38, v64, 48
	v_readlane_b32 s35, v64, 0
	v_readlane_b32 s37, v64, 32
	v_mov_b32_e32 v64, s36
	v_mov_b32_e32 v65, s38
	v_add_f32_e32 v64, s35, v64
	v_add_f32_e32 v65, s37, v65
	v_add_f32_e32 v64, v64, v65
	v_fmamk_f32 v64, v64, 0x3baaaaab, v44
	v_rsq_f32_e32 v64, v64
	s_add_u32 s35, s29, s21
	s_addc_u32 s38, s28, s34
	s_mulk_i32 s38, 0x180
	v_mul_f32_e32 v65, v64, v83
	v_mul_f32_e32 v70, v64, v82
	v_mul_f32_e32 v64, v64, v81
	v_mul_f32_e32 v64, v35, v64
	v_mov_b32_e32 v71, v64
	v_mov_b32_e32 v81, v64
	s_nop 1
	v_permlane32_swap_b32_e32 v71, v81
	v_cndmask_b32_e64 v71, v71, v81, s[4:5]
	v_mul_f32_e32 v71, v77, v71
	v_cndmask_b32_e64 v71, v71, -v71, s[4:5]
	v_mul_f32_e32 v65, v37, v65
	v_fmac_f32_e32 v71, v78, v64
	v_mul_f32_e32 v70, v36, v70
	v_cndmask_b32_e32 v71, v64, v71, vcc
	v_cvt_pk_bf16_f32 v81, v65, v19
	v_mad_u64_u32 v[64:65], s[36:37], s35, v47, v[30:31]
	v_add_u32_e32 v65, s38, v65
	v_cvt_pk_bf16_f32 v70, v70, v19
	global_store_short v[64:65], v81, off
	global_store_short v[64:65], v70, off offset:128
	v_cvt_pk_bf16_f32 v70, v71, v19
	global_store_short v[64:65], v70, off offset:256
	v_mul_f32_e32 v64, v79, v79
	v_fmac_f32_e32 v64, v80, v80
	v_fmac_f32_e32 v64, v69, v69
	s_add_u32 s21, s31, s21
	s_nop 0
	v_add_f32_dpp v64, v64, v64 quad_perm:[1,0,3,2] row_mask:0xf bank_mask:0xf bound_ctrl:1
	s_nop 1
	v_add_f32_dpp v64, v64, v64 quad_perm:[2,3,0,1] row_mask:0xf bank_mask:0xf bound_ctrl:1
	s_nop 1
	v_add_f32_dpp v64, v64, v64 row_half_mirror row_mask:0xf bank_mask:0xf bound_ctrl:1
	s_nop 1
	v_add_f32_dpp v64, v64, v64 row_mirror row_mask:0xf bank_mask:0xf bound_ctrl:1
	s_nop 0
	v_readlane_b32 s37, v64, 16
	v_readlane_b32 s40, v64, 48
	v_readlane_b32 s36, v64, 0
	v_readlane_b32 s39, v64, 32
	v_mov_b32_e32 v64, s37
	v_mov_b32_e32 v65, s40
	v_add_f32_e32 v64, s36, v64
	v_add_f32_e32 v65, s39, v65
	v_add_f32_e32 v64, v64, v65
	v_fmamk_f32 v64, v64, 0x3baaaaab, v44
	v_rsq_f32_e32 v64, v64
	s_nop 0
	v_mul_f32_e32 v65, v64, v80
	v_mul_f32_e32 v70, v64, v79
	v_mul_f32_e32 v64, v64, v69
	v_mul_f32_e32 v64, v11, v64
	v_mov_b32_e32 v71, v64
	v_mov_b32_e32 v79, v64
	s_nop 1
	v_permlane32_swap_b32_e32 v71, v79
	v_cndmask_b32_e64 v71, v71, v79, s[4:5]
	v_mul_f32_e32 v71, v77, v71
	v_cndmask_b32_e64 v71, v71, -v71, s[4:5]
	v_mul_f32_e32 v65, v13, v65
	v_fmac_f32_e32 v71, v78, v64
	v_mul_f32_e32 v70, v12, v70
	v_cndmask_b32_e32 v71, v64, v71, vcc
	v_cvt_pk_bf16_f32 v79, v65, v19
	v_mad_u64_u32 v[64:65], s[36:37], s35, v47, v[32:33]
	v_add_u32_e32 v65, s38, v65
	v_cvt_pk_bf16_f32 v70, v70, v19
	global_store_short v[64:65], v79, off
	global_store_short v[64:65], v70, off offset:128
	v_cvt_pk_bf16_f32 v70, v71, v19
	global_store_short v[64:65], v70, off offset:256
	ds_write_b16 v40, v57 offset:512
	ds_write_b16 v40, v58 offset:640
	v_mul_f32_e32 v57, v75, v75
	v_fmac_f32_e32 v57, v76, v76
	v_fmac_f32_e32 v57, v74, v74
	s_nop 1
	v_add_f32_dpp v57, v57, v57 quad_perm:[1,0,3,2] row_mask:0xf bank_mask:0xf bound_ctrl:1
	s_nop 1
	v_add_f32_dpp v57, v57, v57 quad_perm:[2,3,0,1] row_mask:0xf bank_mask:0xf bound_ctrl:1
	s_nop 1
	v_add_f32_dpp v57, v57, v57 row_half_mirror row_mask:0xf bank_mask:0xf bound_ctrl:1
	s_nop 1
	v_add_f32_dpp v57, v57, v57 row_mirror row_mask:0xf bank_mask:0xf bound_ctrl:1
	s_nop 0
	v_readlane_b32 s36, v57, 16
	v_readlane_b32 s38, v57, 48
	v_readlane_b32 s35, v57, 0
	v_readlane_b32 s37, v57, 32
	v_mov_b32_e32 v57, s36
	v_mov_b32_e32 v58, s38
	v_add_f32_e32 v57, s35, v57
	v_add_f32_e32 v58, s37, v58
	v_add_f32_e32 v57, v57, v58
	v_fmamk_f32 v57, v57, 0x3baaaaab, v44
	v_rsq_f32_e32 v57, v57
	s_addc_u32 s36, s30, s34
	s_mulk_i32 s36, 0x180
	s_cmpk_lt_i32 s13, 0x800
	v_mul_f32_e32 v58, v57, v76
	v_mul_f32_e32 v64, v57, v75
	v_mul_f32_e32 v57, v57, v74
	v_mul_f32_e32 v57, v35, v57
	v_mul_f32_e32 v70, v36, v64
	v_mov_b32_e32 v64, v57
	v_mov_b32_e32 v65, v57
	s_nop 1
	v_permlane32_swap_b32_e32 v64, v65
	v_cndmask_b32_e64 v64, v64, v65, s[4:5]
	v_mul_f32_e32 v64, v77, v64
	v_cndmask_b32_e64 v64, v64, -v64, s[4:5]
	v_fmac_f32_e32 v64, v78, v57
	v_cndmask_b32_e32 v57, v57, v64, vcc
	v_mad_u64_u32 v[64:65], s[34:35], s21, v47, v[30:31]
	v_add_u32_e32 v65, s36, v65
	v_cvt_pk_bf16_f32 v57, v57, v19
	global_store_short v[64:65], v57, off offset:256
	v_mul_f32_e32 v57, v72, v72
	v_fmac_f32_e32 v57, v73, v73
	v_fmac_f32_e32 v57, v69, v69
	v_mul_f32_e32 v58, v37, v58
	v_cvt_pk_bf16_f32 v58, v58, v19
	global_store_short v[64:65], v58, off
	v_add_f32_dpp v57, v57, v57 quad_perm:[1,0,3,2] row_mask:0xf bank_mask:0xf bound_ctrl:1
	v_cvt_pk_bf16_f32 v58, v70, v19
	global_store_short v[64:65], v58, off offset:128
	s_nop 0
	v_add_f32_dpp v57, v57, v57 quad_perm:[2,3,0,1] row_mask:0xf bank_mask:0xf bound_ctrl:1
	s_nop 1
	v_add_f32_dpp v57, v57, v57 row_half_mirror row_mask:0xf bank_mask:0xf bound_ctrl:1
	s_nop 1
	v_add_f32_dpp v57, v57, v57 row_mirror row_mask:0xf bank_mask:0xf bound_ctrl:1
	s_nop 0
	v_readlane_b32 s35, v57, 16
	v_readlane_b32 s38, v57, 48
	v_readlane_b32 s34, v57, 0
	v_readlane_b32 s37, v57, 32
	v_mov_b32_e32 v57, s35
	v_mov_b32_e32 v58, s38
	v_add_f32_e32 v57, s34, v57
	v_add_f32_e32 v58, s37, v58
	v_add_f32_e32 v57, v57, v58
	v_fmamk_f32 v57, v57, 0x3baaaaab, v44
	v_rsq_f32_e32 v57, v57
	s_nop 0
	v_mul_f32_e32 v58, v57, v73
	v_mul_f32_e32 v64, v57, v72
	v_mul_f32_e32 v57, v57, v69
	v_mul_f32_e32 v57, v11, v57
	v_mul_f32_e32 v70, v12, v64
	v_mov_b32_e32 v64, v57
	v_mov_b32_e32 v65, v57
	s_nop 1
	v_permlane32_swap_b32_e32 v64, v65
	v_cndmask_b32_e64 v64, v64, v65, s[4:5]
	v_mul_f32_e32 v64, v77, v64
	v_cndmask_b32_e64 v64, v64, -v64, s[4:5]
	v_fmac_f32_e32 v64, v78, v57
	v_mul_f32_e32 v58, v13, v58
	v_cndmask_b32_e32 v57, v57, v64, vcc
	v_mad_u64_u32 v[64:65], s[34:35], s21, v47, v[32:33]
	v_cvt_pk_bf16_f32 v58, v58, v19
	v_add_u32_e32 v65, s36, v65
	s_cselect_b64 vcc, -1, 0
	s_ashr_i32 s21, s13, 6
	s_and_b32 s34, s13, 63
	global_store_short v[64:65], v58, off
	v_cvt_pk_bf16_f32 v58, v70, v19
	global_store_short v[64:65], v58, off offset:128
	v_cvt_pk_bf16_f32 v57, v57, v19
	global_store_short v[64:65], v57, off offset:256
	ds_write_b16 v40, v50 offset:768
	ds_write_b16 v40, v51 offset:896
	v_mov_b32_e32 v50, s34
	v_mov_b32_e32 v51, s21
	v_cndmask_b32_e64 v50, v50, v51, s[0:1]
	v_cvt_f32_i32_e32 v50, v50
	s_ashr_i32 s21, s13, 31
	v_mul_f32_e32 v50, v1, v50
	v_mul_f32_e32 v50, 0.15915494, v50
	v_cos_f32_e32 v57, v50
	v_sin_f32_e32 v58, v50
	v_mul_f32_e32 v50, v67, v67
	v_fmac_f32_e32 v50, v68, v68
	v_fmac_f32_e32 v50, v66, v66
	s_nop 1
	v_add_f32_dpp v50, v50, v50 quad_perm:[1,0,3,2] row_mask:0xf bank_mask:0xf bound_ctrl:1
	s_nop 1
	v_add_f32_dpp v50, v50, v50 quad_perm:[2,3,0,1] row_mask:0xf bank_mask:0xf bound_ctrl:1
	s_nop 1
	v_add_f32_dpp v50, v50, v50 row_half_mirror row_mask:0xf bank_mask:0xf bound_ctrl:1
	s_nop 1
	v_add_f32_dpp v50, v50, v50 row_mirror row_mask:0xf bank_mask:0xf bound_ctrl:1
	s_nop 0
	v_readlane_b32 s35, v50, 16
	v_readlane_b32 s37, v50, 48
	v_readlane_b32 s34, v50, 0
	v_readlane_b32 s36, v50, 32
	v_mov_b32_e32 v50, s35
	v_mov_b32_e32 v51, s37
	v_add_f32_e32 v50, s34, v50
	v_add_f32_e32 v51, s36, v51
	v_add_f32_e32 v50, v50, v51
	v_fmamk_f32 v50, v50, 0x3baaaaab, v44
	v_rsq_f32_e32 v50, v50
	s_add_u32 s34, s22, s13
	s_addc_u32 s35, s23, s21
	s_mulk_i32 s35, 0x180
	v_mul_f32_e32 v51, v50, v68
	v_mul_f32_e32 v64, v50, v67
	v_mul_f32_e32 v50, v50, v66
	v_mul_f32_e32 v50, v35, v50
	v_mov_b32_e32 v65, v50
	v_mov_b32_e32 v66, v50
	s_nop 1
	v_permlane32_swap_b32_e32 v65, v66
	v_cndmask_b32_e64 v65, v65, v66, s[4:5]
	v_mul_f32_e32 v65, v58, v65
	v_cndmask_b32_e64 v65, v65, -v65, s[4:5]
	v_mul_f32_e32 v51, v37, v51
	v_fmac_f32_e32 v65, v57, v50
	v_mul_f32_e32 v64, v36, v64
	v_cndmask_b32_e32 v65, v50, v65, vcc
	v_cvt_pk_bf16_f32 v66, v51, v19
	v_mad_u64_u32 v[50:51], s[22:23], s34, v47, v[30:31]
	v_add_u32_e32 v51, s35, v51
	v_cvt_pk_bf16_f32 v64, v64, v19
	global_store_short v[50:51], v66, off
	global_store_short v[50:51], v64, off offset:128
	v_cvt_pk_bf16_f32 v64, v65, v19
	global_store_short v[50:51], v64, off offset:256
	v_mul_f32_e32 v50, v62, v62
	v_fmac_f32_e32 v50, v63, v63
	v_fmac_f32_e32 v50, v8, v8
	s_add_u32 s25, s25, s13
	s_addc_u32 s24, s24, s21
	v_add_f32_dpp v50, v50, v50 quad_perm:[1,0,3,2] row_mask:0xf bank_mask:0xf bound_ctrl:1
	s_mulk_i32 s24, 0x180
	s_nop 0
	v_add_f32_dpp v50, v50, v50 quad_perm:[2,3,0,1] row_mask:0xf bank_mask:0xf bound_ctrl:1
	s_nop 1
	v_add_f32_dpp v50, v50, v50 row_half_mirror row_mask:0xf bank_mask:0xf bound_ctrl:1
	s_nop 1
	v_add_f32_dpp v50, v50, v50 row_mirror row_mask:0xf bank_mask:0xf bound_ctrl:1
	s_nop 0
	v_readlane_b32 s23, v50, 16
	v_readlane_b32 s37, v50, 48
	v_readlane_b32 s22, v50, 0
	v_readlane_b32 s36, v50, 32
	v_mov_b32_e32 v50, s23
	v_mov_b32_e32 v51, s37
	v_add_f32_e32 v50, s22, v50
	v_add_f32_e32 v51, s36, v51
	v_add_f32_e32 v50, v50, v51
	v_fmamk_f32 v50, v50, 0x3baaaaab, v44
	v_rsq_f32_e32 v50, v50
	s_nop 0
	v_mul_f32_e32 v51, v50, v63
	v_mul_f32_e32 v62, v50, v62
	v_mul_f32_e32 v50, v50, v8
	v_mul_f32_e32 v50, v11, v50
	v_mov_b32_e32 v63, v50
	v_mov_b32_e32 v64, v50
	s_nop 1
	v_permlane32_swap_b32_e32 v63, v64
	v_cndmask_b32_e64 v63, v63, v64, s[4:5]
	v_mul_f32_e32 v63, v58, v63
	v_cndmask_b32_e64 v63, v63, -v63, s[4:5]
	v_mul_f32_e32 v51, v13, v51
	v_fmac_f32_e32 v63, v57, v50
	v_mul_f32_e32 v62, v12, v62
	v_cndmask_b32_e32 v63, v50, v63, vcc
	v_cvt_pk_bf16_f32 v64, v51, v19
	v_mad_u64_u32 v[50:51], s[22:23], s34, v47, v[32:33]
	v_add_u32_e32 v51, s35, v51
	v_cvt_pk_bf16_f32 v62, v62, v19
	global_store_short v[50:51], v64, off
	global_store_short v[50:51], v62, off offset:128
	v_cvt_pk_bf16_f32 v62, v63, v19
	global_store_short v[50:51], v62, off offset:256
	ds_write_b16 v41, v14
	ds_write_b16 v41, v15 offset:128
	v_mul_f32_e32 v14, v60, v60
	v_fmac_f32_e32 v14, v61, v61
	v_fmac_f32_e32 v14, v59, v59
	s_nop 1
	v_add_f32_dpp v14, v14, v14 quad_perm:[1,0,3,2] row_mask:0xf bank_mask:0xf bound_ctrl:1
	s_nop 1
	v_add_f32_dpp v14, v14, v14 quad_perm:[2,3,0,1] row_mask:0xf bank_mask:0xf bound_ctrl:1
	s_nop 1
	v_add_f32_dpp v14, v14, v14 row_half_mirror row_mask:0xf bank_mask:0xf bound_ctrl:1
	s_nop 1
	v_add_f32_dpp v14, v14, v14 row_mirror row_mask:0xf bank_mask:0xf bound_ctrl:1
	s_nop 0
	v_readlane_b32 s23, v14, 16
	v_readlane_b32 s35, v14, 48
	v_readlane_b32 s22, v14, 0
	v_readlane_b32 s34, v14, 32
	v_mov_b32_e32 v14, s23
	v_mov_b32_e32 v15, s35
	v_add_f32_e32 v14, s22, v14
	v_add_f32_e32 v15, s34, v15
	v_add_f32_e32 v14, v14, v15
	v_fmamk_f32 v14, v14, 0x3baaaaab, v44
	v_rsq_f32_e32 v14, v14
	s_nop 0
	v_mul_f32_e32 v15, v14, v61
	v_mul_f32_e32 v50, v14, v60
	v_mul_f32_e32 v14, v14, v59
	v_mul_f32_e32 v14, v35, v14
	v_mov_b32_e32 v51, v14
	v_mov_b32_e32 v59, v14
	s_nop 1
	v_permlane32_swap_b32_e32 v51, v59
	v_cndmask_b32_e64 v51, v51, v59, s[4:5]
	v_mul_f32_e32 v51, v58, v51
	v_cndmask_b32_e64 v51, v51, -v51, s[4:5]
	v_mul_f32_e32 v15, v37, v15
	v_fmac_f32_e32 v51, v57, v14
	v_mul_f32_e32 v50, v36, v50
	v_cndmask_b32_e32 v51, v14, v51, vcc
	v_cvt_pk_bf16_f32 v59, v15, v19
	v_mad_u64_u32 v[14:15], s[22:23], s25, v47, v[30:31]
	v_add_u32_e32 v15, s24, v15
	v_cvt_pk_bf16_f32 v50, v50, v19
	global_store_short v[14:15], v59, off
	global_store_short v[14:15], v50, off offset:128
	v_cvt_pk_bf16_f32 v50, v51, v19
	global_store_short v[14:15], v50, off offset:256
	v_mul_f32_e32 v14, v55, v55
	v_fmac_f32_e32 v14, v56, v56
	v_fmac_f32_e32 v14, v8, v8
	s_nop 1
	v_add_f32_dpp v14, v14, v14 quad_perm:[1,0,3,2] row_mask:0xf bank_mask:0xf bound_ctrl:1
	s_nop 1
	v_add_f32_dpp v14, v14, v14 quad_perm:[2,3,0,1] row_mask:0xf bank_mask:0xf bound_ctrl:1
	s_nop 1
	v_add_f32_dpp v14, v14, v14 row_half_mirror row_mask:0xf bank_mask:0xf bound_ctrl:1
	s_nop 1
	v_add_f32_dpp v14, v14, v14 row_mirror row_mask:0xf bank_mask:0xf bound_ctrl:1
	s_nop 0
	v_readlane_b32 s23, v14, 16
	v_readlane_b32 s35, v14, 48
	v_readlane_b32 s22, v14, 0
	v_readlane_b32 s34, v14, 32
	v_mov_b32_e32 v14, s23
	v_mov_b32_e32 v15, s35
	v_add_f32_e32 v14, s22, v14
	v_add_f32_e32 v15, s34, v15
	v_add_f32_e32 v14, v14, v15
	v_fmamk_f32 v14, v14, 0x3baaaaab, v44
	v_rsq_f32_e32 v14, v14
	s_nop 0
	v_mul_f32_e32 v15, v14, v56
	v_mul_f32_e32 v50, v14, v55
	v_mul_f32_e32 v14, v14, v8
	v_mul_f32_e32 v14, v11, v14
	v_mov_b32_e32 v51, v14
	v_mov_b32_e32 v55, v14
	s_nop 1
	v_permlane32_swap_b32_e32 v51, v55
	v_cndmask_b32_e64 v51, v51, v55, s[4:5]
	v_mul_f32_e32 v51, v58, v51
	v_cndmask_b32_e64 v51, v51, -v51, s[4:5]
	v_mul_f32_e32 v15, v13, v15
	v_fmac_f32_e32 v51, v57, v14
	v_mul_f32_e32 v50, v12, v50
	v_cndmask_b32_e32 v51, v14, v51, vcc
	v_cvt_pk_bf16_f32 v55, v15, v19
	v_mad_u64_u32 v[14:15], s[22:23], s25, v47, v[32:33]
	v_add_u32_e32 v15, s24, v15
	v_cvt_pk_bf16_f32 v50, v50, v19
	global_store_short v[14:15], v55, off
	global_store_short v[14:15], v50, off offset:128
	v_cvt_pk_bf16_f32 v50, v51, v19
	global_store_short v[14:15], v50, off offset:256
	ds_write_b16 v41, v6 offset:256
	ds_write_b16 v41, v7 offset:384
	v_mul_f32_e32 v6, v53, v53
	v_fmac_f32_e32 v6, v54, v54
	v_fmac_f32_e32 v6, v52, v52
	s_nop 1
	v_add_f32_dpp v6, v6, v6 quad_perm:[1,0,3,2] row_mask:0xf bank_mask:0xf bound_ctrl:1
	s_nop 1
	v_add_f32_dpp v6, v6, v6 quad_perm:[2,3,0,1] row_mask:0xf bank_mask:0xf bound_ctrl:1
	s_nop 1
	v_add_f32_dpp v6, v6, v6 row_half_mirror row_mask:0xf bank_mask:0xf bound_ctrl:1
	s_nop 1
	v_add_f32_dpp v6, v6, v6 row_mirror row_mask:0xf bank_mask:0xf bound_ctrl:1
	s_nop 0
	v_readlane_b32 s23, v6, 16
	v_readlane_b32 s25, v6, 48
	v_readlane_b32 s22, v6, 0
	v_readlane_b32 s24, v6, 32
	v_mov_b32_e32 v6, s23
	v_mov_b32_e32 v7, s25
	v_add_f32_e32 v6, s22, v6
	v_add_f32_e32 v7, s24, v7
	v_add_f32_e32 v6, v6, v7
	v_fmamk_f32 v6, v6, 0x3baaaaab, v44
	v_rsq_f32_e32 v6, v6
	s_add_u32 s24, s29, s13
	s_addc_u32 s25, s28, s21
	s_mulk_i32 s25, 0x180
	v_mul_f32_e32 v7, v6, v54
	v_mul_f32_e32 v14, v6, v53
	v_mul_f32_e32 v6, v6, v52
	v_mul_f32_e32 v6, v35, v6
	v_mov_b32_e32 v15, v6
	v_mov_b32_e32 v50, v6
	s_nop 1
	v_permlane32_swap_b32_e32 v15, v50
	v_cndmask_b32_e64 v15, v15, v50, s[4:5]
	v_mul_f32_e32 v15, v58, v15
	v_cndmask_b32_e64 v15, v15, -v15, s[4:5]
	v_mul_f32_e32 v7, v37, v7
	v_fmac_f32_e32 v15, v57, v6
	v_mul_f32_e32 v14, v36, v14
	v_cndmask_b32_e32 v15, v6, v15, vcc
	v_cvt_pk_bf16_f32 v50, v7, v19
	v_mad_u64_u32 v[6:7], s[22:23], s24, v47, v[30:31]
	v_add_u32_e32 v7, s25, v7
	v_cvt_pk_bf16_f32 v14, v14, v19
	global_store_short v[6:7], v50, off
	global_store_short v[6:7], v14, off offset:128
	v_cvt_pk_bf16_f32 v14, v15, v19
	global_store_short v[6:7], v14, off offset:256
	v_mul_f32_e32 v6, v48, v48
	v_fmac_f32_e32 v6, v49, v49
	v_fmac_f32_e32 v6, v8, v8
	s_add_u32 s13, s31, s13
	s_addc_u32 s21, s30, s21
	v_add_f32_dpp v6, v6, v6 quad_perm:[1,0,3,2] row_mask:0xf bank_mask:0xf bound_ctrl:1
	s_mulk_i32 s21, 0x180
	s_add_i32 s19, s19, s3
	v_add_f32_dpp v6, v6, v6 quad_perm:[2,3,0,1] row_mask:0xf bank_mask:0xf bound_ctrl:1
	s_add_i32 s18, s18, s16
	s_nop 0
	v_add_f32_dpp v6, v6, v6 row_half_mirror row_mask:0xf bank_mask:0xf bound_ctrl:1
	s_nop 1
	v_add_f32_dpp v6, v6, v6 row_mirror row_mask:0xf bank_mask:0xf bound_ctrl:1
	s_nop 0
	v_readlane_b32 s23, v6, 16
	v_readlane_b32 s29, v6, 48
	v_readlane_b32 s22, v6, 0
	v_readlane_b32 s28, v6, 32
	v_mov_b32_e32 v6, s23
	v_mov_b32_e32 v7, s29
	v_add_f32_e32 v6, s22, v6
	v_add_f32_e32 v7, s28, v7
	v_add_f32_e32 v6, v6, v7
	v_fmamk_f32 v6, v6, 0x3baaaaab, v44
	v_rsq_f32_e32 v6, v6
	s_nop 0
	v_mul_f32_e32 v7, v6, v49
	v_mul_f32_e32 v14, v6, v48
	v_mul_f32_e32 v6, v6, v8
	v_mul_f32_e32 v6, v11, v6
	v_mov_b32_e32 v15, v6
	v_mov_b32_e32 v48, v6
	s_nop 1
	v_permlane32_swap_b32_e32 v15, v48
	v_cndmask_b32_e64 v15, v15, v48, s[4:5]
	v_mul_f32_e32 v15, v58, v15
	v_cndmask_b32_e64 v15, v15, -v15, s[4:5]
	v_mul_f32_e32 v7, v13, v7
	v_fmac_f32_e32 v15, v57, v6
	v_mul_f32_e32 v14, v12, v14
	v_cndmask_b32_e32 v15, v6, v15, vcc
	v_cvt_pk_bf16_f32 v48, v7, v19
	v_mad_u64_u32 v[6:7], s[22:23], s24, v47, v[32:33]
	v_add_u32_e32 v7, s25, v7
	v_cvt_pk_bf16_f32 v14, v14, v19
	global_store_short v[6:7], v48, off
	global_store_short v[6:7], v14, off offset:128
	v_cvt_pk_bf16_f32 v14, v15, v19
	global_store_short v[6:7], v14, off offset:256
	ds_write_b16 v41, v4 offset:512
	ds_write_b16 v41, v5 offset:640
	v_mul_f32_e32 v4, v17, v17
	v_fmac_f32_e32 v4, v34, v34
	v_fmac_f32_e32 v4, v16, v16
	s_nop 1
	v_add_f32_dpp v4, v4, v4 quad_perm:[1,0,3,2] row_mask:0xf bank_mask:0xf bound_ctrl:1
	s_nop 1
	v_add_f32_dpp v4, v4, v4 quad_perm:[2,3,0,1] row_mask:0xf bank_mask:0xf bound_ctrl:1
	s_nop 1
	v_add_f32_dpp v4, v4, v4 row_half_mirror row_mask:0xf bank_mask:0xf bound_ctrl:1
	s_nop 1
	v_add_f32_dpp v4, v4, v4 row_mirror row_mask:0xf bank_mask:0xf bound_ctrl:1
	s_nop 0
	v_readlane_b32 s23, v4, 16
	v_readlane_b32 s25, v4, 48
	v_readlane_b32 s22, v4, 0
	v_readlane_b32 s24, v4, 32
	v_mov_b32_e32 v4, s23
	v_mov_b32_e32 v5, s25
	v_add_f32_e32 v4, s22, v4
	v_add_f32_e32 v5, s24, v5
	v_add_f32_e32 v4, v4, v5
	v_fmamk_f32 v4, v4, 0x3baaaaab, v44
	v_rsq_f32_e32 v4, v4
	s_nop 0
	v_mul_f32_e32 v5, v4, v34
	v_mul_f32_e32 v6, v4, v17
	v_mul_f32_e32 v4, v4, v16
	v_mul_f32_e32 v4, v35, v4
	v_mov_b32_e32 v7, v4
	v_mov_b32_e32 v14, v4
	s_nop 1
	v_permlane32_swap_b32_e32 v7, v14
	v_cndmask_b32_e64 v7, v7, v14, s[4:5]
	v_mul_f32_e32 v7, v58, v7
	v_cndmask_b32_e64 v7, v7, -v7, s[4:5]
	v_mul_f32_e32 v5, v37, v5
	v_fmac_f32_e32 v7, v57, v4
	v_mul_f32_e32 v6, v36, v6
	v_cndmask_b32_e32 v7, v4, v7, vcc
	v_cvt_pk_bf16_f32 v14, v5, v19
	v_mad_u64_u32 v[4:5], s[22:23], s13, v47, v[30:31]
	v_add_u32_e32 v5, s21, v5
	v_cvt_pk_bf16_f32 v6, v6, v19
	global_store_short v[4:5], v14, off
	global_store_short v[4:5], v6, off offset:128
	v_cvt_pk_bf16_f32 v6, v7, v19
	global_store_short v[4:5], v6, off offset:256
	v_mul_f32_e32 v4, v9, v9
	v_fmac_f32_e32 v4, v10, v10
	v_fmac_f32_e32 v4, v8, v8
	v_mov_b64_e32 v[36:37], s[8:9]
	s_nop 0
	v_add_f32_dpp v4, v4, v4 quad_perm:[1,0,3,2] row_mask:0xf bank_mask:0xf bound_ctrl:1
	s_nop 1
	v_add_f32_dpp v4, v4, v4 quad_perm:[2,3,0,1] row_mask:0xf bank_mask:0xf bound_ctrl:1
	s_nop 1
	v_add_f32_dpp v4, v4, v4 row_half_mirror row_mask:0xf bank_mask:0xf bound_ctrl:1
	s_nop 1
	v_add_f32_dpp v4, v4, v4 row_mirror row_mask:0xf bank_mask:0xf bound_ctrl:1
	s_nop 0
	v_readlane_b32 s23, v4, 16
	v_readlane_b32 s25, v4, 48
	v_readlane_b32 s22, v4, 0
	v_readlane_b32 s24, v4, 32
	v_mov_b32_e32 v4, s23
	v_mov_b32_e32 v5, s25
	v_add_f32_e32 v4, s22, v4
	v_add_f32_e32 v5, s24, v5
	v_add_f32_e32 v4, v4, v5
	v_fmamk_f32 v4, v4, 0x3baaaaab, v44
	v_rsq_f32_e32 v4, v4
	s_nop 0
	v_mul_f32_e32 v5, v4, v10
	v_mul_f32_e32 v6, v4, v9
	v_mul_f32_e32 v4, v4, v8
	v_mul_f32_e32 v4, v11, v4
	v_mov_b32_e32 v7, v4
	v_mov_b32_e32 v8, v4
	s_nop 1
	v_permlane32_swap_b32_e32 v7, v8
	v_cndmask_b32_e64 v7, v7, v8, s[4:5]
	v_mul_f32_e32 v7, v58, v7
	v_cndmask_b32_e64 v7, v7, -v7, s[4:5]
	v_mul_f32_e32 v5, v13, v5
	v_fmac_f32_e32 v7, v57, v4
	v_mul_f32_e32 v6, v12, v6
	v_cndmask_b32_e32 v7, v4, v7, vcc
	v_cvt_pk_bf16_f32 v8, v5, v19
	v_mad_u64_u32 v[4:5], s[22:23], s13, v47, v[32:33]
	v_add_u32_e32 v5, s21, v5
	v_cvt_pk_bf16_f32 v6, v6, v19
	global_store_short v[4:5], v8, off
	global_store_short v[4:5], v6, off offset:128
	v_cvt_pk_bf16_f32 v6, v7, v19
	global_store_short v[4:5], v6, off offset:256
	ds_write_b16 v41, v2 offset:768
	ds_write_b16 v41, v3 offset:896
	s_waitcnt lgkmcnt(0)
	s_barrier
	ds_read_u16 v2, v42
	ds_read_u16 v248, v42 offset:1040
	ds_read_u16 v3, v42 offset:2080
	ds_read_u16 v249, v42 offset:3120
	ds_read_u16 v4, v42 offset:4160
	ds_read_u16 v250, v42 offset:5200
	ds_read_u16 v5, v42 offset:6240
	ds_read_u16 v251, v42 offset:7280
	ds_read_u16 v6, v42 offset:8320
	ds_read_u16 v252, v42 offset:9360
	ds_read_u16 v7, v42 offset:10400
	ds_read_u16 v253, v42 offset:11440
	ds_read_u16 v8, v42 offset:12480
	ds_read_u16 v254, v42 offset:13520
	ds_read_u16 v9, v42 offset:14560
	ds_read_u16 v255, v42 offset:15600
	s_ashr_i32 s13, s12, 31
	s_cmpk_gt_i32 s19, 0x11f
	s_waitcnt lgkmcnt(0)
	v_lshl_or_b32 v2, v248, 16, v2
	v_lshl_or_b32 v3, v249, 16, v3
	v_lshl_or_b32 v4, v250, 16, v4
	v_lshl_or_b32 v5, v251, 16, v5
	v_lshl_or_b32 v6, v252, 16, v6
	v_lshl_or_b32 v7, v253, 16, v7
	v_lshl_or_b32 v8, v254, 16, v8
	v_lshl_or_b32 v9, v255, 16, v9
	ds_read_u16 v10, v42 offset:16640
	ds_read_u16 v248, v42 offset:17680
	ds_read_u16 v11, v42 offset:18720
	ds_read_u16 v249, v42 offset:19760
	ds_read_u16 v12, v42 offset:20800
	ds_read_u16 v250, v42 offset:21840
	ds_read_u16 v13, v42 offset:22880
	ds_read_u16 v251, v42 offset:23920
	ds_read_u16 v14, v42 offset:24960
	ds_read_u16 v252, v42 offset:26000
	ds_read_u16 v15, v42 offset:27040
	ds_read_u16 v253, v42 offset:28080
	ds_read_u16 v16, v42 offset:29120
	ds_read_u16 v254, v42 offset:30160
	ds_read_u16 v17, v42 offset:31200
	ds_read_u16 v255, v42 offset:32240
	s_waitcnt lgkmcnt(0)
	v_lshl_or_b32 v10, v248, 16, v10
	v_lshl_or_b32 v11, v249, 16, v11
	v_lshl_or_b32 v12, v250, 16, v12
	v_lshl_or_b32 v13, v251, 16, v13
	v_lshl_or_b32 v14, v252, 16, v14
	v_lshl_or_b32 v15, v253, 16, v15
	v_lshl_or_b32 v16, v254, 16, v16
	v_lshl_or_b32 v17, v255, 16, v17
	v_or_b32_e32 v34, s20, v43
	v_ashrrev_i32_e32 v35, 31, v34
	v_lshlrev_b64 v[34:35], 7, v[34:35]
	v_or_b32_e32 v34, v34, v18
	v_mad_u64_u32 v[36:37], s[20:21], v34, s17, v[36:37]
	v_mad_i32_i24 v37, v35, s17, v37
	v_lshl_add_u64 v[34:35], s[12:13], 1, v[36:37]
	global_store_dwordx4 v[34:35], v[2:5], off
	global_store_dwordx4 v[34:35], v[6:9], off offset:16
	global_store_dwordx4 v[34:35], v[10:13], off offset:32
	global_store_dwordx4 v[34:35], v[14:17], off offset:48
	s_waitcnt vmcnt(63) expcnt(7) lgkmcnt(15)
	s_barrier
	s_cbranch_scc0 .LBB0_3145
	s_branch .LBB0_3142
